# v027 + removed the redundant s_waitcnt lgkmcnt(0) at the head of each K-loop MFMA block (already waited before the preceding barrier)
# baseline (speedup 1.0000x reference)
; #define PG8_WAIT_V(n) asm volatile("s_waitcnt vmcnt(" #n ")" ::: "memory")
; #define PG8_WAIT_L(n) asm volatile("s_waitcnt lgkmcnt(" #n ")" ::: "memory")
; #define PG8_BAR __builtin_amdgcn_s_barrier()
;     ...
;         for (int t = 0; t < nt; t += 2) {
;             const bool last = (t == nt - 2);
;             const char* a1 = cA + (size_t)(t + 1) * kstepA;
;             const char* a2 = last ? nA : cA + (size_t)(t + 2) * kstepA; const char* b2 = last ? nB : cB + (size_t)(t + 2) * kstepB;
;             const char* a3 = a2 + kstepA; const char* b3 = b2 + kstepB;
;             unsigned vs[2][2];
;             if constexpr (GATHER) {
;                 if (last && has_next) {
; #pragma unroll
;                     for (int hh = 0; hh < 2; ++hh)
; #pragma unroll
;                         for (int i = 0; i < 2; ++i) voffN[hh][i] = (unsigned)idxl[(ui + 1) * 256 + hh * HALF + sR[i]] * (unsigned)(K * 2) + (unsigned)sC[i] * 2u;
;                 }
; #pragma unroll
;                 for (int hh = 0; hh < 2; ++hh)
; #pragma unroll
;                     for (int i = 0; i < 2; ++i) vs[hh][i] = last ? voffN[hh][i] : voffA[hh][i];
;             } else {
; #pragma unroll
;                 for (int hh = 0; hh < 2; ++hh)
; #pragma unroll
;                     for (int i = 0; i < 2; ++i) vs[hh][i] = voffA[hh][i];
;             }
;             PG8_LDB(B0, 0, 0); PG8_LDB(B1, 0, 1); PG8_SCHED; PG8_LDA(At, 0, 0); PG8_STAGE(PG8_SA(1, 1), a1, voffA[1]);
;             PG8_WAIT_V(8); PG8_WAIT_L(0); PG8_BAR; if (do0) { PG8_MMA(0, 0, At, B0); PG8_MMA(0, 1, At, B1); } PG8_BAR; PG8_SCHED;
;             PG8_LDA(At, 0, 1); PG8_STAGE(PG8_SB(0, 0), b2, voffB); PG8_STAGE(PG8_SB(0, 1), b2 + hstep, voffB); PG8_STAGE(PG8_SA(0, 0), a2, vs[0]);
;             PG8_WAIT_V(8); PG8_WAIT_L(0); PG8_BAR; if (do1) { PG8_MMA(1, 0, At, B0); PG8_MMA(1, 1, At, B1); } PG8_BAR; PG8_SCHED;
;             PG8_LDB(B0, 1, 0); PG8_LDB(B1, 1, 1); PG8_SCHED; PG8_LDA(At, 1, 0); PG8_STAGE(PG8_SA(0, 1), a2, vs[1]);
;             PG8_WAIT_V(8); PG8_WAIT_L(0); PG8_BAR; if (do0) { PG8_MMA(0, 0, At, B0); PG8_MMA(0, 1, At, B1); } PG8_BAR; PG8_SCHED;
;             PG8_LDA(At, 1, 1); PG8_STAGE(PG8_SB(1, 0), b3, voffB); PG8_STAGE(PG8_SB(1, 1), b3 + hstep, voffB); PG8_STAGE(PG8_SA(1, 0), a3, vs[0]);
;             PG8_WAIT_V(8); PG8_WAIT_L(0); PG8_BAR; if (do1) { PG8_MMA(1, 0, At, B0); PG8_MMA(1, 1, At, B1); } PG8_BAR; PG8_SCHED;
.LBB0_192:
	ds_read_b128 v[158:161], v166
	ds_read_b128 v[180:183], v167
	ds_read_b128 v[184:187], v168
	ds_read_b128 v[188:191], v169
	ds_read_b128 v[192:195], v170
	ds_read_b128 v[200:203], v171
	ds_read_b128 v[204:207], v172
	ds_read_b128 v[208:211], v173
	s_add_u32 s28, s4, 0x80
	s_addc_u32 s29, s5, 0
	s_cmp_eq_u32 s64, 12
	s_cselect_b32 s35, s17, s29
	s_cselect_b32 s34, s60, s28
	s_cselect_b32 s29, s19, s63
	s_cselect_b32 s28, s61, s62
	v_lshl_add_u64 v[162:163], s[4:5], 0, v[152:153]
	s_add_i32 m0, s25, 0xc000
	ds_read_b128 v[212:215], v174
	ds_read_b128 v[216:219], v174 offset:2048
	ds_read_b128 v[220:223], v175
	ds_read_b128 v[224:227], v175 offset:2048
	ds_read_b128 v[228:231], v174 offset:4096
	ds_read_b128 v[232:235], v174 offset:6144
	ds_read_b128 v[236:239], v175 offset:4096
	ds_read_b128 v[240:243], v175 offset:6144
	global_load_lds_dwordx4 v[162:163], off
	v_lshl_add_u64 v[162:163], s[4:5], 0, v[150:151]
	s_add_i32 m0, s25, 0xe000
	s_add_u32 s30, s28, 0x4000
	global_load_lds_dwordx4 v[162:163], off
	s_waitcnt vmcnt(8)
	s_waitcnt lgkmcnt(0)
	s_addc_u32 s31, s29, 0
	s_barrier
	s_setprio 1
	v_mfma_f32_16x16x32_bf16 v[126:129], v[158:161], v[212:215], v[126:129]
	v_mfma_f32_16x16x32_bf16 v[122:125], v[184:187], v[212:215], v[122:125]
	v_mfma_f32_16x16x32_bf16 v[110:113], v[158:161], v[216:219], v[110:113]
	v_mfma_f32_16x16x32_bf16 v[106:109], v[184:187], v[216:219], v[106:109]
	v_mfma_f32_16x16x32_bf16 v[94:97], v[158:161], v[228:231], v[94:97]
	v_mfma_f32_16x16x32_bf16 v[90:93], v[184:187], v[228:231], v[90:93]
	v_mfma_f32_16x16x32_bf16 v[78:81], v[158:161], v[232:235], v[78:81]
	v_mfma_f32_16x16x32_bf16 v[74:77], v[184:187], v[232:235], v[74:77]
	v_mfma_f32_16x16x32_bf16 v[126:129], v[180:183], v[220:223], v[126:129]
	v_mfma_f32_16x16x32_bf16 v[122:125], v[188:191], v[220:223], v[122:125]
	v_mfma_f32_16x16x32_bf16 v[110:113], v[180:183], v[224:227], v[110:113]
	v_mfma_f32_16x16x32_bf16 v[106:109], v[188:191], v[224:227], v[106:109]
	v_mfma_f32_16x16x32_bf16 v[94:97], v[180:183], v[236:239], v[94:97]
	v_mfma_f32_16x16x32_bf16 v[90:93], v[188:191], v[236:239], v[90:93]
	v_mfma_f32_16x16x32_bf16 v[78:81], v[180:183], v[240:243], v[78:81]
	v_mfma_f32_16x16x32_bf16 v[74:77], v[188:191], v[240:243], v[74:77]
	v_mfma_f32_16x16x32_bf16 v[118:121], v[192:195], v[212:215], v[118:121]
	v_mfma_f32_16x16x32_bf16 v[114:117], v[204:207], v[212:215], v[114:117]
	v_mfma_f32_16x16x32_bf16 v[102:105], v[192:195], v[216:219], v[102:105]
	v_mfma_f32_16x16x32_bf16 v[98:101], v[204:207], v[216:219], v[98:101]
	v_mfma_f32_16x16x32_bf16 v[86:89], v[192:195], v[228:231], v[86:89]
	v_mfma_f32_16x16x32_bf16 v[82:85], v[204:207], v[228:231], v[82:85]
	v_mfma_f32_16x16x32_bf16 v[70:73], v[192:195], v[232:235], v[70:73]
	v_mfma_f32_16x16x32_bf16 v[66:69], v[204:207], v[232:235], v[66:69]
	v_mfma_f32_16x16x32_bf16 v[118:121], v[200:203], v[220:223], v[118:121]
	v_mfma_f32_16x16x32_bf16 v[114:117], v[208:211], v[220:223], v[114:117]
	v_mfma_f32_16x16x32_bf16 v[102:105], v[200:203], v[224:227], v[102:105]
	v_mfma_f32_16x16x32_bf16 v[98:101], v[208:211], v[224:227], v[98:101]
	v_mfma_f32_16x16x32_bf16 v[86:89], v[200:203], v[236:239], v[86:89]
	v_mfma_f32_16x16x32_bf16 v[82:85], v[208:211], v[236:239], v[82:85]
	v_mfma_f32_16x16x32_bf16 v[70:73], v[200:203], v[240:243], v[70:73]
	v_mfma_f32_16x16x32_bf16 v[66:69], v[208:211], v[240:243], v[66:69]
	s_setprio 0
	s_barrier
	s_add_i32 s65, s56, s37
	v_lshl_add_u64 v[162:163], s[28:29], 0, v[130:131]
	s_mov_b32 m0, s65
	ds_read_b128 v[212:215], v174 offset:16384
	ds_read_b128 v[216:219], v174 offset:18432
	ds_read_b128 v[220:223], v175 offset:16384
	ds_read_b128 v[224:227], v175 offset:18432
	ds_read_b128 v[228:231], v174 offset:20480
	ds_read_b128 v[232:235], v174 offset:22528
	ds_read_b128 v[236:239], v175 offset:20480
	ds_read_b128 v[240:243], v175 offset:22528
	global_load_lds_dwordx4 v[162:163], off
	s_add_i32 m0, s65, 0x2000
	s_add_u32 s66, s28, 0x40000
	v_lshl_add_u64 v[162:163], s[28:29], 0, v[132:133]
	s_addc_u32 s67, s29, 0
	s_add_i32 s65, s57, s37
	global_load_lds_dwordx4 v[162:163], off
	v_lshl_add_u64 v[162:163], s[66:67], 0, v[130:131]
	s_mov_b32 m0, s65
	v_lshl_add_u64 v[196:197], s[34:35], 0, v[136:137]
	global_load_lds_dwordx4 v[162:163], off
	v_lshl_add_u64 v[162:163], s[66:67], 0, v[132:133]
	s_add_i32 m0, s65, 0x2000
	s_nop 0
	global_load_lds_dwordx4 v[162:163], off
	v_lshl_add_u64 v[162:163], s[34:35], 0, v[134:135]
	s_mov_b32 m0, s25
	s_nop 0
	global_load_lds_dwordx4 v[162:163], off
	s_mov_b32 m0, s27
	s_nop 0
	global_load_lds_dwordx4 v[196:197], off
	s_waitcnt vmcnt(8)
	s_waitcnt lgkmcnt(0)
	s_barrier
; #define PG8_STAGE(bufoff, gbase, voff) do { _Pragma("unroll") for (int _i = 0; _i < 2; ++_i) \
;         __builtin_amdgcn_global_load_lds((const unsigned*)((const char*)(gbase) + (voff)[_i]), (LAS unsigned*)(lds + (bufoff) + ldsw + _i * 8192), 16, 0, 0); } while (0)
; #define PG8_LDA(dst, b, h) do { _Pragma("unroll") for (int m = 0; m < 4; ++m) _Pragma("unroll") for (int k = 0; k < 2; ++k) dst[m][k] = *(const LAS bf16x8*)(lds + PG8_SA(b, h) + ((aoff ^ (k * 64)) + m * 2048)); } while (0)
; #define PG8_LDB(dst, b, h) do { _Pragma("unroll") for (int n = 0; n < 2; ++n) _Pragma("unroll") for (int k = 0; k < 2; ++k) dst[n][k] = *(const LAS bf16x8*)(lds + PG8_SB(b, h) + ((boff ^ (k * 64)) + n * 2048)); } while (0)
; #define PG8_MMA(ai, bj, At, Bt) do { __builtin_amdgcn_s_setprio(1); _Pragma("unroll") for (int m = 0; m < 4; ++m) _Pragma("unroll") for (int n = 0; n < 2; ++n) _Pragma("unroll") for (int k = 0; k < 2; ++k) \
;         acc[ai][bj][m][n] = __builtin_amdgcn_mfma_f32_16x16x32_bf16(Bt[n][k], At[m][k], acc[ai][bj][m][n], 0, 0, 0); __builtin_amdgcn_s_setprio(0); } while (0)
; #define PG8_WAIT_V(n) asm volatile("s_waitcnt vmcnt(" #n ")" ::: "memory")
; #define PG8_WAIT_L(n) asm volatile("s_waitcnt lgkmcnt(" #n ")" ::: "memory")
; #define PG8_BAR __builtin_amdgcn_s_barrier()
;     ...
;             PG8_LDB(B0, 0, 0); PG8_LDB(B1, 0, 1); PG8_SCHED; PG8_LDA(At, 0, 0); PG8_STAGE(PG8_SA(1, 1), a1, voffA[1]);
;             PG8_WAIT_V(8); PG8_WAIT_L(0); PG8_BAR; if (do0) { PG8_MMA(0, 0, At, B0); PG8_MMA(0, 1, At, B1); } PG8_BAR; PG8_SCHED;
;             PG8_LDA(At, 0, 1); PG8_STAGE(PG8_SB(0, 0), b2, voffB); PG8_STAGE(PG8_SB(0, 1), b2 + hstep, voffB); PG8_STAGE(PG8_SA(0, 0), a2, vs[0]);
;             PG8_WAIT_V(8); PG8_WAIT_L(0); PG8_BAR; if (do1) { PG8_MMA(1, 0, At, B0); PG8_MMA(1, 1, At, B1); } PG8_BAR; PG8_SCHED;
;             PG8_LDB(B0, 1, 0); PG8_LDB(B1, 1, 1); PG8_SCHED; PG8_LDA(At, 1, 0); PG8_STAGE(PG8_SA(0, 1), a2, vs[1]);
;             PG8_WAIT_V(8); PG8_WAIT_L(0); PG8_BAR; if (do0) { PG8_MMA(0, 0, At, B0); PG8_MMA(0, 1, At, B1); } PG8_BAR; PG8_SCHED;
;             PG8_LDA(At, 1, 1); PG8_STAGE(PG8_SB(1, 0), b3, voffB); PG8_STAGE(PG8_SB(1, 1), b3 + hstep, voffB); PG8_STAGE(PG8_SA(1, 0), a3, vs[0]);
;             PG8_WAIT_V(8); PG8_WAIT_L(0); PG8_BAR; if (do1) { PG8_MMA(1, 0, At, B0); PG8_MMA(1, 1, At, B1); } PG8_BAR; PG8_SCHED;
	s_setprio 1
	v_mfma_f32_16x16x32_bf16 v[62:65], v[158:161], v[212:215], v[62:65]
	v_mfma_f32_16x16x32_bf16 v[58:61], v[184:187], v[212:215], v[58:61]
	v_mfma_f32_16x16x32_bf16 v[46:49], v[158:161], v[216:219], v[46:49]
	v_mfma_f32_16x16x32_bf16 v[42:45], v[184:187], v[216:219], v[42:45]
	v_mfma_f32_16x16x32_bf16 v[30:33], v[158:161], v[228:231], v[30:33]
	v_mfma_f32_16x16x32_bf16 v[26:29], v[184:187], v[228:231], v[26:29]
	v_mfma_f32_16x16x32_bf16 v[14:17], v[158:161], v[232:235], v[14:17]
	v_mfma_f32_16x16x32_bf16 v[10:13], v[184:187], v[232:235], v[10:13]
	v_mfma_f32_16x16x32_bf16 v[62:65], v[180:183], v[220:223], v[62:65]
	v_mfma_f32_16x16x32_bf16 v[58:61], v[188:191], v[220:223], v[58:61]
	v_mfma_f32_16x16x32_bf16 v[46:49], v[180:183], v[224:227], v[46:49]
	v_mfma_f32_16x16x32_bf16 v[42:45], v[188:191], v[224:227], v[42:45]
	v_mfma_f32_16x16x32_bf16 v[30:33], v[180:183], v[236:239], v[30:33]
	v_mfma_f32_16x16x32_bf16 v[26:29], v[188:191], v[236:239], v[26:29]
	v_mfma_f32_16x16x32_bf16 v[14:17], v[180:183], v[240:243], v[14:17]
	v_mfma_f32_16x16x32_bf16 v[10:13], v[188:191], v[240:243], v[10:13]
	v_mfma_f32_16x16x32_bf16 v[54:57], v[192:195], v[212:215], v[54:57]
	v_mfma_f32_16x16x32_bf16 v[50:53], v[204:207], v[212:215], v[50:53]
	v_mfma_f32_16x16x32_bf16 v[38:41], v[192:195], v[216:219], v[38:41]
	v_mfma_f32_16x16x32_bf16 v[34:37], v[204:207], v[216:219], v[34:37]
	v_mfma_f32_16x16x32_bf16 v[22:25], v[192:195], v[228:231], v[22:25]
	v_mfma_f32_16x16x32_bf16 v[18:21], v[204:207], v[228:231], v[18:21]
	v_mfma_f32_16x16x32_bf16 v[6:9], v[192:195], v[232:235], v[6:9]
	v_mfma_f32_16x16x32_bf16 v[2:5], v[204:207], v[232:235], v[2:5]
	v_mfma_f32_16x16x32_bf16 v[54:57], v[200:203], v[220:223], v[54:57]
	v_mfma_f32_16x16x32_bf16 v[50:53], v[208:211], v[220:223], v[50:53]
	v_mfma_f32_16x16x32_bf16 v[38:41], v[200:203], v[224:227], v[38:41]
	v_mfma_f32_16x16x32_bf16 v[34:37], v[208:211], v[224:227], v[34:37]
	v_mfma_f32_16x16x32_bf16 v[22:25], v[200:203], v[236:239], v[22:25]
	v_mfma_f32_16x16x32_bf16 v[18:21], v[208:211], v[236:239], v[18:21]
	v_mfma_f32_16x16x32_bf16 v[6:9], v[200:203], v[240:243], v[6:9]
	v_mfma_f32_16x16x32_bf16 v[2:5], v[208:211], v[240:243], v[2:5]
	s_setprio 0
	s_barrier
	s_add_i32 s65, 0, 0x18000
	v_add_u32_e32 v142, s65, v145
	v_add_u32_e32 v180, s65, v165
	s_add_i32 s66, 0, 0x1c000
	ds_read_b128 v[158:161], v142
	ds_read_b128 v[180:183], v180
	ds_read_b128 v[184:187], v176
	ds_read_b128 v[188:191], v177
	v_add_u32_e32 v142, s66, v145
	v_add_u32_e32 v199, s66, v165
	ds_read_b128 v[192:195], v142
	ds_read_b128 v[200:203], v199
	ds_read_b128 v[204:207], v178
	ds_read_b128 v[208:211], v179
	s_mov_b32 m0, s38
	v_lshl_add_u64 v[244:245], s[34:35], 0, v[138:139]
	ds_read_b128 v[212:215], v174 offset:32768
	ds_read_b128 v[216:219], v174 offset:34816
	ds_read_b128 v[220:223], v175 offset:32768
	ds_read_b128 v[224:227], v175 offset:34816
	ds_read_b128 v[228:231], v174 offset:36864
	ds_read_b128 v[232:235], v174 offset:38912
	ds_read_b128 v[236:239], v175 offset:36864
	ds_read_b128 v[240:243], v175 offset:38912
	global_load_lds_dwordx4 v[244:245], off
	v_lshl_add_u64 v[244:245], s[34:35], 0, v[140:141]
	s_mov_b32 m0, s39
	s_nop 0
	global_load_lds_dwordx4 v[244:245], off
	s_waitcnt vmcnt(8)
	s_waitcnt lgkmcnt(0)
	s_barrier
	s_setprio 1
	v_mfma_f32_16x16x32_bf16 v[126:129], v[158:161], v[212:215], v[126:129]
	v_mfma_f32_16x16x32_bf16 v[122:125], v[184:187], v[212:215], v[122:125]
	v_mfma_f32_16x16x32_bf16 v[110:113], v[158:161], v[216:219], v[110:113]
	v_mfma_f32_16x16x32_bf16 v[106:109], v[184:187], v[216:219], v[106:109]
	v_mfma_f32_16x16x32_bf16 v[94:97], v[158:161], v[228:231], v[94:97]
	v_mfma_f32_16x16x32_bf16 v[90:93], v[184:187], v[228:231], v[90:93]
	v_mfma_f32_16x16x32_bf16 v[78:81], v[158:161], v[232:235], v[78:81]
	v_mfma_f32_16x16x32_bf16 v[74:77], v[184:187], v[232:235], v[74:77]
	v_mfma_f32_16x16x32_bf16 v[126:129], v[180:183], v[220:223], v[126:129]
	v_mfma_f32_16x16x32_bf16 v[122:125], v[188:191], v[220:223], v[122:125]
	v_mfma_f32_16x16x32_bf16 v[110:113], v[180:183], v[224:227], v[110:113]
	v_mfma_f32_16x16x32_bf16 v[106:109], v[188:191], v[224:227], v[106:109]
	v_mfma_f32_16x16x32_bf16 v[94:97], v[180:183], v[236:239], v[94:97]
	v_mfma_f32_16x16x32_bf16 v[90:93], v[188:191], v[236:239], v[90:93]
	v_mfma_f32_16x16x32_bf16 v[78:81], v[180:183], v[240:243], v[78:81]
	v_mfma_f32_16x16x32_bf16 v[74:77], v[188:191], v[240:243], v[74:77]
	v_mfma_f32_16x16x32_bf16 v[118:121], v[192:195], v[212:215], v[118:121]
	v_mfma_f32_16x16x32_bf16 v[114:117], v[204:207], v[212:215], v[114:117]
	v_mfma_f32_16x16x32_bf16 v[102:105], v[192:195], v[216:219], v[102:105]
	v_mfma_f32_16x16x32_bf16 v[98:101], v[204:207], v[216:219], v[98:101]
	v_mfma_f32_16x16x32_bf16 v[86:89], v[192:195], v[228:231], v[86:89]
	v_mfma_f32_16x16x32_bf16 v[82:85], v[204:207], v[228:231], v[82:85]
	v_mfma_f32_16x16x32_bf16 v[70:73], v[192:195], v[232:235], v[70:73]
	v_mfma_f32_16x16x32_bf16 v[66:69], v[204:207], v[232:235], v[66:69]
	v_mfma_f32_16x16x32_bf16 v[118:121], v[200:203], v[220:223], v[118:121]
	v_mfma_f32_16x16x32_bf16 v[114:117], v[208:211], v[220:223], v[114:117]
	v_mfma_f32_16x16x32_bf16 v[102:105], v[200:203], v[224:227], v[102:105]
	v_mfma_f32_16x16x32_bf16 v[98:101], v[208:211], v[224:227], v[98:101]
	v_mfma_f32_16x16x32_bf16 v[86:89], v[200:203], v[236:239], v[86:89]
	v_mfma_f32_16x16x32_bf16 v[82:85], v[208:211], v[236:239], v[82:85]
	v_mfma_f32_16x16x32_bf16 v[70:73], v[200:203], v[240:243], v[70:73]
	v_mfma_f32_16x16x32_bf16 v[66:69], v[208:211], v[240:243], v[66:69]
	s_setprio 0
	s_barrier
; #define PG8_STAGE(bufoff, gbase, voff) do { _Pragma("unroll") for (int _i = 0; _i < 2; ++_i) \
;         __builtin_amdgcn_global_load_lds((const unsigned*)((const char*)(gbase) + (voff)[_i]), (LAS unsigned*)(lds + (bufoff) + ldsw + _i * 8192), 16, 0, 0); } while (0)
; #define PG8_LDA(dst, b, h) do { _Pragma("unroll") for (int m = 0; m < 4; ++m) _Pragma("unroll") for (int k = 0; k < 2; ++k) dst[m][k] = *(const LAS bf16x8*)(lds + PG8_SA(b, h) + ((aoff ^ (k * 64)) + m * 2048)); } while (0)
; #define PG8_MMA(ai, bj, At, Bt) do { __builtin_amdgcn_s_setprio(1); _Pragma("unroll") for (int m = 0; m < 4; ++m) _Pragma("unroll") for (int n = 0; n < 2; ++n) _Pragma("unroll") for (int k = 0; k < 2; ++k) \
;         acc[ai][bj][m][n] = __builtin_amdgcn_mfma_f32_16x16x32_bf16(Bt[n][k], At[m][k], acc[ai][bj][m][n], 0, 0, 0); __builtin_amdgcn_s_setprio(0); } while (0)
; #define PG8_WAIT_V(n) asm volatile("s_waitcnt vmcnt(" #n ")" ::: "memory")
; #define PG8_WAIT_L(n) asm volatile("s_waitcnt lgkmcnt(" #n ")" ::: "memory")
; #define PG8_BAR __builtin_amdgcn_s_barrier()
; #define PG8_SCHED __builtin_amdgcn_sched_barrier(0)
;     ...
;             PG8_LDA(At, 1, 1); PG8_STAGE(PG8_SB(1, 0), b3, voffB); PG8_STAGE(PG8_SB(1, 1), b3 + hstep, voffB); PG8_STAGE(PG8_SA(1, 0), a3, vs[0]);
;             PG8_WAIT_V(8); PG8_WAIT_L(0); PG8_BAR; if (do1) { PG8_MMA(1, 0, At, B0); PG8_MMA(1, 1, At, B1); } PG8_BAR; PG8_SCHED;
;         }
	s_add_i32 s34, s65, s37
	v_lshl_add_u64 v[244:245], s[30:31], 0, v[130:131]
	s_mov_b32 m0, s34
	ds_read_b128 v[212:215], v174 offset:49152
	ds_read_b128 v[216:219], v174 offset:51200
	ds_read_b128 v[220:223], v175 offset:49152
	ds_read_b128 v[224:227], v175 offset:51200
	ds_read_b128 v[228:231], v174 offset:53248
	ds_read_b128 v[232:235], v174 offset:55296
	ds_read_b128 v[236:239], v175 offset:53248
	ds_read_b128 v[240:243], v175 offset:55296
	global_load_lds_dwordx4 v[244:245], off
	s_add_i32 m0, s34, 0x2000
	s_add_u32 s28, s28, 0x44000
	v_lshl_add_u64 v[244:245], s[30:31], 0, v[132:133]
	s_addc_u32 s29, s29, 0
	s_add_i32 s30, s66, s37
	global_load_lds_dwordx4 v[244:245], off
	v_lshl_add_u64 v[244:245], s[28:29], 0, v[130:131]
	s_mov_b32 m0, s30
	v_lshl_add_u64 v[162:163], v[162:163], 0, s[8:9]
	global_load_lds_dwordx4 v[244:245], off
	v_lshl_add_u64 v[244:245], s[28:29], 0, v[132:133]
	s_add_i32 m0, s30, 0x2000
	s_nop 0
	global_load_lds_dwordx4 v[244:245], off
	s_mov_b32 m0, s51
	s_nop 0
	global_load_lds_dwordx4 v[162:163], off
	v_lshl_add_u64 v[162:163], v[196:197], 0, s[8:9]
	s_mov_b32 m0, s54
	s_nop 0
	global_load_lds_dwordx4 v[162:163], off
	s_waitcnt vmcnt(8)
	s_waitcnt lgkmcnt(0)
	s_barrier
	s_setprio 1
	v_mfma_f32_16x16x32_bf16 v[62:65], v[158:161], v[212:215], v[62:65]
	v_mfma_f32_16x16x32_bf16 v[58:61], v[184:187], v[212:215], v[58:61]
	v_mfma_f32_16x16x32_bf16 v[46:49], v[158:161], v[216:219], v[46:49]
	v_mfma_f32_16x16x32_bf16 v[42:45], v[184:187], v[216:219], v[42:45]
	v_mfma_f32_16x16x32_bf16 v[30:33], v[158:161], v[228:231], v[30:33]
	v_mfma_f32_16x16x32_bf16 v[26:29], v[184:187], v[228:231], v[26:29]
	v_mfma_f32_16x16x32_bf16 v[14:17], v[158:161], v[232:235], v[14:17]
	v_mfma_f32_16x16x32_bf16 v[10:13], v[184:187], v[232:235], v[10:13]
	v_mfma_f32_16x16x32_bf16 v[62:65], v[180:183], v[220:223], v[62:65]
	v_mfma_f32_16x16x32_bf16 v[58:61], v[188:191], v[220:223], v[58:61]
	v_mfma_f32_16x16x32_bf16 v[46:49], v[180:183], v[224:227], v[46:49]
	v_mfma_f32_16x16x32_bf16 v[42:45], v[188:191], v[224:227], v[42:45]
	v_mfma_f32_16x16x32_bf16 v[30:33], v[180:183], v[236:239], v[30:33]
	v_mfma_f32_16x16x32_bf16 v[26:29], v[188:191], v[236:239], v[26:29]
	v_mfma_f32_16x16x32_bf16 v[14:17], v[180:183], v[240:243], v[14:17]
	v_mfma_f32_16x16x32_bf16 v[10:13], v[188:191], v[240:243], v[10:13]
	v_mfma_f32_16x16x32_bf16 v[54:57], v[192:195], v[212:215], v[54:57]
	v_mfma_f32_16x16x32_bf16 v[50:53], v[204:207], v[212:215], v[50:53]
	v_mfma_f32_16x16x32_bf16 v[38:41], v[192:195], v[216:219], v[38:41]
	v_mfma_f32_16x16x32_bf16 v[34:37], v[204:207], v[216:219], v[34:37]
	v_mfma_f32_16x16x32_bf16 v[22:25], v[192:195], v[228:231], v[22:25]
	v_mfma_f32_16x16x32_bf16 v[18:21], v[204:207], v[228:231], v[18:21]
	v_mfma_f32_16x16x32_bf16 v[6:9], v[192:195], v[232:235], v[6:9]
	v_mfma_f32_16x16x32_bf16 v[2:5], v[204:207], v[232:235], v[2:5]
	v_mfma_f32_16x16x32_bf16 v[54:57], v[200:203], v[220:223], v[54:57]
	v_mfma_f32_16x16x32_bf16 v[50:53], v[208:211], v[220:223], v[50:53]
	v_mfma_f32_16x16x32_bf16 v[38:41], v[200:203], v[224:227], v[38:41]
	v_mfma_f32_16x16x32_bf16 v[34:37], v[208:211], v[224:227], v[34:37]
	v_mfma_f32_16x16x32_bf16 v[22:25], v[200:203], v[236:239], v[22:25]
	v_mfma_f32_16x16x32_bf16 v[18:21], v[208:211], v[236:239], v[18:21]
	v_mfma_f32_16x16x32_bf16 v[6:9], v[200:203], v[240:243], v[6:9]
	v_mfma_f32_16x16x32_bf16 v[2:5], v[208:211], v[240:243], v[2:5]
	s_setprio 0
	s_barrier
	s_add_i32 s64, s64, 2
	s_add_u32 s62, s62, 0x8000
	s_addc_u32 s63, s63, 0
	s_add_u32 s4, s4, 0x100
	s_addc_u32 s5, s5, 0
	s_cmp_gt_u32 s64, 13
	s_cbranch_scc0 .LBB0_192
	s_and_b64 vcc, exec, s[12:13]
	s_cbranch_vccz .LBB0_195
	s_barrier

; #define PG8_WAIT_V(n) asm volatile("s_waitcnt vmcnt(" #n ")" ::: "memory")
; #define PG8_WAIT_L(n) asm volatile("s_waitcnt lgkmcnt(" #n ")" ::: "memory")
; #define PG8_BAR __builtin_amdgcn_s_barrier()
;     ...
;         for (int t = 0; t < nt; t += 2) {
;             const bool last = (t == nt - 2);
;             const char* a1 = cA + (size_t)(t + 1) * kstepA;
;             const char* a2 = last ? nA : cA + (size_t)(t + 2) * kstepA; const char* b2 = last ? nB : cB + (size_t)(t + 2) * kstepB;
;             const char* a3 = a2 + kstepA; const char* b3 = b2 + kstepB;
;             unsigned vs[2][2];
;             if constexpr (GATHER) {
;                 if (last && has_next) {
; #pragma unroll
;                     for (int hh = 0; hh < 2; ++hh)
; #pragma unroll
;                         for (int i = 0; i < 2; ++i) voffN[hh][i] = (unsigned)idxl[(ui + 1) * 256 + hh * HALF + sR[i]] * (unsigned)(K * 2) + (unsigned)sC[i] * 2u;
;                 }
; #pragma unroll
;                 for (int hh = 0; hh < 2; ++hh)
; #pragma unroll
;                     for (int i = 0; i < 2; ++i) vs[hh][i] = last ? voffN[hh][i] : voffA[hh][i];
;             } else {
; #pragma unroll
;                 for (int hh = 0; hh < 2; ++hh)
; #pragma unroll
;                     for (int i = 0; i < 2; ++i) vs[hh][i] = voffA[hh][i];
;             }
;             PG8_LDB(B0, 0, 0); PG8_LDB(B1, 0, 1); PG8_SCHED; PG8_LDA(At, 0, 0); PG8_STAGE(PG8_SA(1, 1), a1, voffA[1]);
;             PG8_WAIT_V(8); PG8_WAIT_L(0); PG8_BAR; if (do0) { PG8_MMA(0, 0, At, B0); PG8_MMA(0, 1, At, B1); } PG8_BAR; PG8_SCHED;
;             PG8_LDA(At, 0, 1); PG8_STAGE(PG8_SB(0, 0), b2, voffB); PG8_STAGE(PG8_SB(0, 1), b2 + hstep, voffB); PG8_STAGE(PG8_SA(0, 0), a2, vs[0]);
;             PG8_WAIT_V(8); PG8_WAIT_L(0); PG8_BAR; if (do1) { PG8_MMA(1, 0, At, B0); PG8_MMA(1, 1, At, B1); } PG8_BAR; PG8_SCHED;
;             PG8_LDB(B0, 1, 0); PG8_LDB(B1, 1, 1); PG8_SCHED; PG8_LDA(At, 1, 0); PG8_STAGE(PG8_SA(0, 1), a2, vs[1]);
;             PG8_WAIT_V(8); PG8_WAIT_L(0); PG8_BAR; if (do0) { PG8_MMA(0, 0, At, B0); PG8_MMA(0, 1, At, B1); } PG8_BAR; PG8_SCHED;
;             PG8_LDA(At, 1, 1); PG8_STAGE(PG8_SB(1, 0), b3, voffB); PG8_STAGE(PG8_SB(1, 1), b3 + hstep, voffB); PG8_STAGE(PG8_SA(1, 0), a3, vs[0]);
;             PG8_WAIT_V(8); PG8_WAIT_L(0); PG8_BAR; if (do1) { PG8_MMA(1, 0, At, B0); PG8_MMA(1, 1, At, B1); } PG8_BAR; PG8_SCHED;
.LBB0_212:
	ds_read_b128 v[168:171], v153
	ds_read_b128 v[172:175], v154
	ds_read_b128 v[176:179], v155
	ds_read_b128 v[180:183], v156
	ds_read_b128 v[184:187], v157
	ds_read_b128 v[188:191], v158
	ds_read_b128 v[192:195], v159
	ds_read_b128 v[200:203], v160
	s_add_u32 s30, s4, 0x4000
	s_addc_u32 s31, s5, 0
	s_cmp_eq_u32 s64, 12
	s_cselect_b32 s36, s29, s30
	s_cselect_b32 s37, s17, s31
	s_cselect_b32 s34, s61, s62
	s_cselect_b32 s35, s19, s63
	s_add_u32 s30, s36, 0x4000
	s_addc_u32 s31, s37, 0
	v_lshl_add_u64 v[196:197], s[4:5], 0, v[148:149]
	s_add_i32 m0, s27, 0xc000
	ds_read_b128 v[204:207], v161
	ds_read_b128 v[208:211], v161 offset:2048
	ds_read_b128 v[212:215], v162
	ds_read_b128 v[216:219], v162 offset:2048
	ds_read_b128 v[220:223], v161 offset:4096
	ds_read_b128 v[224:227], v161 offset:6144
	ds_read_b128 v[228:231], v162 offset:4096
	ds_read_b128 v[232:235], v162 offset:6144
	global_load_lds_dwordx4 v[196:197], off
	v_lshl_add_u64 v[196:197], s[4:5], 0, v[150:151]
	s_add_i32 m0, s27, 0xe000
	s_nop 0
	global_load_lds_dwordx4 v[196:197], off
	s_waitcnt vmcnt(8)
	s_waitcnt lgkmcnt(0)
	s_barrier
	s_setprio 1
	v_mfma_f32_16x16x32_bf16 v[126:129], v[168:171], v[204:207], v[126:129]
	v_mfma_f32_16x16x32_bf16 v[122:125], v[176:179], v[204:207], v[122:125]
	v_mfma_f32_16x16x32_bf16 v[110:113], v[168:171], v[208:211], v[110:113]
	v_mfma_f32_16x16x32_bf16 v[106:109], v[176:179], v[208:211], v[106:109]
	v_mfma_f32_16x16x32_bf16 v[94:97], v[168:171], v[220:223], v[94:97]
	v_mfma_f32_16x16x32_bf16 v[90:93], v[176:179], v[220:223], v[90:93]
	v_mfma_f32_16x16x32_bf16 v[78:81], v[168:171], v[224:227], v[78:81]
	v_mfma_f32_16x16x32_bf16 v[74:77], v[176:179], v[224:227], v[74:77]
	v_mfma_f32_16x16x32_bf16 v[126:129], v[172:175], v[212:215], v[126:129]
	v_mfma_f32_16x16x32_bf16 v[122:125], v[180:183], v[212:215], v[122:125]
	v_mfma_f32_16x16x32_bf16 v[110:113], v[172:175], v[216:219], v[110:113]
	v_mfma_f32_16x16x32_bf16 v[106:109], v[180:183], v[216:219], v[106:109]
	v_mfma_f32_16x16x32_bf16 v[94:97], v[172:175], v[228:231], v[94:97]
	v_mfma_f32_16x16x32_bf16 v[90:93], v[180:183], v[228:231], v[90:93]
	v_mfma_f32_16x16x32_bf16 v[78:81], v[172:175], v[232:235], v[78:81]
	v_mfma_f32_16x16x32_bf16 v[74:77], v[180:183], v[232:235], v[74:77]
	v_mfma_f32_16x16x32_bf16 v[118:121], v[184:187], v[204:207], v[118:121]
	v_mfma_f32_16x16x32_bf16 v[114:117], v[192:195], v[204:207], v[114:117]
	v_mfma_f32_16x16x32_bf16 v[102:105], v[184:187], v[208:211], v[102:105]
	v_mfma_f32_16x16x32_bf16 v[98:101], v[192:195], v[208:211], v[98:101]
	v_mfma_f32_16x16x32_bf16 v[86:89], v[184:187], v[220:223], v[86:89]
	v_mfma_f32_16x16x32_bf16 v[82:85], v[192:195], v[220:223], v[82:85]
	v_mfma_f32_16x16x32_bf16 v[70:73], v[184:187], v[224:227], v[70:73]
	v_mfma_f32_16x16x32_bf16 v[66:69], v[192:195], v[224:227], v[66:69]
	v_mfma_f32_16x16x32_bf16 v[118:121], v[188:191], v[212:215], v[118:121]
	v_mfma_f32_16x16x32_bf16 v[114:117], v[200:203], v[212:215], v[114:117]
	v_mfma_f32_16x16x32_bf16 v[102:105], v[188:191], v[216:219], v[102:105]
	v_mfma_f32_16x16x32_bf16 v[98:101], v[200:203], v[216:219], v[98:101]
	v_mfma_f32_16x16x32_bf16 v[86:89], v[188:191], v[228:231], v[86:89]
	v_mfma_f32_16x16x32_bf16 v[82:85], v[200:203], v[228:231], v[82:85]
	v_mfma_f32_16x16x32_bf16 v[70:73], v[188:191], v[232:235], v[70:73]
	v_mfma_f32_16x16x32_bf16 v[66:69], v[200:203], v[232:235], v[66:69]
	s_setprio 0
	s_barrier
	s_add_i32 s65, s58, s39
	v_lshl_add_u64 v[196:197], s[34:35], 0, v[132:133]
	s_mov_b32 m0, s65
	ds_read_b128 v[204:207], v161 offset:16384
	ds_read_b128 v[208:211], v161 offset:18432
	ds_read_b128 v[212:215], v162 offset:16384
	ds_read_b128 v[216:219], v162 offset:18432
	ds_read_b128 v[220:223], v161 offset:20480
	ds_read_b128 v[224:227], v161 offset:22528
	ds_read_b128 v[228:231], v162 offset:20480
	ds_read_b128 v[232:235], v162 offset:22528
	global_load_lds_dwordx4 v[196:197], off
	s_add_i32 m0, s65, 0x2000
	s_add_u32 s66, s34, 0x40000
	v_lshl_add_u64 v[236:237], s[34:35], 0, v[130:131]
	s_addc_u32 s67, s35, 0
	s_add_i32 s65, s59, s39
	global_load_lds_dwordx4 v[236:237], off
	v_lshl_add_u64 v[238:239], s[66:67], 0, v[132:133]
	s_mov_b32 m0, s65
	s_nop 0
	global_load_lds_dwordx4 v[238:239], off
	v_lshl_add_u64 v[238:239], s[66:67], 0, v[130:131]
	s_add_i32 m0, s65, 0x2000
	s_nop 0
	global_load_lds_dwordx4 v[238:239], off
	v_lshl_add_u64 v[238:239], s[36:37], 0, v[134:135]
	s_mov_b32 m0, s27
	s_nop 0
	global_load_lds_dwordx4 v[238:239], off
	v_lshl_add_u64 v[238:239], s[36:37], 0, v[136:137]
	s_mov_b32 m0, s48
	s_nop 0
	global_load_lds_dwordx4 v[238:239], off
	s_waitcnt vmcnt(8)
	s_waitcnt lgkmcnt(0)
	s_barrier
; #define PG8_STAGE(bufoff, gbase, voff) do { _Pragma("unroll") for (int _i = 0; _i < 2; ++_i) \
;         __builtin_amdgcn_global_load_lds((const unsigned*)((const char*)(gbase) + (voff)[_i]), (LAS unsigned*)(lds + (bufoff) + ldsw + _i * 8192), 16, 0, 0); } while (0)
; #define PG8_LDA(dst, b, h) do { _Pragma("unroll") for (int m = 0; m < 4; ++m) _Pragma("unroll") for (int k = 0; k < 2; ++k) dst[m][k] = *(const LAS bf16x8*)(lds + PG8_SA(b, h) + ((aoff ^ (k * 64)) + m * 2048)); } while (0)
; #define PG8_LDB(dst, b, h) do { _Pragma("unroll") for (int n = 0; n < 2; ++n) _Pragma("unroll") for (int k = 0; k < 2; ++k) dst[n][k] = *(const LAS bf16x8*)(lds + PG8_SB(b, h) + ((boff ^ (k * 64)) + n * 2048)); } while (0)
; #define PG8_MMA(ai, bj, At, Bt) do { __builtin_amdgcn_s_setprio(1); _Pragma("unroll") for (int m = 0; m < 4; ++m) _Pragma("unroll") for (int n = 0; n < 2; ++n) _Pragma("unroll") for (int k = 0; k < 2; ++k) \
;         acc[ai][bj][m][n] = __builtin_amdgcn_mfma_f32_16x16x32_bf16(Bt[n][k], At[m][k], acc[ai][bj][m][n], 0, 0, 0); __builtin_amdgcn_s_setprio(0); } while (0)
; #define PG8_WAIT_V(n) asm volatile("s_waitcnt vmcnt(" #n ")" ::: "memory")
; #define PG8_WAIT_L(n) asm volatile("s_waitcnt lgkmcnt(" #n ")" ::: "memory")
; #define PG8_BAR __builtin_amdgcn_s_barrier()
;     ...
;             PG8_LDB(B0, 0, 0); PG8_LDB(B1, 0, 1); PG8_SCHED; PG8_LDA(At, 0, 0); PG8_STAGE(PG8_SA(1, 1), a1, voffA[1]);
;             PG8_WAIT_V(8); PG8_WAIT_L(0); PG8_BAR; if (do0) { PG8_MMA(0, 0, At, B0); PG8_MMA(0, 1, At, B1); } PG8_BAR; PG8_SCHED;
;             PG8_LDA(At, 0, 1); PG8_STAGE(PG8_SB(0, 0), b2, voffB); PG8_STAGE(PG8_SB(0, 1), b2 + hstep, voffB); PG8_STAGE(PG8_SA(0, 0), a2, vs[0]);
;             PG8_WAIT_V(8); PG8_WAIT_L(0); PG8_BAR; if (do1) { PG8_MMA(1, 0, At, B0); PG8_MMA(1, 1, At, B1); } PG8_BAR; PG8_SCHED;
;             PG8_LDB(B0, 1, 0); PG8_LDB(B1, 1, 1); PG8_SCHED; PG8_LDA(At, 1, 0); PG8_STAGE(PG8_SA(0, 1), a2, vs[1]);
;             PG8_WAIT_V(8); PG8_WAIT_L(0); PG8_BAR; if (do0) { PG8_MMA(0, 0, At, B0); PG8_MMA(0, 1, At, B1); } PG8_BAR; PG8_SCHED;
;             PG8_LDA(At, 1, 1); PG8_STAGE(PG8_SB(1, 0), b3, voffB); PG8_STAGE(PG8_SB(1, 1), b3 + hstep, voffB); PG8_STAGE(PG8_SA(1, 0), a3, vs[0]);
;             PG8_WAIT_V(8); PG8_WAIT_L(0); PG8_BAR; if (do1) { PG8_MMA(1, 0, At, B0); PG8_MMA(1, 1, At, B1); } PG8_BAR; PG8_SCHED;
	s_setprio 1
	v_mfma_f32_16x16x32_bf16 v[62:65], v[168:171], v[204:207], v[62:65]
	v_mfma_f32_16x16x32_bf16 v[58:61], v[176:179], v[204:207], v[58:61]
	v_mfma_f32_16x16x32_bf16 v[46:49], v[168:171], v[208:211], v[46:49]
	v_mfma_f32_16x16x32_bf16 v[42:45], v[176:179], v[208:211], v[42:45]
	v_mfma_f32_16x16x32_bf16 v[30:33], v[168:171], v[220:223], v[30:33]
	v_mfma_f32_16x16x32_bf16 v[26:29], v[176:179], v[220:223], v[26:29]
	v_mfma_f32_16x16x32_bf16 v[14:17], v[168:171], v[224:227], v[14:17]
	v_mfma_f32_16x16x32_bf16 v[10:13], v[176:179], v[224:227], v[10:13]
	v_mfma_f32_16x16x32_bf16 v[62:65], v[172:175], v[212:215], v[62:65]
	v_mfma_f32_16x16x32_bf16 v[58:61], v[180:183], v[212:215], v[58:61]
	v_mfma_f32_16x16x32_bf16 v[46:49], v[172:175], v[216:219], v[46:49]
	v_mfma_f32_16x16x32_bf16 v[42:45], v[180:183], v[216:219], v[42:45]
	v_mfma_f32_16x16x32_bf16 v[30:33], v[172:175], v[228:231], v[30:33]
	v_mfma_f32_16x16x32_bf16 v[26:29], v[180:183], v[228:231], v[26:29]
	v_mfma_f32_16x16x32_bf16 v[14:17], v[172:175], v[232:235], v[14:17]
	v_mfma_f32_16x16x32_bf16 v[10:13], v[180:183], v[232:235], v[10:13]
	v_mfma_f32_16x16x32_bf16 v[54:57], v[184:187], v[204:207], v[54:57]
	v_mfma_f32_16x16x32_bf16 v[50:53], v[192:195], v[204:207], v[50:53]
	v_mfma_f32_16x16x32_bf16 v[38:41], v[184:187], v[208:211], v[38:41]
	v_mfma_f32_16x16x32_bf16 v[34:37], v[192:195], v[208:211], v[34:37]
	v_mfma_f32_16x16x32_bf16 v[22:25], v[184:187], v[220:223], v[22:25]
	v_mfma_f32_16x16x32_bf16 v[18:21], v[192:195], v[220:223], v[18:21]
	v_mfma_f32_16x16x32_bf16 v[6:9], v[184:187], v[224:227], v[6:9]
	v_mfma_f32_16x16x32_bf16 v[2:5], v[192:195], v[224:227], v[2:5]
	v_mfma_f32_16x16x32_bf16 v[54:57], v[188:191], v[212:215], v[54:57]
	v_mfma_f32_16x16x32_bf16 v[50:53], v[200:203], v[212:215], v[50:53]
	v_mfma_f32_16x16x32_bf16 v[38:41], v[188:191], v[216:219], v[38:41]
	v_mfma_f32_16x16x32_bf16 v[34:37], v[200:203], v[216:219], v[34:37]
	v_mfma_f32_16x16x32_bf16 v[22:25], v[188:191], v[228:231], v[22:25]
	v_mfma_f32_16x16x32_bf16 v[18:21], v[200:203], v[228:231], v[18:21]
	v_mfma_f32_16x16x32_bf16 v[6:9], v[188:191], v[232:235], v[6:9]
	v_mfma_f32_16x16x32_bf16 v[2:5], v[200:203], v[232:235], v[2:5]
	s_setprio 0
	s_barrier
	s_add_i32 s65, 0, 0x18000
	v_add_u32_e32 v167, s65, v143
	v_add_u32_e32 v172, s65, v152
	s_add_i32 s66, 0, 0x1c000
	ds_read_b128 v[168:171], v167
	ds_read_b128 v[172:175], v172
	ds_read_b128 v[176:179], v163
	ds_read_b128 v[180:183], v164
	v_add_u32_e32 v167, s66, v143
	v_add_u32_e32 v188, s66, v152
	ds_read_b128 v[184:187], v167
	ds_read_b128 v[188:191], v188
	ds_read_b128 v[192:195], v165
	ds_read_b128 v[200:203], v166
	s_mov_b32 m0, s49
	v_lshl_add_u64 v[238:239], s[36:37], 0, v[138:139]
	ds_read_b128 v[204:207], v161 offset:32768
	ds_read_b128 v[208:211], v161 offset:34816
	ds_read_b128 v[212:215], v162 offset:32768
	ds_read_b128 v[216:219], v162 offset:34816
	ds_read_b128 v[220:223], v161 offset:36864
	ds_read_b128 v[224:227], v161 offset:38912
	ds_read_b128 v[228:231], v162 offset:36864
	ds_read_b128 v[232:235], v162 offset:38912
	global_load_lds_dwordx4 v[238:239], off
	v_lshl_add_u64 v[238:239], s[36:37], 0, v[140:141]
	s_mov_b32 m0, s50
	s_nop 0
	global_load_lds_dwordx4 v[238:239], off
	s_waitcnt vmcnt(8)
	s_waitcnt lgkmcnt(0)
	s_barrier
	s_setprio 1
	v_mfma_f32_16x16x32_bf16 v[126:129], v[168:171], v[204:207], v[126:129]
	v_mfma_f32_16x16x32_bf16 v[122:125], v[176:179], v[204:207], v[122:125]
	v_mfma_f32_16x16x32_bf16 v[110:113], v[168:171], v[208:211], v[110:113]
	v_mfma_f32_16x16x32_bf16 v[106:109], v[176:179], v[208:211], v[106:109]
	v_mfma_f32_16x16x32_bf16 v[94:97], v[168:171], v[220:223], v[94:97]
	v_mfma_f32_16x16x32_bf16 v[90:93], v[176:179], v[220:223], v[90:93]
	v_mfma_f32_16x16x32_bf16 v[78:81], v[168:171], v[224:227], v[78:81]
	v_mfma_f32_16x16x32_bf16 v[74:77], v[176:179], v[224:227], v[74:77]
	v_mfma_f32_16x16x32_bf16 v[126:129], v[172:175], v[212:215], v[126:129]
	v_mfma_f32_16x16x32_bf16 v[122:125], v[180:183], v[212:215], v[122:125]
	v_mfma_f32_16x16x32_bf16 v[110:113], v[172:175], v[216:219], v[110:113]
	v_mfma_f32_16x16x32_bf16 v[106:109], v[180:183], v[216:219], v[106:109]
	v_mfma_f32_16x16x32_bf16 v[94:97], v[172:175], v[228:231], v[94:97]
	v_mfma_f32_16x16x32_bf16 v[90:93], v[180:183], v[228:231], v[90:93]
	v_mfma_f32_16x16x32_bf16 v[78:81], v[172:175], v[232:235], v[78:81]
	v_mfma_f32_16x16x32_bf16 v[74:77], v[180:183], v[232:235], v[74:77]
	v_mfma_f32_16x16x32_bf16 v[118:121], v[184:187], v[204:207], v[118:121]
	v_mfma_f32_16x16x32_bf16 v[114:117], v[192:195], v[204:207], v[114:117]
	v_mfma_f32_16x16x32_bf16 v[102:105], v[184:187], v[208:211], v[102:105]
	v_mfma_f32_16x16x32_bf16 v[98:101], v[192:195], v[208:211], v[98:101]
	v_mfma_f32_16x16x32_bf16 v[86:89], v[184:187], v[220:223], v[86:89]
	v_mfma_f32_16x16x32_bf16 v[82:85], v[192:195], v[220:223], v[82:85]
	v_mfma_f32_16x16x32_bf16 v[70:73], v[184:187], v[224:227], v[70:73]
	v_mfma_f32_16x16x32_bf16 v[66:69], v[192:195], v[224:227], v[66:69]
	v_mfma_f32_16x16x32_bf16 v[118:121], v[188:191], v[212:215], v[118:121]
	v_mfma_f32_16x16x32_bf16 v[114:117], v[200:203], v[212:215], v[114:117]
	v_mfma_f32_16x16x32_bf16 v[102:105], v[188:191], v[216:219], v[102:105]
	v_mfma_f32_16x16x32_bf16 v[98:101], v[200:203], v[216:219], v[98:101]
	v_mfma_f32_16x16x32_bf16 v[86:89], v[188:191], v[228:231], v[86:89]
	v_mfma_f32_16x16x32_bf16 v[82:85], v[200:203], v[228:231], v[82:85]
	v_mfma_f32_16x16x32_bf16 v[70:73], v[188:191], v[232:235], v[70:73]
	v_mfma_f32_16x16x32_bf16 v[66:69], v[200:203], v[232:235], v[66:69]
	s_setprio 0
	s_barrier
; #define PG8_STAGE(bufoff, gbase, voff) do { _Pragma("unroll") for (int _i = 0; _i < 2; ++_i) \
;         __builtin_amdgcn_global_load_lds((const unsigned*)((const char*)(gbase) + (voff)[_i]), (LAS unsigned*)(lds + (bufoff) + ldsw + _i * 8192), 16, 0, 0); } while (0)
; #define PG8_LDA(dst, b, h) do { _Pragma("unroll") for (int m = 0; m < 4; ++m) _Pragma("unroll") for (int k = 0; k < 2; ++k) dst[m][k] = *(const LAS bf16x8*)(lds + PG8_SA(b, h) + ((aoff ^ (k * 64)) + m * 2048)); } while (0)
; #define PG8_MMA(ai, bj, At, Bt) do { __builtin_amdgcn_s_setprio(1); _Pragma("unroll") for (int m = 0; m < 4; ++m) _Pragma("unroll") for (int n = 0; n < 2; ++n) _Pragma("unroll") for (int k = 0; k < 2; ++k) \
;         acc[ai][bj][m][n] = __builtin_amdgcn_mfma_f32_16x16x32_bf16(Bt[n][k], At[m][k], acc[ai][bj][m][n], 0, 0, 0); __builtin_amdgcn_s_setprio(0); } while (0)
; #define PG8_WAIT_V(n) asm volatile("s_waitcnt vmcnt(" #n ")" ::: "memory")
; #define PG8_WAIT_L(n) asm volatile("s_waitcnt lgkmcnt(" #n ")" ::: "memory")
; #define PG8_BAR __builtin_amdgcn_s_barrier()
; #define PG8_SCHED __builtin_amdgcn_sched_barrier(0)
;     ...
;             PG8_LDA(At, 1, 1); PG8_STAGE(PG8_SB(1, 0), b3, voffB); PG8_STAGE(PG8_SB(1, 1), b3 + hstep, voffB); PG8_STAGE(PG8_SA(1, 0), a3, vs[0]);
;             PG8_WAIT_V(8); PG8_WAIT_L(0); PG8_BAR; if (do1) { PG8_MMA(1, 0, At, B0); PG8_MMA(1, 1, At, B1); } PG8_BAR; PG8_SCHED;
;         }
	s_add_i32 s36, s65, s39
	v_lshl_add_u64 v[196:197], v[196:197], 0, s[12:13]
	s_mov_b32 m0, s36
	ds_read_b128 v[204:207], v161 offset:49152
	ds_read_b128 v[208:211], v161 offset:51200
	ds_read_b128 v[212:215], v162 offset:49152
	ds_read_b128 v[216:219], v162 offset:51200
	ds_read_b128 v[220:223], v161 offset:53248
	ds_read_b128 v[224:227], v161 offset:55296
	ds_read_b128 v[228:231], v162 offset:53248
	ds_read_b128 v[232:235], v162 offset:55296
	global_load_lds_dwordx4 v[196:197], off
	s_add_i32 m0, s36, 0x2000
	s_add_u32 s34, s34, 0x40080
	v_lshl_add_u64 v[196:197], v[236:237], 0, s[12:13]
	s_addc_u32 s35, s35, 0
	s_add_i32 s36, s66, s39
	global_load_lds_dwordx4 v[196:197], off
	v_lshl_add_u64 v[196:197], s[34:35], 0, v[132:133]
	s_mov_b32 m0, s36
	s_nop 0
	global_load_lds_dwordx4 v[196:197], off
	v_lshl_add_u64 v[196:197], s[34:35], 0, v[130:131]
	s_add_i32 m0, s36, 0x2000
	s_nop 0
	global_load_lds_dwordx4 v[196:197], off
	v_lshl_add_u64 v[196:197], s[30:31], 0, v[134:135]
	s_mov_b32 m0, s55
	s_nop 0
	global_load_lds_dwordx4 v[196:197], off
	v_lshl_add_u64 v[196:197], s[30:31], 0, v[136:137]
	s_mov_b32 m0, s56
	s_nop 0
	global_load_lds_dwordx4 v[196:197], off
	s_waitcnt vmcnt(8)
	s_waitcnt lgkmcnt(0)
	s_barrier
	s_setprio 1
	v_mfma_f32_16x16x32_bf16 v[62:65], v[168:171], v[204:207], v[62:65]
	v_mfma_f32_16x16x32_bf16 v[58:61], v[176:179], v[204:207], v[58:61]
	v_mfma_f32_16x16x32_bf16 v[46:49], v[168:171], v[208:211], v[46:49]
	v_mfma_f32_16x16x32_bf16 v[42:45], v[176:179], v[208:211], v[42:45]
	v_mfma_f32_16x16x32_bf16 v[30:33], v[168:171], v[220:223], v[30:33]
	v_mfma_f32_16x16x32_bf16 v[26:29], v[176:179], v[220:223], v[26:29]
	v_mfma_f32_16x16x32_bf16 v[14:17], v[168:171], v[224:227], v[14:17]
	v_mfma_f32_16x16x32_bf16 v[10:13], v[176:179], v[224:227], v[10:13]
	v_mfma_f32_16x16x32_bf16 v[62:65], v[172:175], v[212:215], v[62:65]
	v_mfma_f32_16x16x32_bf16 v[58:61], v[180:183], v[212:215], v[58:61]
	v_mfma_f32_16x16x32_bf16 v[46:49], v[172:175], v[216:219], v[46:49]
	v_mfma_f32_16x16x32_bf16 v[42:45], v[180:183], v[216:219], v[42:45]
	v_mfma_f32_16x16x32_bf16 v[30:33], v[172:175], v[228:231], v[30:33]
	v_mfma_f32_16x16x32_bf16 v[26:29], v[180:183], v[228:231], v[26:29]
	v_mfma_f32_16x16x32_bf16 v[14:17], v[172:175], v[232:235], v[14:17]
	v_mfma_f32_16x16x32_bf16 v[10:13], v[180:183], v[232:235], v[10:13]
	v_mfma_f32_16x16x32_bf16 v[54:57], v[184:187], v[204:207], v[54:57]
	v_mfma_f32_16x16x32_bf16 v[50:53], v[192:195], v[204:207], v[50:53]
	v_mfma_f32_16x16x32_bf16 v[38:41], v[184:187], v[208:211], v[38:41]
	v_mfma_f32_16x16x32_bf16 v[34:37], v[192:195], v[208:211], v[34:37]
	v_mfma_f32_16x16x32_bf16 v[22:25], v[184:187], v[220:223], v[22:25]
	v_mfma_f32_16x16x32_bf16 v[18:21], v[192:195], v[220:223], v[18:21]
	v_mfma_f32_16x16x32_bf16 v[6:9], v[184:187], v[224:227], v[6:9]
	v_mfma_f32_16x16x32_bf16 v[2:5], v[192:195], v[224:227], v[2:5]
	v_mfma_f32_16x16x32_bf16 v[54:57], v[188:191], v[212:215], v[54:57]
	v_mfma_f32_16x16x32_bf16 v[50:53], v[200:203], v[212:215], v[50:53]
	v_mfma_f32_16x16x32_bf16 v[38:41], v[188:191], v[216:219], v[38:41]
	v_mfma_f32_16x16x32_bf16 v[34:37], v[200:203], v[216:219], v[34:37]
	v_mfma_f32_16x16x32_bf16 v[22:25], v[188:191], v[228:231], v[22:25]
	v_mfma_f32_16x16x32_bf16 v[18:21], v[200:203], v[228:231], v[18:21]
	v_mfma_f32_16x16x32_bf16 v[6:9], v[188:191], v[232:235], v[6:9]
	v_mfma_f32_16x16x32_bf16 v[2:5], v[200:203], v[232:235], v[2:5]
	s_setprio 0
	s_barrier
	s_add_i32 s64, s64, 2
	s_add_u32 s62, s62, 0x100
	s_addc_u32 s63, s63, 0
	s_add_u32 s4, s4, 0x8000
	s_addc_u32 s5, s5, 0
	s_cmp_gt_u32 s64, 13
	s_cbranch_scc0 .LBB0_212
	s_and_b64 vcc, exec, s[14:15]
	s_cbranch_vccz .LBB0_215
	s_barrier

; #define PG8_WAIT_V(n) asm volatile("s_waitcnt vmcnt(" #n ")" ::: "memory")
; #define PG8_WAIT_L(n) asm volatile("s_waitcnt lgkmcnt(" #n ")" ::: "memory")
; #define PG8_BAR __builtin_amdgcn_s_barrier()
;     ...
;         for (int t = 0; t < nt; t += 2) {
;             const bool last = (t == nt - 2);
;             const char* a1 = cA + (size_t)(t + 1) * kstepA;
;             const char* a2 = last ? nA : cA + (size_t)(t + 2) * kstepA; const char* b2 = last ? nB : cB + (size_t)(t + 2) * kstepB;
;             const char* a3 = a2 + kstepA; const char* b3 = b2 + kstepB;
;             unsigned vs[2][2];
;             if constexpr (GATHER) {
;                 if (last && has_next) {
; #pragma unroll
;                     for (int hh = 0; hh < 2; ++hh)
; #pragma unroll
;                         for (int i = 0; i < 2; ++i) voffN[hh][i] = (unsigned)idxl[(ui + 1) * 256 + hh * HALF + sR[i]] * (unsigned)(K * 2) + (unsigned)sC[i] * 2u;
;                 }
; #pragma unroll
;                 for (int hh = 0; hh < 2; ++hh)
; #pragma unroll
;                     for (int i = 0; i < 2; ++i) vs[hh][i] = last ? voffN[hh][i] : voffA[hh][i];
;             } else {
; #pragma unroll
;                 for (int hh = 0; hh < 2; ++hh)
; #pragma unroll
;                     for (int i = 0; i < 2; ++i) vs[hh][i] = voffA[hh][i];
;             }
;             PG8_LDB(B0, 0, 0); PG8_LDB(B1, 0, 1); PG8_SCHED; PG8_LDA(At, 0, 0); PG8_STAGE(PG8_SA(1, 1), a1, voffA[1]);
;             PG8_WAIT_V(8); PG8_WAIT_L(0); PG8_BAR; if (do0) { PG8_MMA(0, 0, At, B0); PG8_MMA(0, 1, At, B1); } PG8_BAR; PG8_SCHED;
;             PG8_LDA(At, 0, 1); PG8_STAGE(PG8_SB(0, 0), b2, voffB); PG8_STAGE(PG8_SB(0, 1), b2 + hstep, voffB); PG8_STAGE(PG8_SA(0, 0), a2, vs[0]);
;             PG8_WAIT_V(8); PG8_WAIT_L(0); PG8_BAR; if (do1) { PG8_MMA(1, 0, At, B0); PG8_MMA(1, 1, At, B1); } PG8_BAR; PG8_SCHED;
;             PG8_LDB(B0, 1, 0); PG8_LDB(B1, 1, 1); PG8_SCHED; PG8_LDA(At, 1, 0); PG8_STAGE(PG8_SA(0, 1), a2, vs[1]);
;             PG8_WAIT_V(8); PG8_WAIT_L(0); PG8_BAR; if (do0) { PG8_MMA(0, 0, At, B0); PG8_MMA(0, 1, At, B1); } PG8_BAR; PG8_SCHED;
;             PG8_LDA(At, 1, 1); PG8_STAGE(PG8_SB(1, 0), b3, voffB); PG8_STAGE(PG8_SB(1, 1), b3 + hstep, voffB); PG8_STAGE(PG8_SA(1, 0), a3, vs[0]);
;             PG8_WAIT_V(8); PG8_WAIT_L(0); PG8_BAR; if (do1) { PG8_MMA(1, 0, At, B0); PG8_MMA(1, 1, At, B1); } PG8_BAR; PG8_SCHED;
.LBB0_460:
	ds_read_b128 v[130:133], v203
	ds_read_b128 v[134:137], v204
	ds_read_b128 v[138:141], v205
	ds_read_b128 v[142:145], v206
	ds_read_b128 v[168:171], v207
	ds_read_b128 v[172:175], v208
	ds_read_b128 v[176:179], v209
	ds_read_b128 v[180:183], v210
	s_add_u32 s4, s2, 0x80
	s_addc_u32 s5, s3, 0
	s_cmp_eq_u32 s41, 12
	s_cselect_b32 s39, s9, s5
	s_cselect_b32 s38, s12, s4
	s_cselect_b32 s5, s27, s40
	s_cselect_b32 s4, s29, s37
	v_lshl_add_u64 v[196:197], s[2:3], 0, v[162:163]
	s_add_i32 m0, s50, 0xc000
	ds_read_b128 v[184:187], v211
	ds_read_b128 v[188:191], v211 offset:2048
	ds_read_b128 v[192:195], v212
	ds_read_b128 v[220:223], v212 offset:2048
	ds_read_b128 v[224:227], v211 offset:4096
	ds_read_b128 v[228:231], v211 offset:6144
	ds_read_b128 v[232:235], v212 offset:4096
	ds_read_b128 v[236:239], v212 offset:6144
	global_load_lds_dwordx4 v[196:197], off
	v_lshl_add_u64 v[196:197], s[2:3], 0, v[160:161]
	s_add_i32 m0, s50, 0xe000
	s_add_u32 s6, s4, 0x4000
	global_load_lds_dwordx4 v[196:197], off
	s_waitcnt vmcnt(8)
	s_waitcnt lgkmcnt(0)
	s_addc_u32 s7, s5, 0
	s_barrier
	s_setprio 1
	v_mfma_f32_16x16x32_bf16 v[126:129], v[130:133], v[184:187], v[126:129]
	v_mfma_f32_16x16x32_bf16 v[58:61], v[138:141], v[184:187], v[58:61]
	v_mfma_f32_16x16x32_bf16 v[122:125], v[130:133], v[188:191], v[122:125]
	v_mfma_f32_16x16x32_bf16 v[118:121], v[138:141], v[188:191], v[118:121]
	v_mfma_f32_16x16x32_bf16 v[114:117], v[130:133], v[224:227], v[114:117]
	v_mfma_f32_16x16x32_bf16 v[110:113], v[138:141], v[224:227], v[110:113]
	v_mfma_f32_16x16x32_bf16 v[106:109], v[130:133], v[228:231], v[106:109]
	v_mfma_f32_16x16x32_bf16 v[102:105], v[138:141], v[228:231], v[102:105]
	v_mfma_f32_16x16x32_bf16 v[126:129], v[134:137], v[192:195], v[126:129]
	v_mfma_f32_16x16x32_bf16 v[58:61], v[142:145], v[192:195], v[58:61]
	v_mfma_f32_16x16x32_bf16 v[122:125], v[134:137], v[220:223], v[122:125]
	v_mfma_f32_16x16x32_bf16 v[118:121], v[142:145], v[220:223], v[118:121]
	v_mfma_f32_16x16x32_bf16 v[114:117], v[134:137], v[232:235], v[114:117]
	v_mfma_f32_16x16x32_bf16 v[110:113], v[142:145], v[232:235], v[110:113]
	v_mfma_f32_16x16x32_bf16 v[106:109], v[134:137], v[236:239], v[106:109]
	v_mfma_f32_16x16x32_bf16 v[102:105], v[142:145], v[236:239], v[102:105]
	v_mfma_f32_16x16x32_bf16 v[66:69], v[168:171], v[184:187], v[66:69]
	v_mfma_f32_16x16x32_bf16 v[50:53], v[176:179], v[184:187], v[50:53]
	v_mfma_f32_16x16x32_bf16 v[54:57], v[168:171], v[188:191], v[54:57]
	v_mfma_f32_16x16x32_bf16 v[42:45], v[176:179], v[188:191], v[42:45]
	v_mfma_f32_16x16x32_bf16 v[46:49], v[168:171], v[224:227], v[46:49]
	v_mfma_f32_16x16x32_bf16 v[34:37], v[176:179], v[224:227], v[34:37]
	v_mfma_f32_16x16x32_bf16 v[98:101], v[168:171], v[228:231], v[98:101]
	v_mfma_f32_16x16x32_bf16 v[38:41], v[176:179], v[228:231], v[38:41]
	v_mfma_f32_16x16x32_bf16 v[66:69], v[172:175], v[192:195], v[66:69]
	v_mfma_f32_16x16x32_bf16 v[50:53], v[180:183], v[192:195], v[50:53]
	v_mfma_f32_16x16x32_bf16 v[54:57], v[172:175], v[220:223], v[54:57]
	v_mfma_f32_16x16x32_bf16 v[42:45], v[180:183], v[220:223], v[42:45]
	v_mfma_f32_16x16x32_bf16 v[46:49], v[172:175], v[232:235], v[46:49]
	v_mfma_f32_16x16x32_bf16 v[34:37], v[180:183], v[232:235], v[34:37]
	v_mfma_f32_16x16x32_bf16 v[98:101], v[172:175], v[236:239], v[98:101]
	v_mfma_f32_16x16x32_bf16 v[38:41], v[180:183], v[236:239], v[38:41]
	s_setprio 0
	s_barrier
	s_add_i32 s42, s65, s49
	v_lshl_add_u64 v[196:197], s[4:5], 0, v[146:147]
	s_mov_b32 m0, s42
	ds_read_b128 v[184:187], v211 offset:16384
	ds_read_b128 v[188:191], v211 offset:18432
	ds_read_b128 v[192:195], v212 offset:16384
	ds_read_b128 v[220:223], v212 offset:18432
	ds_read_b128 v[224:227], v211 offset:20480
	ds_read_b128 v[228:231], v211 offset:22528
	ds_read_b128 v[232:235], v212 offset:20480
	ds_read_b128 v[236:239], v212 offset:22528
	global_load_lds_dwordx4 v[196:197], off
	s_add_i32 m0, s42, 0x2000
	s_add_u32 s42, s4, 0x40000
	v_lshl_add_u64 v[196:197], s[4:5], 0, v[148:149]
	s_addc_u32 s43, s5, 0
	s_add_i32 s74, s66, s49
	global_load_lds_dwordx4 v[196:197], off
	v_lshl_add_u64 v[196:197], s[42:43], 0, v[146:147]
	s_mov_b32 m0, s74
	v_lshl_add_u64 v[240:241], s[38:39], 0, v[152:153]
	global_load_lds_dwordx4 v[196:197], off
	v_lshl_add_u64 v[196:197], s[42:43], 0, v[148:149]
	s_add_i32 m0, s74, 0x2000
	s_nop 0
	global_load_lds_dwordx4 v[196:197], off
	v_lshl_add_u64 v[196:197], s[38:39], 0, v[150:151]
	s_mov_b32 m0, s50
	s_nop 0
	global_load_lds_dwordx4 v[196:197], off
	s_mov_b32 m0, s51
	s_nop 0
	global_load_lds_dwordx4 v[240:241], off
	s_waitcnt vmcnt(8)
	s_waitcnt lgkmcnt(0)
	s_barrier
; #define PG8_STAGE(bufoff, gbase, voff) do { _Pragma("unroll") for (int _i = 0; _i < 2; ++_i) \
;         __builtin_amdgcn_global_load_lds((const unsigned*)((const char*)(gbase) + (voff)[_i]), (LAS unsigned*)(lds + (bufoff) + ldsw + _i * 8192), 16, 0, 0); } while (0)
; #define PG8_LDA(dst, b, h) do { _Pragma("unroll") for (int m = 0; m < 4; ++m) _Pragma("unroll") for (int k = 0; k < 2; ++k) dst[m][k] = *(const LAS bf16x8*)(lds + PG8_SA(b, h) + ((aoff ^ (k * 64)) + m * 2048)); } while (0)
; #define PG8_LDB(dst, b, h) do { _Pragma("unroll") for (int n = 0; n < 2; ++n) _Pragma("unroll") for (int k = 0; k < 2; ++k) dst[n][k] = *(const LAS bf16x8*)(lds + PG8_SB(b, h) + ((boff ^ (k * 64)) + n * 2048)); } while (0)
; #define PG8_MMA(ai, bj, At, Bt) do { __builtin_amdgcn_s_setprio(1); _Pragma("unroll") for (int m = 0; m < 4; ++m) _Pragma("unroll") for (int n = 0; n < 2; ++n) _Pragma("unroll") for (int k = 0; k < 2; ++k) \
;         acc[ai][bj][m][n] = __builtin_amdgcn_mfma_f32_16x16x32_bf16(Bt[n][k], At[m][k], acc[ai][bj][m][n], 0, 0, 0); __builtin_amdgcn_s_setprio(0); } while (0)
; #define PG8_WAIT_V(n) asm volatile("s_waitcnt vmcnt(" #n ")" ::: "memory")
; #define PG8_WAIT_L(n) asm volatile("s_waitcnt lgkmcnt(" #n ")" ::: "memory")
; #define PG8_BAR __builtin_amdgcn_s_barrier()
;     ...
;             PG8_LDB(B0, 0, 0); PG8_LDB(B1, 0, 1); PG8_SCHED; PG8_LDA(At, 0, 0); PG8_STAGE(PG8_SA(1, 1), a1, voffA[1]);
;             PG8_WAIT_V(8); PG8_WAIT_L(0); PG8_BAR; if (do0) { PG8_MMA(0, 0, At, B0); PG8_MMA(0, 1, At, B1); } PG8_BAR; PG8_SCHED;
;             PG8_LDA(At, 0, 1); PG8_STAGE(PG8_SB(0, 0), b2, voffB); PG8_STAGE(PG8_SB(0, 1), b2 + hstep, voffB); PG8_STAGE(PG8_SA(0, 0), a2, vs[0]);
;             PG8_WAIT_V(8); PG8_WAIT_L(0); PG8_BAR; if (do1) { PG8_MMA(1, 0, At, B0); PG8_MMA(1, 1, At, B1); } PG8_BAR; PG8_SCHED;
;             PG8_LDB(B0, 1, 0); PG8_LDB(B1, 1, 1); PG8_SCHED; PG8_LDA(At, 1, 0); PG8_STAGE(PG8_SA(0, 1), a2, vs[1]);
;             PG8_WAIT_V(8); PG8_WAIT_L(0); PG8_BAR; if (do0) { PG8_MMA(0, 0, At, B0); PG8_MMA(0, 1, At, B1); } PG8_BAR; PG8_SCHED;
;             PG8_LDA(At, 1, 1); PG8_STAGE(PG8_SB(1, 0), b3, voffB); PG8_STAGE(PG8_SB(1, 1), b3 + hstep, voffB); PG8_STAGE(PG8_SA(1, 0), a3, vs[0]);
;             PG8_WAIT_V(8); PG8_WAIT_L(0); PG8_BAR; if (do1) { PG8_MMA(1, 0, At, B0); PG8_MMA(1, 1, At, B1); } PG8_BAR; PG8_SCHED;
	s_setprio 1
	v_mfma_f32_16x16x32_bf16 v[94:97], v[130:133], v[184:187], v[94:97]
	v_mfma_f32_16x16x32_bf16 v[26:29], v[138:141], v[184:187], v[26:29]
	v_mfma_f32_16x16x32_bf16 v[90:93], v[130:133], v[188:191], v[90:93]
	v_mfma_f32_16x16x32_bf16 v[86:89], v[138:141], v[188:191], v[86:89]
	v_mfma_f32_16x16x32_bf16 v[82:85], v[130:133], v[224:227], v[82:85]
	v_mfma_f32_16x16x32_bf16 v[78:81], v[138:141], v[224:227], v[78:81]
	v_mfma_f32_16x16x32_bf16 v[74:77], v[130:133], v[228:231], v[74:77]
	v_mfma_f32_16x16x32_bf16 v[70:73], v[138:141], v[228:231], v[70:73]
	v_mfma_f32_16x16x32_bf16 v[94:97], v[134:137], v[192:195], v[94:97]
	v_mfma_f32_16x16x32_bf16 v[26:29], v[142:145], v[192:195], v[26:29]
	v_mfma_f32_16x16x32_bf16 v[90:93], v[134:137], v[220:223], v[90:93]
	v_mfma_f32_16x16x32_bf16 v[86:89], v[142:145], v[220:223], v[86:89]
	v_mfma_f32_16x16x32_bf16 v[82:85], v[134:137], v[232:235], v[82:85]
	v_mfma_f32_16x16x32_bf16 v[78:81], v[142:145], v[232:235], v[78:81]
	v_mfma_f32_16x16x32_bf16 v[74:77], v[134:137], v[236:239], v[74:77]
	v_mfma_f32_16x16x32_bf16 v[70:73], v[142:145], v[236:239], v[70:73]
	v_mfma_f32_16x16x32_bf16 v[30:33], v[168:171], v[184:187], v[30:33]
	v_mfma_f32_16x16x32_bf16 v[18:21], v[176:179], v[184:187], v[18:21]
	v_mfma_f32_16x16x32_bf16 v[22:25], v[168:171], v[188:191], v[22:25]
	v_mfma_f32_16x16x32_bf16 v[10:13], v[176:179], v[188:191], v[10:13]
	v_mfma_f32_16x16x32_bf16 v[14:17], v[168:171], v[224:227], v[14:17]
	v_mfma_f32_16x16x32_bf16 v[2:5], v[176:179], v[224:227], v[2:5]
	v_mfma_f32_16x16x32_bf16 v[62:65], v[168:171], v[228:231], v[62:65]
	v_mfma_f32_16x16x32_bf16 v[6:9], v[176:179], v[228:231], v[6:9]
	v_mfma_f32_16x16x32_bf16 v[30:33], v[172:175], v[192:195], v[30:33]
	v_mfma_f32_16x16x32_bf16 v[18:21], v[180:183], v[192:195], v[18:21]
	v_mfma_f32_16x16x32_bf16 v[22:25], v[172:175], v[220:223], v[22:25]
	v_mfma_f32_16x16x32_bf16 v[10:13], v[180:183], v[220:223], v[10:13]
	v_mfma_f32_16x16x32_bf16 v[14:17], v[172:175], v[232:235], v[14:17]
	v_mfma_f32_16x16x32_bf16 v[2:5], v[180:183], v[232:235], v[2:5]
	v_mfma_f32_16x16x32_bf16 v[62:65], v[172:175], v[236:239], v[62:65]
	v_mfma_f32_16x16x32_bf16 v[6:9], v[180:183], v[236:239], v[6:9]
	s_setprio 0
	s_barrier
	s_add_i32 s42, 0, 0x18000
	s_add_i32 s43, 0, 0x1c000
	v_add_u32_e32 v130, s42, v201
	v_add_u32_e32 v134, s42, v202
	v_add_u32_e32 v158, s43, v201
	v_add_u32_e32 v172, s43, v202
	ds_read_b128 v[130:133], v130
	ds_read_b128 v[134:137], v134
	ds_read_b128 v[138:141], v213
	ds_read_b128 v[142:145], v214
	ds_read_b128 v[168:171], v158
	ds_read_b128 v[172:175], v172
	ds_read_b128 v[176:179], v215
	ds_read_b128 v[180:183], v216
	s_mov_b32 m0, s52
	v_lshl_add_u64 v[242:243], s[38:39], 0, v[154:155]
	ds_read_b128 v[184:187], v211 offset:32768
	ds_read_b128 v[188:191], v211 offset:34816
	ds_read_b128 v[192:195], v212 offset:32768
	ds_read_b128 v[220:223], v212 offset:34816
	ds_read_b128 v[224:227], v211 offset:36864
	ds_read_b128 v[228:231], v211 offset:38912
	ds_read_b128 v[232:235], v212 offset:36864
	ds_read_b128 v[236:239], v212 offset:38912
	global_load_lds_dwordx4 v[242:243], off
	v_lshl_add_u64 v[242:243], s[38:39], 0, v[156:157]
	s_mov_b32 m0, s53
	s_nop 0
	global_load_lds_dwordx4 v[242:243], off
	s_waitcnt vmcnt(8)
	s_waitcnt lgkmcnt(0)
	s_barrier
	s_setprio 1
	v_mfma_f32_16x16x32_bf16 v[126:129], v[130:133], v[184:187], v[126:129]
	v_mfma_f32_16x16x32_bf16 v[58:61], v[138:141], v[184:187], v[58:61]
	v_mfma_f32_16x16x32_bf16 v[122:125], v[130:133], v[188:191], v[122:125]
	v_mfma_f32_16x16x32_bf16 v[118:121], v[138:141], v[188:191], v[118:121]
	v_mfma_f32_16x16x32_bf16 v[114:117], v[130:133], v[224:227], v[114:117]
	v_mfma_f32_16x16x32_bf16 v[110:113], v[138:141], v[224:227], v[110:113]
	v_mfma_f32_16x16x32_bf16 v[106:109], v[130:133], v[228:231], v[106:109]
	v_mfma_f32_16x16x32_bf16 v[102:105], v[138:141], v[228:231], v[102:105]
	v_mfma_f32_16x16x32_bf16 v[126:129], v[134:137], v[192:195], v[126:129]
	v_mfma_f32_16x16x32_bf16 v[58:61], v[142:145], v[192:195], v[58:61]
	v_mfma_f32_16x16x32_bf16 v[122:125], v[134:137], v[220:223], v[122:125]
	v_mfma_f32_16x16x32_bf16 v[118:121], v[142:145], v[220:223], v[118:121]
	v_mfma_f32_16x16x32_bf16 v[114:117], v[134:137], v[232:235], v[114:117]
	v_mfma_f32_16x16x32_bf16 v[110:113], v[142:145], v[232:235], v[110:113]
	v_mfma_f32_16x16x32_bf16 v[106:109], v[134:137], v[236:239], v[106:109]
	v_mfma_f32_16x16x32_bf16 v[102:105], v[142:145], v[236:239], v[102:105]
	v_mfma_f32_16x16x32_bf16 v[66:69], v[168:171], v[184:187], v[66:69]
	v_mfma_f32_16x16x32_bf16 v[50:53], v[176:179], v[184:187], v[50:53]
	v_mfma_f32_16x16x32_bf16 v[54:57], v[168:171], v[188:191], v[54:57]
	v_mfma_f32_16x16x32_bf16 v[42:45], v[176:179], v[188:191], v[42:45]
	v_mfma_f32_16x16x32_bf16 v[46:49], v[168:171], v[224:227], v[46:49]
	v_mfma_f32_16x16x32_bf16 v[34:37], v[176:179], v[224:227], v[34:37]
	v_mfma_f32_16x16x32_bf16 v[98:101], v[168:171], v[228:231], v[98:101]
	v_mfma_f32_16x16x32_bf16 v[38:41], v[176:179], v[228:231], v[38:41]
	v_mfma_f32_16x16x32_bf16 v[66:69], v[172:175], v[192:195], v[66:69]
	v_mfma_f32_16x16x32_bf16 v[50:53], v[180:183], v[192:195], v[50:53]
	v_mfma_f32_16x16x32_bf16 v[54:57], v[172:175], v[220:223], v[54:57]
	v_mfma_f32_16x16x32_bf16 v[42:45], v[180:183], v[220:223], v[42:45]
	v_mfma_f32_16x16x32_bf16 v[46:49], v[172:175], v[232:235], v[46:49]
	v_mfma_f32_16x16x32_bf16 v[34:37], v[180:183], v[232:235], v[34:37]
	v_mfma_f32_16x16x32_bf16 v[98:101], v[172:175], v[236:239], v[98:101]
	v_mfma_f32_16x16x32_bf16 v[38:41], v[180:183], v[236:239], v[38:41]
	s_setprio 0
	s_barrier
; #define PG8_STAGE(bufoff, gbase, voff) do { _Pragma("unroll") for (int _i = 0; _i < 2; ++_i) \
;         __builtin_amdgcn_global_load_lds((const unsigned*)((const char*)(gbase) + (voff)[_i]), (LAS unsigned*)(lds + (bufoff) + ldsw + _i * 8192), 16, 0, 0); } while (0)
; #define PG8_LDA(dst, b, h) do { _Pragma("unroll") for (int m = 0; m < 4; ++m) _Pragma("unroll") for (int k = 0; k < 2; ++k) dst[m][k] = *(const LAS bf16x8*)(lds + PG8_SA(b, h) + ((aoff ^ (k * 64)) + m * 2048)); } while (0)
; #define PG8_MMA(ai, bj, At, Bt) do { __builtin_amdgcn_s_setprio(1); _Pragma("unroll") for (int m = 0; m < 4; ++m) _Pragma("unroll") for (int n = 0; n < 2; ++n) _Pragma("unroll") for (int k = 0; k < 2; ++k) \
;         acc[ai][bj][m][n] = __builtin_amdgcn_mfma_f32_16x16x32_bf16(Bt[n][k], At[m][k], acc[ai][bj][m][n], 0, 0, 0); __builtin_amdgcn_s_setprio(0); } while (0)
; #define PG8_WAIT_V(n) asm volatile("s_waitcnt vmcnt(" #n ")" ::: "memory")
; #define PG8_WAIT_L(n) asm volatile("s_waitcnt lgkmcnt(" #n ")" ::: "memory")
; #define PG8_BAR __builtin_amdgcn_s_barrier()
; #define PG8_SCHED __builtin_amdgcn_sched_barrier(0)
;     ...
;             PG8_LDA(At, 1, 1); PG8_STAGE(PG8_SB(1, 0), b3, voffB); PG8_STAGE(PG8_SB(1, 1), b3 + hstep, voffB); PG8_STAGE(PG8_SA(1, 0), a3, vs[0]);
;             PG8_WAIT_V(8); PG8_WAIT_L(0); PG8_BAR; if (do1) { PG8_MMA(1, 0, At, B0); PG8_MMA(1, 1, At, B1); } PG8_BAR; PG8_SCHED;
;         }
	s_add_i32 s38, s42, s49
	v_lshl_add_u64 v[242:243], s[6:7], 0, v[146:147]
	s_mov_b32 m0, s38
	ds_read_b128 v[184:187], v211 offset:49152
	ds_read_b128 v[188:191], v211 offset:51200
	ds_read_b128 v[192:195], v212 offset:49152
	ds_read_b128 v[220:223], v212 offset:51200
	ds_read_b128 v[224:227], v211 offset:53248
	ds_read_b128 v[228:231], v211 offset:55296
	ds_read_b128 v[232:235], v212 offset:53248
	ds_read_b128 v[236:239], v212 offset:55296
	global_load_lds_dwordx4 v[242:243], off
	s_add_i32 m0, s38, 0x2000
	s_add_u32 s4, s4, 0x44000
	v_lshl_add_u64 v[242:243], s[6:7], 0, v[148:149]
	s_addc_u32 s5, s5, 0
	s_add_i32 s6, s43, s49
	global_load_lds_dwordx4 v[242:243], off
	v_lshl_add_u64 v[242:243], s[4:5], 0, v[146:147]
	s_mov_b32 m0, s6
	v_lshl_add_u64 v[196:197], v[196:197], 0, s[92:93]
	global_load_lds_dwordx4 v[242:243], off
	v_lshl_add_u64 v[242:243], s[4:5], 0, v[148:149]
	s_add_i32 m0, s6, 0x2000
	s_nop 0
	global_load_lds_dwordx4 v[242:243], off
	s_mov_b32 m0, s55
	s_nop 0
	global_load_lds_dwordx4 v[196:197], off
	v_lshl_add_u64 v[196:197], v[240:241], 0, s[92:93]
	s_mov_b32 m0, s56
	s_nop 0
	global_load_lds_dwordx4 v[196:197], off
	s_waitcnt vmcnt(8)
	s_waitcnt lgkmcnt(0)
	s_barrier
	s_setprio 1
	v_mfma_f32_16x16x32_bf16 v[94:97], v[130:133], v[184:187], v[94:97]
	v_mfma_f32_16x16x32_bf16 v[26:29], v[138:141], v[184:187], v[26:29]
	v_mfma_f32_16x16x32_bf16 v[90:93], v[130:133], v[188:191], v[90:93]
	v_mfma_f32_16x16x32_bf16 v[86:89], v[138:141], v[188:191], v[86:89]
	v_mfma_f32_16x16x32_bf16 v[82:85], v[130:133], v[224:227], v[82:85]
	v_mfma_f32_16x16x32_bf16 v[78:81], v[138:141], v[224:227], v[78:81]
	v_mfma_f32_16x16x32_bf16 v[74:77], v[130:133], v[228:231], v[74:77]
	v_mfma_f32_16x16x32_bf16 v[70:73], v[138:141], v[228:231], v[70:73]
	v_mfma_f32_16x16x32_bf16 v[94:97], v[134:137], v[192:195], v[94:97]
	v_mfma_f32_16x16x32_bf16 v[26:29], v[142:145], v[192:195], v[26:29]
	v_mfma_f32_16x16x32_bf16 v[90:93], v[134:137], v[220:223], v[90:93]
	v_mfma_f32_16x16x32_bf16 v[86:89], v[142:145], v[220:223], v[86:89]
	v_mfma_f32_16x16x32_bf16 v[82:85], v[134:137], v[232:235], v[82:85]
	v_mfma_f32_16x16x32_bf16 v[78:81], v[142:145], v[232:235], v[78:81]
	v_mfma_f32_16x16x32_bf16 v[74:77], v[134:137], v[236:239], v[74:77]
	v_mfma_f32_16x16x32_bf16 v[70:73], v[142:145], v[236:239], v[70:73]
	v_mfma_f32_16x16x32_bf16 v[30:33], v[168:171], v[184:187], v[30:33]
	v_mfma_f32_16x16x32_bf16 v[18:21], v[176:179], v[184:187], v[18:21]
	v_mfma_f32_16x16x32_bf16 v[22:25], v[168:171], v[188:191], v[22:25]
	v_mfma_f32_16x16x32_bf16 v[10:13], v[176:179], v[188:191], v[10:13]
	v_mfma_f32_16x16x32_bf16 v[14:17], v[168:171], v[224:227], v[14:17]
	v_mfma_f32_16x16x32_bf16 v[2:5], v[176:179], v[224:227], v[2:5]
	v_mfma_f32_16x16x32_bf16 v[62:65], v[168:171], v[228:231], v[62:65]
	v_mfma_f32_16x16x32_bf16 v[6:9], v[176:179], v[228:231], v[6:9]
	v_mfma_f32_16x16x32_bf16 v[30:33], v[172:175], v[192:195], v[30:33]
	v_mfma_f32_16x16x32_bf16 v[18:21], v[180:183], v[192:195], v[18:21]
	v_mfma_f32_16x16x32_bf16 v[22:25], v[172:175], v[220:223], v[22:25]
	v_mfma_f32_16x16x32_bf16 v[10:13], v[180:183], v[220:223], v[10:13]
	v_mfma_f32_16x16x32_bf16 v[14:17], v[172:175], v[232:235], v[14:17]
	v_mfma_f32_16x16x32_bf16 v[2:5], v[180:183], v[232:235], v[2:5]
	v_mfma_f32_16x16x32_bf16 v[62:65], v[172:175], v[236:239], v[62:65]
	v_mfma_f32_16x16x32_bf16 v[6:9], v[180:183], v[236:239], v[6:9]
	s_setprio 0
	s_barrier
	s_add_i32 s41, s41, 2
	s_add_u32 s37, s37, 0x8000
	s_addc_u32 s40, s40, 0
	s_add_u32 s2, s2, 0x100
	s_addc_u32 s3, s3, 0
	s_cmp_gt_u32 s41, 13
	s_cbranch_scc0 .LBB0_460
	s_and_b64 vcc, exec, s[24:25]
	s_cbranch_vccz .LBB0_463
	s_barrier

; #define PG8_WAIT_V(n) asm volatile("s_waitcnt vmcnt(" #n ")" ::: "memory")
; #define PG8_WAIT_L(n) asm volatile("s_waitcnt lgkmcnt(" #n ")" ::: "memory")
; #define PG8_BAR __builtin_amdgcn_s_barrier()
;     ...
;         for (int t = 0; t < nt; t += 2) {
;             const bool last = (t == nt - 2);
;             const char* a1 = cA + (size_t)(t + 1) * kstepA;
;             const char* a2 = last ? nA : cA + (size_t)(t + 2) * kstepA; const char* b2 = last ? nB : cB + (size_t)(t + 2) * kstepB;
;             const char* a3 = a2 + kstepA; const char* b3 = b2 + kstepB;
;             unsigned vs[2][2];
;             if constexpr (GATHER) {
;                 if (last && has_next) {
; #pragma unroll
;                     for (int hh = 0; hh < 2; ++hh)
; #pragma unroll
;                         for (int i = 0; i < 2; ++i) voffN[hh][i] = (unsigned)idxl[(ui + 1) * 256 + hh * HALF + sR[i]] * (unsigned)(K * 2) + (unsigned)sC[i] * 2u;
;                 }
; #pragma unroll
;                 for (int hh = 0; hh < 2; ++hh)
; #pragma unroll
;                     for (int i = 0; i < 2; ++i) vs[hh][i] = last ? voffN[hh][i] : voffA[hh][i];
;             } else {
; #pragma unroll
;                 for (int hh = 0; hh < 2; ++hh)
; #pragma unroll
;                     for (int i = 0; i < 2; ++i) vs[hh][i] = voffA[hh][i];
;             }
;             PG8_LDB(B0, 0, 0); PG8_LDB(B1, 0, 1); PG8_SCHED; PG8_LDA(At, 0, 0); PG8_STAGE(PG8_SA(1, 1), a1, voffA[1]);
;             PG8_WAIT_V(8); PG8_WAIT_L(0); PG8_BAR; if (do0) { PG8_MMA(0, 0, At, B0); PG8_MMA(0, 1, At, B1); } PG8_BAR; PG8_SCHED;
;             PG8_LDA(At, 0, 1); PG8_STAGE(PG8_SB(0, 0), b2, voffB); PG8_STAGE(PG8_SB(0, 1), b2 + hstep, voffB); PG8_STAGE(PG8_SA(0, 0), a2, vs[0]);
;             PG8_WAIT_V(8); PG8_WAIT_L(0); PG8_BAR; if (do1) { PG8_MMA(1, 0, At, B0); PG8_MMA(1, 1, At, B1); } PG8_BAR; PG8_SCHED;
;             PG8_LDB(B0, 1, 0); PG8_LDB(B1, 1, 1); PG8_SCHED; PG8_LDA(At, 1, 0); PG8_STAGE(PG8_SA(0, 1), a2, vs[1]);
;             PG8_WAIT_V(8); PG8_WAIT_L(0); PG8_BAR; if (do0) { PG8_MMA(0, 0, At, B0); PG8_MMA(0, 1, At, B1); } PG8_BAR; PG8_SCHED;
;             PG8_LDA(At, 1, 1); PG8_STAGE(PG8_SB(1, 0), b3, voffB); PG8_STAGE(PG8_SB(1, 1), b3 + hstep, voffB); PG8_STAGE(PG8_SA(1, 0), a3, vs[0]);
;             PG8_WAIT_V(8); PG8_WAIT_L(0); PG8_BAR; if (do1) { PG8_MMA(1, 0, At, B0); PG8_MMA(1, 1, At, B1); } PG8_BAR; PG8_SCHED;
.LBB0_557:
	ds_read_b128 v[130:133], v199
	ds_read_b128 v[134:137], v200
	ds_read_b128 v[138:141], v201
	ds_read_b128 v[142:145], v202
	ds_read_b128 v[164:167], v203
	ds_read_b128 v[168:171], v204
	ds_read_b128 v[172:175], v205
	ds_read_b128 v[176:179], v206
	s_add_u32 s2, s0, 0x80
	s_addc_u32 s3, s1, 0
	s_cmp_eq_u32 s41, 12
	s_cselect_b32 s39, s7, s3
	s_cselect_b32 s38, s8, s2
	s_cselect_b32 s3, s25, s40
	s_cselect_b32 s2, s27, s37
	v_lshl_add_u64 v[192:193], s[0:1], 0, v[162:163]
	s_add_i32 m0, s50, 0xc000
	ds_read_b128 v[180:183], v207
	ds_read_b128 v[184:187], v207 offset:2048
	ds_read_b128 v[188:191], v208
	ds_read_b128 v[216:219], v208 offset:2048
	ds_read_b128 v[220:223], v207 offset:4096
	ds_read_b128 v[224:227], v207 offset:6144
	ds_read_b128 v[228:231], v208 offset:4096
	ds_read_b128 v[232:235], v208 offset:6144
	global_load_lds_dwordx4 v[192:193], off
	v_lshl_add_u64 v[192:193], s[0:1], 0, v[160:161]
	s_add_i32 m0, s50, 0xe000
	s_add_u32 s4, s2, 0x4000
	global_load_lds_dwordx4 v[192:193], off
	s_waitcnt vmcnt(8)
	s_waitcnt lgkmcnt(0)
	s_addc_u32 s5, s3, 0
	s_barrier
	s_setprio 1
	v_mfma_f32_16x16x32_bf16 v[126:129], v[130:133], v[180:183], v[126:129]
	v_mfma_f32_16x16x32_bf16 v[58:61], v[138:141], v[180:183], v[58:61]
	v_mfma_f32_16x16x32_bf16 v[122:125], v[130:133], v[184:187], v[122:125]
	v_mfma_f32_16x16x32_bf16 v[118:121], v[138:141], v[184:187], v[118:121]
	v_mfma_f32_16x16x32_bf16 v[114:117], v[130:133], v[220:223], v[114:117]
	v_mfma_f32_16x16x32_bf16 v[110:113], v[138:141], v[220:223], v[110:113]
	v_mfma_f32_16x16x32_bf16 v[106:109], v[130:133], v[224:227], v[106:109]
	v_mfma_f32_16x16x32_bf16 v[102:105], v[138:141], v[224:227], v[102:105]
	v_mfma_f32_16x16x32_bf16 v[126:129], v[134:137], v[188:191], v[126:129]
	v_mfma_f32_16x16x32_bf16 v[58:61], v[142:145], v[188:191], v[58:61]
	v_mfma_f32_16x16x32_bf16 v[122:125], v[134:137], v[216:219], v[122:125]
	v_mfma_f32_16x16x32_bf16 v[118:121], v[142:145], v[216:219], v[118:121]
	v_mfma_f32_16x16x32_bf16 v[114:117], v[134:137], v[228:231], v[114:117]
	v_mfma_f32_16x16x32_bf16 v[110:113], v[142:145], v[228:231], v[110:113]
	v_mfma_f32_16x16x32_bf16 v[106:109], v[134:137], v[232:235], v[106:109]
	v_mfma_f32_16x16x32_bf16 v[102:105], v[142:145], v[232:235], v[102:105]
	v_mfma_f32_16x16x32_bf16 v[66:69], v[164:167], v[180:183], v[66:69]
	v_mfma_f32_16x16x32_bf16 v[50:53], v[172:175], v[180:183], v[50:53]
	v_mfma_f32_16x16x32_bf16 v[54:57], v[164:167], v[184:187], v[54:57]
	v_mfma_f32_16x16x32_bf16 v[42:45], v[172:175], v[184:187], v[42:45]
	v_mfma_f32_16x16x32_bf16 v[46:49], v[164:167], v[220:223], v[46:49]
	v_mfma_f32_16x16x32_bf16 v[34:37], v[172:175], v[220:223], v[34:37]
	v_mfma_f32_16x16x32_bf16 v[98:101], v[164:167], v[224:227], v[98:101]
	v_mfma_f32_16x16x32_bf16 v[38:41], v[172:175], v[224:227], v[38:41]
	v_mfma_f32_16x16x32_bf16 v[66:69], v[168:171], v[188:191], v[66:69]
	v_mfma_f32_16x16x32_bf16 v[50:53], v[176:179], v[188:191], v[50:53]
	v_mfma_f32_16x16x32_bf16 v[54:57], v[168:171], v[216:219], v[54:57]
	v_mfma_f32_16x16x32_bf16 v[42:45], v[176:179], v[216:219], v[42:45]
	v_mfma_f32_16x16x32_bf16 v[46:49], v[168:171], v[228:231], v[46:49]
	v_mfma_f32_16x16x32_bf16 v[34:37], v[176:179], v[228:231], v[34:37]
	v_mfma_f32_16x16x32_bf16 v[98:101], v[168:171], v[232:235], v[98:101]
	v_mfma_f32_16x16x32_bf16 v[38:41], v[176:179], v[232:235], v[38:41]
	s_setprio 0
	s_barrier
	s_add_i32 s42, s63, s49
	v_lshl_add_u64 v[192:193], s[2:3], 0, v[146:147]
	s_mov_b32 m0, s42
	ds_read_b128 v[180:183], v207 offset:16384
	ds_read_b128 v[184:187], v207 offset:18432
	ds_read_b128 v[188:191], v208 offset:16384
	ds_read_b128 v[216:219], v208 offset:18432
	ds_read_b128 v[220:223], v207 offset:20480
	ds_read_b128 v[224:227], v207 offset:22528
	ds_read_b128 v[228:231], v208 offset:20480
	ds_read_b128 v[232:235], v208 offset:22528
	global_load_lds_dwordx4 v[192:193], off
	s_add_i32 m0, s42, 0x2000
	s_add_u32 s42, s2, 0x40000
	v_lshl_add_u64 v[192:193], s[2:3], 0, v[148:149]
	s_addc_u32 s43, s3, 0
	s_add_i32 s73, s64, s49
	global_load_lds_dwordx4 v[192:193], off
	v_lshl_add_u64 v[192:193], s[42:43], 0, v[146:147]
	s_mov_b32 m0, s73
	v_lshl_add_u64 v[236:237], s[38:39], 0, v[152:153]
	global_load_lds_dwordx4 v[192:193], off
	v_lshl_add_u64 v[192:193], s[42:43], 0, v[148:149]
	s_add_i32 m0, s73, 0x2000
	s_nop 0
	global_load_lds_dwordx4 v[192:193], off
	v_lshl_add_u64 v[192:193], s[38:39], 0, v[150:151]
	s_mov_b32 m0, s50
	s_nop 0
	global_load_lds_dwordx4 v[192:193], off
	s_mov_b32 m0, s51
	s_nop 0
	global_load_lds_dwordx4 v[236:237], off
	s_waitcnt vmcnt(8)
	s_waitcnt lgkmcnt(0)
	s_barrier
; #define PG8_STAGE(bufoff, gbase, voff) do { _Pragma("unroll") for (int _i = 0; _i < 2; ++_i) \
;         __builtin_amdgcn_global_load_lds((const unsigned*)((const char*)(gbase) + (voff)[_i]), (LAS unsigned*)(lds + (bufoff) + ldsw + _i * 8192), 16, 0, 0); } while (0)
; #define PG8_LDA(dst, b, h) do { _Pragma("unroll") for (int m = 0; m < 4; ++m) _Pragma("unroll") for (int k = 0; k < 2; ++k) dst[m][k] = *(const LAS bf16x8*)(lds + PG8_SA(b, h) + ((aoff ^ (k * 64)) + m * 2048)); } while (0)
; #define PG8_LDB(dst, b, h) do { _Pragma("unroll") for (int n = 0; n < 2; ++n) _Pragma("unroll") for (int k = 0; k < 2; ++k) dst[n][k] = *(const LAS bf16x8*)(lds + PG8_SB(b, h) + ((boff ^ (k * 64)) + n * 2048)); } while (0)
; #define PG8_MMA(ai, bj, At, Bt) do { __builtin_amdgcn_s_setprio(1); _Pragma("unroll") for (int m = 0; m < 4; ++m) _Pragma("unroll") for (int n = 0; n < 2; ++n) _Pragma("unroll") for (int k = 0; k < 2; ++k) \
;         acc[ai][bj][m][n] = __builtin_amdgcn_mfma_f32_16x16x32_bf16(Bt[n][k], At[m][k], acc[ai][bj][m][n], 0, 0, 0); __builtin_amdgcn_s_setprio(0); } while (0)
; #define PG8_WAIT_V(n) asm volatile("s_waitcnt vmcnt(" #n ")" ::: "memory")
; #define PG8_WAIT_L(n) asm volatile("s_waitcnt lgkmcnt(" #n ")" ::: "memory")
; #define PG8_BAR __builtin_amdgcn_s_barrier()
; #define PG8_SCHED __builtin_amdgcn_sched_barrier(0)
;     ...
;             PG8_LDA(At, 0, 1); PG8_STAGE(PG8_SB(0, 0), b2, voffB); PG8_STAGE(PG8_SB(0, 1), b2 + hstep, voffB); PG8_STAGE(PG8_SA(0, 0), a2, vs[0]);
;             PG8_WAIT_V(8); PG8_WAIT_L(0); PG8_BAR; if (do1) { PG8_MMA(1, 0, At, B0); PG8_MMA(1, 1, At, B1); } PG8_BAR; PG8_SCHED;
;             PG8_LDB(B0, 1, 0); PG8_LDB(B1, 1, 1); PG8_SCHED; PG8_LDA(At, 1, 0); PG8_STAGE(PG8_SA(0, 1), a2, vs[1]);
;             PG8_WAIT_V(8); PG8_WAIT_L(0); PG8_BAR; if (do0) { PG8_MMA(0, 0, At, B0); PG8_MMA(0, 1, At, B1); } PG8_BAR; PG8_SCHED;
	s_setprio 1
	v_mfma_f32_16x16x32_bf16 v[94:97], v[130:133], v[180:183], v[94:97]
	v_mfma_f32_16x16x32_bf16 v[26:29], v[138:141], v[180:183], v[26:29]
	v_mfma_f32_16x16x32_bf16 v[90:93], v[130:133], v[184:187], v[90:93]
	v_mfma_f32_16x16x32_bf16 v[86:89], v[138:141], v[184:187], v[86:89]
	v_mfma_f32_16x16x32_bf16 v[82:85], v[130:133], v[220:223], v[82:85]
	v_mfma_f32_16x16x32_bf16 v[78:81], v[138:141], v[220:223], v[78:81]
	v_mfma_f32_16x16x32_bf16 v[74:77], v[130:133], v[224:227], v[74:77]
	v_mfma_f32_16x16x32_bf16 v[70:73], v[138:141], v[224:227], v[70:73]
	v_mfma_f32_16x16x32_bf16 v[94:97], v[134:137], v[188:191], v[94:97]
	v_mfma_f32_16x16x32_bf16 v[26:29], v[142:145], v[188:191], v[26:29]
	v_mfma_f32_16x16x32_bf16 v[90:93], v[134:137], v[216:219], v[90:93]
	v_mfma_f32_16x16x32_bf16 v[86:89], v[142:145], v[216:219], v[86:89]
	v_mfma_f32_16x16x32_bf16 v[82:85], v[134:137], v[228:231], v[82:85]
	v_mfma_f32_16x16x32_bf16 v[78:81], v[142:145], v[228:231], v[78:81]
	v_mfma_f32_16x16x32_bf16 v[74:77], v[134:137], v[232:235], v[74:77]
	v_mfma_f32_16x16x32_bf16 v[70:73], v[142:145], v[232:235], v[70:73]
	v_mfma_f32_16x16x32_bf16 v[30:33], v[164:167], v[180:183], v[30:33]
	v_mfma_f32_16x16x32_bf16 v[18:21], v[172:175], v[180:183], v[18:21]
	v_mfma_f32_16x16x32_bf16 v[22:25], v[164:167], v[184:187], v[22:25]
	v_mfma_f32_16x16x32_bf16 v[10:13], v[172:175], v[184:187], v[10:13]
	v_mfma_f32_16x16x32_bf16 v[14:17], v[164:167], v[220:223], v[14:17]
	v_mfma_f32_16x16x32_bf16 v[2:5], v[172:175], v[220:223], v[2:5]
	v_mfma_f32_16x16x32_bf16 v[62:65], v[164:167], v[224:227], v[62:65]
	v_mfma_f32_16x16x32_bf16 v[6:9], v[172:175], v[224:227], v[6:9]
	v_mfma_f32_16x16x32_bf16 v[30:33], v[168:171], v[188:191], v[30:33]
	v_mfma_f32_16x16x32_bf16 v[18:21], v[176:179], v[188:191], v[18:21]
	v_mfma_f32_16x16x32_bf16 v[22:25], v[168:171], v[216:219], v[22:25]
	v_mfma_f32_16x16x32_bf16 v[10:13], v[176:179], v[216:219], v[10:13]
	v_mfma_f32_16x16x32_bf16 v[14:17], v[168:171], v[228:231], v[14:17]
	v_mfma_f32_16x16x32_bf16 v[2:5], v[176:179], v[228:231], v[2:5]
	v_mfma_f32_16x16x32_bf16 v[62:65], v[168:171], v[232:235], v[62:65]
	v_mfma_f32_16x16x32_bf16 v[6:9], v[176:179], v[232:235], v[6:9]
	s_setprio 0
	s_barrier
	s_add_i32 s42, 0, 0x18000
	s_add_i32 s43, 0, 0x1c000
	v_add_u32_e32 v130, s42, v196
	v_add_u32_e32 v134, s42, v197
	v_add_u32_e32 v158, s43, v196
	v_add_u32_e32 v168, s43, v197
	ds_read_b128 v[130:133], v130
	ds_read_b128 v[134:137], v134
	ds_read_b128 v[138:141], v209
	ds_read_b128 v[142:145], v210
	ds_read_b128 v[164:167], v158
	ds_read_b128 v[168:171], v168
	ds_read_b128 v[172:175], v211
	ds_read_b128 v[176:179], v212
	s_mov_b32 m0, s52
	v_lshl_add_u64 v[238:239], s[38:39], 0, v[154:155]
	ds_read_b128 v[180:183], v207 offset:32768
	ds_read_b128 v[184:187], v207 offset:34816
	ds_read_b128 v[188:191], v208 offset:32768
	ds_read_b128 v[216:219], v208 offset:34816
	ds_read_b128 v[220:223], v207 offset:36864
	ds_read_b128 v[224:227], v207 offset:38912
	ds_read_b128 v[228:231], v208 offset:36864
	ds_read_b128 v[232:235], v208 offset:38912
	global_load_lds_dwordx4 v[238:239], off
	v_lshl_add_u64 v[238:239], s[38:39], 0, v[156:157]
	s_mov_b32 m0, s53
	s_nop 0
	global_load_lds_dwordx4 v[238:239], off
	s_waitcnt vmcnt(8)
	s_waitcnt lgkmcnt(0)
	s_barrier
	s_setprio 1
	v_mfma_f32_16x16x32_bf16 v[126:129], v[130:133], v[180:183], v[126:129]
	v_mfma_f32_16x16x32_bf16 v[58:61], v[138:141], v[180:183], v[58:61]
	v_mfma_f32_16x16x32_bf16 v[122:125], v[130:133], v[184:187], v[122:125]
	v_mfma_f32_16x16x32_bf16 v[118:121], v[138:141], v[184:187], v[118:121]
	v_mfma_f32_16x16x32_bf16 v[114:117], v[130:133], v[220:223], v[114:117]
	v_mfma_f32_16x16x32_bf16 v[110:113], v[138:141], v[220:223], v[110:113]
	v_mfma_f32_16x16x32_bf16 v[106:109], v[130:133], v[224:227], v[106:109]
	v_mfma_f32_16x16x32_bf16 v[102:105], v[138:141], v[224:227], v[102:105]
	v_mfma_f32_16x16x32_bf16 v[126:129], v[134:137], v[188:191], v[126:129]
	v_mfma_f32_16x16x32_bf16 v[58:61], v[142:145], v[188:191], v[58:61]
	v_mfma_f32_16x16x32_bf16 v[122:125], v[134:137], v[216:219], v[122:125]
	v_mfma_f32_16x16x32_bf16 v[118:121], v[142:145], v[216:219], v[118:121]
	v_mfma_f32_16x16x32_bf16 v[114:117], v[134:137], v[228:231], v[114:117]
	v_mfma_f32_16x16x32_bf16 v[110:113], v[142:145], v[228:231], v[110:113]
	v_mfma_f32_16x16x32_bf16 v[106:109], v[134:137], v[232:235], v[106:109]
	v_mfma_f32_16x16x32_bf16 v[102:105], v[142:145], v[232:235], v[102:105]
	v_mfma_f32_16x16x32_bf16 v[66:69], v[164:167], v[180:183], v[66:69]
	v_mfma_f32_16x16x32_bf16 v[50:53], v[172:175], v[180:183], v[50:53]
	v_mfma_f32_16x16x32_bf16 v[54:57], v[164:167], v[184:187], v[54:57]
	v_mfma_f32_16x16x32_bf16 v[42:45], v[172:175], v[184:187], v[42:45]
	v_mfma_f32_16x16x32_bf16 v[46:49], v[164:167], v[220:223], v[46:49]
	v_mfma_f32_16x16x32_bf16 v[34:37], v[172:175], v[220:223], v[34:37]
	v_mfma_f32_16x16x32_bf16 v[98:101], v[164:167], v[224:227], v[98:101]
	v_mfma_f32_16x16x32_bf16 v[38:41], v[172:175], v[224:227], v[38:41]
	v_mfma_f32_16x16x32_bf16 v[66:69], v[168:171], v[188:191], v[66:69]
	v_mfma_f32_16x16x32_bf16 v[50:53], v[176:179], v[188:191], v[50:53]
	v_mfma_f32_16x16x32_bf16 v[54:57], v[168:171], v[216:219], v[54:57]
	v_mfma_f32_16x16x32_bf16 v[42:45], v[176:179], v[216:219], v[42:45]
	v_mfma_f32_16x16x32_bf16 v[46:49], v[168:171], v[228:231], v[46:49]
	v_mfma_f32_16x16x32_bf16 v[34:37], v[176:179], v[228:231], v[34:37]
	v_mfma_f32_16x16x32_bf16 v[98:101], v[168:171], v[232:235], v[98:101]
	v_mfma_f32_16x16x32_bf16 v[38:41], v[176:179], v[232:235], v[38:41]
	s_setprio 0
	s_barrier
; #define PG8_STAGE(bufoff, gbase, voff) do { _Pragma("unroll") for (int _i = 0; _i < 2; ++_i) \
;         __builtin_amdgcn_global_load_lds((const unsigned*)((const char*)(gbase) + (voff)[_i]), (LAS unsigned*)(lds + (bufoff) + ldsw + _i * 8192), 16, 0, 0); } while (0)
; #define PG8_LDA(dst, b, h) do { _Pragma("unroll") for (int m = 0; m < 4; ++m) _Pragma("unroll") for (int k = 0; k < 2; ++k) dst[m][k] = *(const LAS bf16x8*)(lds + PG8_SA(b, h) + ((aoff ^ (k * 64)) + m * 2048)); } while (0)
; #define PG8_MMA(ai, bj, At, Bt) do { __builtin_amdgcn_s_setprio(1); _Pragma("unroll") for (int m = 0; m < 4; ++m) _Pragma("unroll") for (int n = 0; n < 2; ++n) _Pragma("unroll") for (int k = 0; k < 2; ++k) \
;         acc[ai][bj][m][n] = __builtin_amdgcn_mfma_f32_16x16x32_bf16(Bt[n][k], At[m][k], acc[ai][bj][m][n], 0, 0, 0); __builtin_amdgcn_s_setprio(0); } while (0)
; #define PG8_WAIT_V(n) asm volatile("s_waitcnt vmcnt(" #n ")" ::: "memory")
; #define PG8_WAIT_L(n) asm volatile("s_waitcnt lgkmcnt(" #n ")" ::: "memory")
; #define PG8_BAR __builtin_amdgcn_s_barrier()
; #define PG8_SCHED __builtin_amdgcn_sched_barrier(0)
;     ...
;             PG8_LDA(At, 1, 1); PG8_STAGE(PG8_SB(1, 0), b3, voffB); PG8_STAGE(PG8_SB(1, 1), b3 + hstep, voffB); PG8_STAGE(PG8_SA(1, 0), a3, vs[0]);
;             PG8_WAIT_V(8); PG8_WAIT_L(0); PG8_BAR; if (do1) { PG8_MMA(1, 0, At, B0); PG8_MMA(1, 1, At, B1); } PG8_BAR; PG8_SCHED;
;         }
	s_add_i32 s38, s42, s49
	v_lshl_add_u64 v[238:239], s[4:5], 0, v[146:147]
	s_mov_b32 m0, s38
	ds_read_b128 v[180:183], v207 offset:49152
	ds_read_b128 v[184:187], v207 offset:51200
	ds_read_b128 v[188:191], v208 offset:49152
	ds_read_b128 v[216:219], v208 offset:51200
	ds_read_b128 v[220:223], v207 offset:53248
	ds_read_b128 v[224:227], v207 offset:55296
	ds_read_b128 v[228:231], v208 offset:53248
	ds_read_b128 v[232:235], v208 offset:55296
	global_load_lds_dwordx4 v[238:239], off
	s_add_i32 m0, s38, 0x2000
	s_add_u32 s2, s2, 0x44000
	v_lshl_add_u64 v[238:239], s[4:5], 0, v[148:149]
	s_addc_u32 s3, s3, 0
	s_add_i32 s4, s43, s49
	global_load_lds_dwordx4 v[238:239], off
	v_lshl_add_u64 v[238:239], s[2:3], 0, v[146:147]
	s_mov_b32 m0, s4
	v_lshl_add_u64 v[192:193], v[192:193], 0, s[92:93]
	global_load_lds_dwordx4 v[238:239], off
	v_lshl_add_u64 v[238:239], s[2:3], 0, v[148:149]
	s_add_i32 m0, s4, 0x2000
	s_nop 0
	global_load_lds_dwordx4 v[238:239], off
	s_mov_b32 m0, s55
	s_nop 0
	global_load_lds_dwordx4 v[192:193], off
	v_lshl_add_u64 v[192:193], v[236:237], 0, s[92:93]
	s_mov_b32 m0, s56
	s_nop 0
	global_load_lds_dwordx4 v[192:193], off
	s_waitcnt vmcnt(8)
	s_waitcnt lgkmcnt(0)
	s_barrier
	s_setprio 1
	v_mfma_f32_16x16x32_bf16 v[94:97], v[130:133], v[180:183], v[94:97]
	v_mfma_f32_16x16x32_bf16 v[26:29], v[138:141], v[180:183], v[26:29]
	v_mfma_f32_16x16x32_bf16 v[90:93], v[130:133], v[184:187], v[90:93]
	v_mfma_f32_16x16x32_bf16 v[86:89], v[138:141], v[184:187], v[86:89]
	v_mfma_f32_16x16x32_bf16 v[82:85], v[130:133], v[220:223], v[82:85]
	v_mfma_f32_16x16x32_bf16 v[78:81], v[138:141], v[220:223], v[78:81]
	v_mfma_f32_16x16x32_bf16 v[74:77], v[130:133], v[224:227], v[74:77]
	v_mfma_f32_16x16x32_bf16 v[70:73], v[138:141], v[224:227], v[70:73]
	v_mfma_f32_16x16x32_bf16 v[94:97], v[134:137], v[188:191], v[94:97]
	v_mfma_f32_16x16x32_bf16 v[26:29], v[142:145], v[188:191], v[26:29]
	v_mfma_f32_16x16x32_bf16 v[90:93], v[134:137], v[216:219], v[90:93]
	v_mfma_f32_16x16x32_bf16 v[86:89], v[142:145], v[216:219], v[86:89]
	v_mfma_f32_16x16x32_bf16 v[82:85], v[134:137], v[228:231], v[82:85]
	v_mfma_f32_16x16x32_bf16 v[78:81], v[142:145], v[228:231], v[78:81]
	v_mfma_f32_16x16x32_bf16 v[74:77], v[134:137], v[232:235], v[74:77]
	v_mfma_f32_16x16x32_bf16 v[70:73], v[142:145], v[232:235], v[70:73]
	v_mfma_f32_16x16x32_bf16 v[30:33], v[164:167], v[180:183], v[30:33]
	v_mfma_f32_16x16x32_bf16 v[18:21], v[172:175], v[180:183], v[18:21]
	v_mfma_f32_16x16x32_bf16 v[22:25], v[164:167], v[184:187], v[22:25]
	v_mfma_f32_16x16x32_bf16 v[10:13], v[172:175], v[184:187], v[10:13]
	v_mfma_f32_16x16x32_bf16 v[14:17], v[164:167], v[220:223], v[14:17]
	v_mfma_f32_16x16x32_bf16 v[2:5], v[172:175], v[220:223], v[2:5]
	v_mfma_f32_16x16x32_bf16 v[62:65], v[164:167], v[224:227], v[62:65]
	v_mfma_f32_16x16x32_bf16 v[6:9], v[172:175], v[224:227], v[6:9]
	v_mfma_f32_16x16x32_bf16 v[30:33], v[168:171], v[188:191], v[30:33]
	v_mfma_f32_16x16x32_bf16 v[18:21], v[176:179], v[188:191], v[18:21]
	v_mfma_f32_16x16x32_bf16 v[22:25], v[168:171], v[216:219], v[22:25]
	v_mfma_f32_16x16x32_bf16 v[10:13], v[176:179], v[216:219], v[10:13]
	v_mfma_f32_16x16x32_bf16 v[14:17], v[168:171], v[228:231], v[14:17]
	v_mfma_f32_16x16x32_bf16 v[2:5], v[176:179], v[228:231], v[2:5]
	v_mfma_f32_16x16x32_bf16 v[62:65], v[168:171], v[232:235], v[62:65]
	v_mfma_f32_16x16x32_bf16 v[6:9], v[176:179], v[232:235], v[6:9]
	s_setprio 0
	s_barrier
	s_add_i32 s41, s41, 2
	s_add_u32 s37, s37, 0x8000
	s_addc_u32 s40, s40, 0
	s_add_u32 s0, s0, 0x100
	s_addc_u32 s1, s1, 0
	s_cmp_gt_u32 s41, 13
	s_cbranch_scc0 .LBB0_557
	s_and_b64 vcc, exec, s[80:81]
	s_cbranch_vccz .LBB0_560
	s_barrier

; #define PG8_STAGE(bufoff, gbase, voff) do { _Pragma("unroll") for (int _i = 0; _i < 2; ++_i) \
;         __builtin_amdgcn_global_load_lds((const unsigned*)((const char*)(gbase) + (voff)[_i]), (LAS unsigned*)(lds + (bufoff) + ldsw + _i * 8192), 16, 0, 0); } while (0)
; #define PG8_LDA(dst, b, h) do { _Pragma("unroll") for (int m = 0; m < 4; ++m) _Pragma("unroll") for (int k = 0; k < 2; ++k) dst[m][k] = *(const LAS bf16x8*)(lds + PG8_SA(b, h) + ((aoff ^ (k * 64)) + m * 2048)); } while (0)
; #define PG8_LDB(dst, b, h) do { _Pragma("unroll") for (int n = 0; n < 2; ++n) _Pragma("unroll") for (int k = 0; k < 2; ++k) dst[n][k] = *(const LAS bf16x8*)(lds + PG8_SB(b, h) + ((boff ^ (k * 64)) + n * 2048)); } while (0)
; #define PG8_MMA(ai, bj, At, Bt) do { __builtin_amdgcn_s_setprio(1); _Pragma("unroll") for (int m = 0; m < 4; ++m) _Pragma("unroll") for (int n = 0; n < 2; ++n) _Pragma("unroll") for (int k = 0; k < 2; ++k) \
;         acc[ai][bj][m][n] = __builtin_amdgcn_mfma_f32_16x16x32_bf16(Bt[n][k], At[m][k], acc[ai][bj][m][n], 0, 0, 0); __builtin_amdgcn_s_setprio(0); } while (0)
; #define PG8_WAIT_V(n) asm volatile("s_waitcnt vmcnt(" #n ")" ::: "memory")
; #define PG8_WAIT_L(n) asm volatile("s_waitcnt lgkmcnt(" #n ")" ::: "memory")
; #define PG8_BAR __builtin_amdgcn_s_barrier()
; #define PG8_SCHED __builtin_amdgcn_sched_barrier(0)
;     ...
;             PG8_LDB(B0, 0, 0); PG8_LDB(B1, 0, 1); PG8_SCHED; PG8_LDA(At, 0, 0); PG8_STAGE(PG8_SA(1, 1), a1, voffA[1]);
;             PG8_WAIT_V(8); PG8_WAIT_L(0); PG8_BAR; if (do0) { PG8_MMA(0, 0, At, B0); PG8_MMA(0, 1, At, B1); } PG8_BAR; PG8_SCHED;
;             PG8_LDA(At, 0, 1); PG8_STAGE(PG8_SB(0, 0), b2, voffB); PG8_STAGE(PG8_SB(0, 1), b2 + hstep, voffB); PG8_STAGE(PG8_SA(0, 0), a2, vs[0]);
;             PG8_WAIT_V(8); PG8_WAIT_L(0); PG8_BAR; if (do1) { PG8_MMA(1, 0, At, B0); PG8_MMA(1, 1, At, B1); } PG8_BAR; PG8_SCHED;
;             PG8_LDB(B0, 1, 0); PG8_LDB(B1, 1, 1); PG8_SCHED; PG8_LDA(At, 1, 0); PG8_STAGE(PG8_SA(0, 1), a2, vs[1]);
;             PG8_WAIT_V(8); PG8_WAIT_L(0); PG8_BAR; if (do0) { PG8_MMA(0, 0, At, B0); PG8_MMA(0, 1, At, B1); } PG8_BAR; PG8_SCHED;
.LBB0_1008:
	v_add_u32_e32 v2, s54, v226
	v_add_u32_e32 v134, s54, v227
	ds_read_b128 v[150:153], v2
	ds_read_b128 v[154:157], v134
	v_add_u32_e32 v2, s55, v226
	v_add_u32_e32 v134, s55, v227
	ds_read_b128 v[158:161], v2
	ds_read_b128 v[162:165], v134
	v_add_u32_e32 v2, s56, v226
	v_add_u32_e32 v138, s56, v227
	ds_read_b128 v[134:137], v2
	ds_read_b128 v[138:141], v138
	v_add_u32_e32 v2, s57, v226
	v_add_u32_e32 v146, s57, v227
	ds_read_b128 v[142:145], v2
	ds_read_b128 v[146:149], v146
	v_lshl_add_u64 v[224:225], v[222:223], 0, s[28:29]
	s_add_i32 m0, s23, 0xc000
	s_waitcnt lgkmcnt(0)
	ds_read_b128 v[190:193], v228
	ds_read_b128 v[178:181], v228 offset:2048
	ds_read_b128 v[194:197], v229
	ds_read_b128 v[182:185], v229 offset:2048
	ds_read_b128 v[174:177], v228 offset:4096
	ds_read_b128 v[166:169], v228 offset:6144
	ds_read_b128 v[186:189], v229 offset:4096
	ds_read_b128 v[170:173], v229 offset:6144
	global_load_lds_dwordx4 v[224:225], off
	v_lshl_add_u64 v[224:225], v[220:221], 0, s[28:29]
	s_add_i32 m0, s23, 0xe000
	v_cndmask_b32_e64 v2, 0, 1, s[26:27]
	global_load_lds_dwordx4 v[224:225], off
	s_waitcnt vmcnt(8)
	s_waitcnt lgkmcnt(0)
	v_cmp_ne_u32_e64 s[8:9], 1, v2
	s_andn2_b64 vcc, exec, s[26:27]
	s_barrier
	s_cbranch_vccnz .LBB0_1010
	s_setprio 1
	v_mfma_f32_16x16x32_bf16 v[130:133], v[150:153], v[190:193], v[130:133]
	v_mfma_f32_16x16x32_bf16 v[126:129], v[158:161], v[190:193], v[126:129]
	v_mfma_f32_16x16x32_bf16 v[114:117], v[150:153], v[178:181], v[114:117]
	v_mfma_f32_16x16x32_bf16 v[110:113], v[158:161], v[178:181], v[110:113]
	v_mfma_f32_16x16x32_bf16 v[98:101], v[150:153], v[174:177], v[98:101]
	v_mfma_f32_16x16x32_bf16 v[94:97], v[158:161], v[174:177], v[94:97]
	v_mfma_f32_16x16x32_bf16 v[82:85], v[150:153], v[166:169], v[82:85]
	v_mfma_f32_16x16x32_bf16 v[78:81], v[158:161], v[166:169], v[78:81]
	v_mfma_f32_16x16x32_bf16 v[130:133], v[154:157], v[194:197], v[130:133]
	v_mfma_f32_16x16x32_bf16 v[126:129], v[162:165], v[194:197], v[126:129]
	v_mfma_f32_16x16x32_bf16 v[114:117], v[154:157], v[182:185], v[114:117]
	v_mfma_f32_16x16x32_bf16 v[110:113], v[162:165], v[182:185], v[110:113]
	v_mfma_f32_16x16x32_bf16 v[98:101], v[154:157], v[186:189], v[98:101]
	v_mfma_f32_16x16x32_bf16 v[94:97], v[162:165], v[186:189], v[94:97]
	v_mfma_f32_16x16x32_bf16 v[82:85], v[154:157], v[170:173], v[82:85]
	v_mfma_f32_16x16x32_bf16 v[78:81], v[162:165], v[170:173], v[78:81]
	v_mfma_f32_16x16x32_bf16 v[122:125], v[134:137], v[190:193], v[122:125]
	v_mfma_f32_16x16x32_bf16 v[118:121], v[142:145], v[190:193], v[118:121]
	v_mfma_f32_16x16x32_bf16 v[106:109], v[134:137], v[178:181], v[106:109]
	v_mfma_f32_16x16x32_bf16 v[102:105], v[142:145], v[178:181], v[102:105]
	v_mfma_f32_16x16x32_bf16 v[90:93], v[134:137], v[174:177], v[90:93]
	v_mfma_f32_16x16x32_bf16 v[86:89], v[142:145], v[174:177], v[86:89]
	v_mfma_f32_16x16x32_bf16 v[74:77], v[134:137], v[166:169], v[74:77]
	v_mfma_f32_16x16x32_bf16 v[70:73], v[142:145], v[166:169], v[70:73]
	v_mfma_f32_16x16x32_bf16 v[122:125], v[138:141], v[194:197], v[122:125]
	v_mfma_f32_16x16x32_bf16 v[118:121], v[146:149], v[194:197], v[118:121]
	v_mfma_f32_16x16x32_bf16 v[106:109], v[138:141], v[182:185], v[106:109]
	v_mfma_f32_16x16x32_bf16 v[102:105], v[146:149], v[182:185], v[102:105]
	v_mfma_f32_16x16x32_bf16 v[90:93], v[138:141], v[186:189], v[90:93]
	v_mfma_f32_16x16x32_bf16 v[86:89], v[146:149], v[186:189], v[86:89]
	v_mfma_f32_16x16x32_bf16 v[74:77], v[138:141], v[170:173], v[74:77]
	v_mfma_f32_16x16x32_bf16 v[70:73], v[146:149], v[170:173], v[70:73]
	s_setprio 0
.LBB0_1010:
	s_add_u32 s10, s90, s28
	s_addc_u32 s11, s91, s29
	s_add_u32 s30, s10, 0x4213700
	s_addc_u32 s31, s11, 0
	s_and_b64 s[10:11], s[6:7], exec
	v_cndmask_b32_e64 v2, v218, v4, s[6:7]
	v_cndmask_b32_e64 v224, v219, v5, s[6:7]
	s_cselect_b32 s35, s83, s31
	s_cselect_b32 s34, s82, s30
	s_cselect_b32 s31, s21, s64
	s_cselect_b32 s30, s20, s19
	s_barrier
	s_mov_b32 m0, s37
	v_lshl_add_u64 v[232:233], s[30:31], 0, v[202:203]
	s_add_u32 s10, s30, 0x40000
	s_waitcnt lgkmcnt(0)
	ds_read_b128 v[190:193], v228 offset:16384
	ds_read_b128 v[178:181], v228 offset:18432
	ds_read_b128 v[194:197], v229 offset:16384
	ds_read_b128 v[182:185], v229 offset:18432
	ds_read_b128 v[174:177], v228 offset:20480
	ds_read_b128 v[166:169], v228 offset:22528
	ds_read_b128 v[186:189], v229 offset:20480
	ds_read_b128 v[170:173], v229 offset:22528
	global_load_lds_dwordx4 v[232:233], off
	v_lshl_add_u64 v[232:233], s[30:31], 0, v[204:205]
	s_mov_b32 m0, s38
	s_addc_u32 s11, s31, 0
	global_load_lds_dwordx4 v[232:233], off
	v_lshl_add_u64 v[232:233], s[10:11], 0, v[202:203]
	s_mov_b32 m0, s39
	v_cndmask_b32_e64 v213, 0, 1, s[24:25]
	global_load_lds_dwordx4 v[232:233], off
	v_lshl_add_u64 v[232:233], s[10:11], 0, v[204:205]
	s_mov_b32 m0, s40
	v_cmp_ne_u32_e64 s[10:11], 1, v213
	global_load_lds_dwordx4 v[232:233], off
	s_mov_b32 m0, s23
	s_andn2_b64 vcc, exec, s[24:25]
	global_load_lds_dwordx4 v2, s[34:35]
	s_mov_b32 m0, s41
	s_nop 0
	global_load_lds_dwordx4 v224, s[34:35]
	s_waitcnt vmcnt(8)
	s_waitcnt lgkmcnt(0)
	s_barrier
	s_cbranch_vccnz .LBB0_1012
; #define PG8_STAGE(bufoff, gbase, voff) do { _Pragma("unroll") for (int _i = 0; _i < 2; ++_i) \
;         __builtin_amdgcn_global_load_lds((const unsigned*)((const char*)(gbase) + (voff)[_i]), (LAS unsigned*)(lds + (bufoff) + ldsw + _i * 8192), 16, 0, 0); } while (0)
; #define PG8_LDA(dst, b, h) do { _Pragma("unroll") for (int m = 0; m < 4; ++m) _Pragma("unroll") for (int k = 0; k < 2; ++k) dst[m][k] = *(const LAS bf16x8*)(lds + PG8_SA(b, h) + ((aoff ^ (k * 64)) + m * 2048)); } while (0)
; #define PG8_LDB(dst, b, h) do { _Pragma("unroll") for (int n = 0; n < 2; ++n) _Pragma("unroll") for (int k = 0; k < 2; ++k) dst[n][k] = *(const LAS bf16x8*)(lds + PG8_SB(b, h) + ((boff ^ (k * 64)) + n * 2048)); } while (0)
; #define PG8_MMA(ai, bj, At, Bt) do { __builtin_amdgcn_s_setprio(1); _Pragma("unroll") for (int m = 0; m < 4; ++m) _Pragma("unroll") for (int n = 0; n < 2; ++n) _Pragma("unroll") for (int k = 0; k < 2; ++k) \
;         acc[ai][bj][m][n] = __builtin_amdgcn_mfma_f32_16x16x32_bf16(Bt[n][k], At[m][k], acc[ai][bj][m][n], 0, 0, 0); __builtin_amdgcn_s_setprio(0); } while (0)
; #define PG8_WAIT_V(n) asm volatile("s_waitcnt vmcnt(" #n ")" ::: "memory")
; #define PG8_WAIT_L(n) asm volatile("s_waitcnt lgkmcnt(" #n ")" ::: "memory")
; #define PG8_BAR __builtin_amdgcn_s_barrier()
; #define PG8_SCHED __builtin_amdgcn_sched_barrier(0)
;     ...
;             PG8_LDB(B0, 1, 0); PG8_LDB(B1, 1, 1); PG8_SCHED; PG8_LDA(At, 1, 0); PG8_STAGE(PG8_SA(0, 1), a2, vs[1]);
;             PG8_WAIT_V(8); PG8_WAIT_L(0); PG8_BAR; if (do0) { PG8_MMA(0, 0, At, B0); PG8_MMA(0, 1, At, B1); } PG8_BAR; PG8_SCHED;
;             PG8_LDA(At, 1, 1); PG8_STAGE(PG8_SB(1, 0), b3, voffB); PG8_STAGE(PG8_SB(1, 1), b3 + hstep, voffB); PG8_STAGE(PG8_SA(1, 0), a3, vs[0]);
;             PG8_WAIT_V(8); PG8_WAIT_L(0); PG8_BAR; if (do1) { PG8_MMA(1, 0, At, B0); PG8_MMA(1, 1, At, B1); } PG8_BAR; PG8_SCHED;
	s_setprio 1
	v_mfma_f32_16x16x32_bf16 v[66:69], v[150:153], v[190:193], v[66:69]
	v_mfma_f32_16x16x32_bf16 v[62:65], v[158:161], v[190:193], v[62:65]
	v_mfma_f32_16x16x32_bf16 v[50:53], v[150:153], v[178:181], v[50:53]
	v_mfma_f32_16x16x32_bf16 v[46:49], v[158:161], v[178:181], v[46:49]
	v_mfma_f32_16x16x32_bf16 v[34:37], v[150:153], v[174:177], v[34:37]
	v_mfma_f32_16x16x32_bf16 v[30:33], v[158:161], v[174:177], v[30:33]
	v_mfma_f32_16x16x32_bf16 v[18:21], v[150:153], v[166:169], v[18:21]
	v_mfma_f32_16x16x32_bf16 v[14:17], v[158:161], v[166:169], v[14:17]
	v_mfma_f32_16x16x32_bf16 v[66:69], v[154:157], v[194:197], v[66:69]
	v_mfma_f32_16x16x32_bf16 v[62:65], v[162:165], v[194:197], v[62:65]
	v_mfma_f32_16x16x32_bf16 v[50:53], v[154:157], v[182:185], v[50:53]
	v_mfma_f32_16x16x32_bf16 v[46:49], v[162:165], v[182:185], v[46:49]
	v_mfma_f32_16x16x32_bf16 v[34:37], v[154:157], v[186:189], v[34:37]
	v_mfma_f32_16x16x32_bf16 v[30:33], v[162:165], v[186:189], v[30:33]
	v_mfma_f32_16x16x32_bf16 v[18:21], v[154:157], v[170:173], v[18:21]
	v_mfma_f32_16x16x32_bf16 v[14:17], v[162:165], v[170:173], v[14:17]
	v_mfma_f32_16x16x32_bf16 v[58:61], v[134:137], v[190:193], v[58:61]
	v_mfma_f32_16x16x32_bf16 v[54:57], v[142:145], v[190:193], v[54:57]
	v_mfma_f32_16x16x32_bf16 v[42:45], v[134:137], v[178:181], v[42:45]
	v_mfma_f32_16x16x32_bf16 v[38:41], v[142:145], v[178:181], v[38:41]
	v_mfma_f32_16x16x32_bf16 v[26:29], v[134:137], v[174:177], v[26:29]
	v_mfma_f32_16x16x32_bf16 v[22:25], v[142:145], v[174:177], v[22:25]
	v_mfma_f32_16x16x32_bf16 v[10:13], v[134:137], v[166:169], v[10:13]
	v_mfma_f32_16x16x32_bf16 v[6:9], v[142:145], v[166:169], v[6:9]
	v_mfma_f32_16x16x32_bf16 v[58:61], v[138:141], v[194:197], v[58:61]
	v_mfma_f32_16x16x32_bf16 v[54:57], v[146:149], v[194:197], v[54:57]
	v_mfma_f32_16x16x32_bf16 v[42:45], v[138:141], v[182:185], v[42:45]
	v_mfma_f32_16x16x32_bf16 v[38:41], v[146:149], v[182:185], v[38:41]
	v_mfma_f32_16x16x32_bf16 v[26:29], v[138:141], v[186:189], v[26:29]
	v_mfma_f32_16x16x32_bf16 v[22:25], v[146:149], v[186:189], v[22:25]
	v_mfma_f32_16x16x32_bf16 v[10:13], v[138:141], v[170:173], v[10:13]
	v_mfma_f32_16x16x32_bf16 v[6:9], v[146:149], v[170:173], v[6:9]
	s_setprio 0
.LBB0_1012:
	v_cndmask_b32_e64 v213, v214, v215, s[6:7]
	v_cndmask_b32_e64 v225, v216, v217, s[6:7]
	s_barrier
	s_add_i32 s6, 0, 0x18000
	v_add_u32_e32 v134, s6, v226
	v_add_u32_e32 v135, s6, v227
	ds_read_b128 v[150:153], v134
	ds_read_b128 v[154:157], v135
	v_add_u32_e32 v134, s58, v226
	s_add_i32 s6, 0, 0x1c000
	v_add_u32_e32 v135, s58, v227
	ds_read_b128 v[158:161], v134
	ds_read_b128 v[162:165], v135
	v_add_u32_e32 v134, s6, v226
	v_add_u32_e32 v138, s6, v227
	v_add_u32_e32 v142, s59, v226
	v_add_u32_e32 v146, s59, v227
	ds_read_b128 v[134:137], v134
	ds_read_b128 v[138:141], v138
	ds_read_b128 v[142:145], v142
	ds_read_b128 v[146:149], v146
	s_mov_b32 m0, s42
	s_waitcnt lgkmcnt(0)
	ds_read_b128 v[190:193], v228 offset:32768
	ds_read_b128 v[178:181], v228 offset:34816
	ds_read_b128 v[194:197], v229 offset:32768
	ds_read_b128 v[182:185], v229 offset:34816
	ds_read_b128 v[174:177], v228 offset:36864
	ds_read_b128 v[166:169], v228 offset:38912
	ds_read_b128 v[186:189], v229 offset:36864
	ds_read_b128 v[170:173], v229 offset:38912
	global_load_lds_dwordx4 v213, s[34:35]
	s_mov_b32 m0, s43
	s_and_b64 vcc, exec, s[8:9]
	global_load_lds_dwordx4 v225, s[34:35]
	s_waitcnt vmcnt(8)
	s_waitcnt lgkmcnt(0)
	s_barrier
	s_cbranch_vccnz .LBB0_1014
	s_setprio 1
	v_mfma_f32_16x16x32_bf16 v[130:133], v[150:153], v[190:193], v[130:133]
	v_mfma_f32_16x16x32_bf16 v[126:129], v[158:161], v[190:193], v[126:129]
	v_mfma_f32_16x16x32_bf16 v[114:117], v[150:153], v[178:181], v[114:117]
	v_mfma_f32_16x16x32_bf16 v[110:113], v[158:161], v[178:181], v[110:113]
	v_mfma_f32_16x16x32_bf16 v[98:101], v[150:153], v[174:177], v[98:101]
	v_mfma_f32_16x16x32_bf16 v[94:97], v[158:161], v[174:177], v[94:97]
	v_mfma_f32_16x16x32_bf16 v[82:85], v[150:153], v[166:169], v[82:85]
	v_mfma_f32_16x16x32_bf16 v[78:81], v[158:161], v[166:169], v[78:81]
	v_mfma_f32_16x16x32_bf16 v[130:133], v[154:157], v[194:197], v[130:133]
	v_mfma_f32_16x16x32_bf16 v[126:129], v[162:165], v[194:197], v[126:129]
	v_mfma_f32_16x16x32_bf16 v[114:117], v[154:157], v[182:185], v[114:117]
	v_mfma_f32_16x16x32_bf16 v[110:113], v[162:165], v[182:185], v[110:113]
	v_mfma_f32_16x16x32_bf16 v[98:101], v[154:157], v[186:189], v[98:101]
	v_mfma_f32_16x16x32_bf16 v[94:97], v[162:165], v[186:189], v[94:97]
	v_mfma_f32_16x16x32_bf16 v[82:85], v[154:157], v[170:173], v[82:85]
	v_mfma_f32_16x16x32_bf16 v[78:81], v[162:165], v[170:173], v[78:81]
	v_mfma_f32_16x16x32_bf16 v[122:125], v[134:137], v[190:193], v[122:125]
	v_mfma_f32_16x16x32_bf16 v[118:121], v[142:145], v[190:193], v[118:121]
	v_mfma_f32_16x16x32_bf16 v[106:109], v[134:137], v[178:181], v[106:109]
	v_mfma_f32_16x16x32_bf16 v[102:105], v[142:145], v[178:181], v[102:105]
	v_mfma_f32_16x16x32_bf16 v[90:93], v[134:137], v[174:177], v[90:93]
	v_mfma_f32_16x16x32_bf16 v[86:89], v[142:145], v[174:177], v[86:89]
	v_mfma_f32_16x16x32_bf16 v[74:77], v[134:137], v[166:169], v[74:77]
	v_mfma_f32_16x16x32_bf16 v[70:73], v[142:145], v[166:169], v[70:73]
	v_mfma_f32_16x16x32_bf16 v[122:125], v[138:141], v[194:197], v[122:125]
	v_mfma_f32_16x16x32_bf16 v[118:121], v[146:149], v[194:197], v[118:121]
	v_mfma_f32_16x16x32_bf16 v[106:109], v[138:141], v[182:185], v[106:109]
	v_mfma_f32_16x16x32_bf16 v[102:105], v[146:149], v[182:185], v[102:105]
	v_mfma_f32_16x16x32_bf16 v[90:93], v[138:141], v[186:189], v[90:93]
	v_mfma_f32_16x16x32_bf16 v[86:89], v[146:149], v[186:189], v[86:89]
	v_mfma_f32_16x16x32_bf16 v[74:77], v[138:141], v[170:173], v[74:77]
	v_mfma_f32_16x16x32_bf16 v[70:73], v[146:149], v[170:173], v[70:73]
	s_setprio 0
; #define PG8_STAGE(bufoff, gbase, voff) do { _Pragma("unroll") for (int _i = 0; _i < 2; ++_i) \
;         __builtin_amdgcn_global_load_lds((const unsigned*)((const char*)(gbase) + (voff)[_i]), (LAS unsigned*)(lds + (bufoff) + ldsw + _i * 8192), 16, 0, 0); } while (0)
; #define PG8_LDA(dst, b, h) do { _Pragma("unroll") for (int m = 0; m < 4; ++m) _Pragma("unroll") for (int k = 0; k < 2; ++k) dst[m][k] = *(const LAS bf16x8*)(lds + PG8_SA(b, h) + ((aoff ^ (k * 64)) + m * 2048)); } while (0)
; #define PG8_MMA(ai, bj, At, Bt) do { __builtin_amdgcn_s_setprio(1); _Pragma("unroll") for (int m = 0; m < 4; ++m) _Pragma("unroll") for (int n = 0; n < 2; ++n) _Pragma("unroll") for (int k = 0; k < 2; ++k) \
;         acc[ai][bj][m][n] = __builtin_amdgcn_mfma_f32_16x16x32_bf16(Bt[n][k], At[m][k], acc[ai][bj][m][n], 0, 0, 0); __builtin_amdgcn_s_setprio(0); } while (0)
; #define PG8_WAIT_V(n) asm volatile("s_waitcnt vmcnt(" #n ")" ::: "memory")
; #define PG8_WAIT_L(n) asm volatile("s_waitcnt lgkmcnt(" #n ")" ::: "memory")
; #define PG8_BAR __builtin_amdgcn_s_barrier()
; #define PG8_SCHED __builtin_amdgcn_sched_barrier(0)
;     ...
;             PG8_LDA(At, 1, 1); PG8_STAGE(PG8_SB(1, 0), b3, voffB); PG8_STAGE(PG8_SB(1, 1), b3 + hstep, voffB); PG8_STAGE(PG8_SA(1, 0), a3, vs[0]);
;             PG8_WAIT_V(8); PG8_WAIT_L(0); PG8_BAR; if (do1) { PG8_MMA(1, 0, At, B0); PG8_MMA(1, 1, At, B1); } PG8_BAR; PG8_SCHED;
;         }
.LBB0_1014:
	v_mov_b32_e32 v225, v3
	s_add_u32 s6, s30, 0x4000
	v_lshl_add_u64 v[232:233], s[34:35], 0, v[2:3]
	v_lshl_add_u64 v[224:225], s[34:35], 0, v[224:225]
	s_addc_u32 s7, s31, 0
	s_barrier
	s_mov_b32 m0, s47
	v_lshl_add_u64 v[234:235], s[6:7], 0, v[202:203]
	s_waitcnt lgkmcnt(0)
	ds_read_b128 v[190:193], v228 offset:49152
	ds_read_b128 v[178:181], v228 offset:51200
	ds_read_b128 v[194:197], v229 offset:49152
	ds_read_b128 v[182:185], v229 offset:51200
	ds_read_b128 v[174:177], v228 offset:53248
	ds_read_b128 v[166:169], v228 offset:55296
	ds_read_b128 v[186:189], v229 offset:53248
	ds_read_b128 v[170:173], v229 offset:55296
	global_load_lds_dwordx4 v[234:235], off
	v_lshl_add_u64 v[234:235], s[6:7], 0, v[204:205]
	s_add_u32 s6, s30, 0x44000
	s_mov_b32 m0, s48
	s_addc_u32 s7, s31, 0
	global_load_lds_dwordx4 v[234:235], off
	v_lshl_add_u64 v[234:235], s[6:7], 0, v[202:203]
	s_mov_b32 m0, s51
	v_lshl_add_u64 v[232:233], v[232:233], 0, s[16:17]
	global_load_lds_dwordx4 v[234:235], off
	v_lshl_add_u64 v[234:235], s[6:7], 0, v[204:205]
	s_mov_b32 m0, s52
	v_lshl_add_u64 v[224:225], v[224:225], 0, s[16:17]
	global_load_lds_dwordx4 v[234:235], off
	s_mov_b32 m0, s49
	s_and_b64 vcc, exec, s[10:11]
	global_load_lds_dwordx4 v[232:233], off
	s_mov_b32 m0, s50
	s_nop 0
	global_load_lds_dwordx4 v[224:225], off
	s_waitcnt vmcnt(8)
	s_waitcnt lgkmcnt(0)
	s_barrier
	s_cbranch_vccnz .LBB0_1005
	s_setprio 1
	v_mfma_f32_16x16x32_bf16 v[66:69], v[150:153], v[190:193], v[66:69]
	v_mfma_f32_16x16x32_bf16 v[62:65], v[158:161], v[190:193], v[62:65]
	v_mfma_f32_16x16x32_bf16 v[50:53], v[150:153], v[178:181], v[50:53]
	v_mfma_f32_16x16x32_bf16 v[46:49], v[158:161], v[178:181], v[46:49]
	v_mfma_f32_16x16x32_bf16 v[34:37], v[150:153], v[174:177], v[34:37]
	v_mfma_f32_16x16x32_bf16 v[30:33], v[158:161], v[174:177], v[30:33]
	v_mfma_f32_16x16x32_bf16 v[18:21], v[150:153], v[166:169], v[18:21]
	v_mfma_f32_16x16x32_bf16 v[14:17], v[158:161], v[166:169], v[14:17]
	v_mfma_f32_16x16x32_bf16 v[66:69], v[154:157], v[194:197], v[66:69]
	v_mfma_f32_16x16x32_bf16 v[62:65], v[162:165], v[194:197], v[62:65]
	v_mfma_f32_16x16x32_bf16 v[50:53], v[154:157], v[182:185], v[50:53]
	v_mfma_f32_16x16x32_bf16 v[46:49], v[162:165], v[182:185], v[46:49]
	v_mfma_f32_16x16x32_bf16 v[34:37], v[154:157], v[186:189], v[34:37]
	v_mfma_f32_16x16x32_bf16 v[30:33], v[162:165], v[186:189], v[30:33]
	v_mfma_f32_16x16x32_bf16 v[18:21], v[154:157], v[170:173], v[18:21]
	v_mfma_f32_16x16x32_bf16 v[14:17], v[162:165], v[170:173], v[14:17]
	v_mfma_f32_16x16x32_bf16 v[58:61], v[134:137], v[190:193], v[58:61]
	v_mfma_f32_16x16x32_bf16 v[54:57], v[142:145], v[190:193], v[54:57]
	v_mfma_f32_16x16x32_bf16 v[42:45], v[134:137], v[178:181], v[42:45]
	v_mfma_f32_16x16x32_bf16 v[38:41], v[142:145], v[178:181], v[38:41]
	v_mfma_f32_16x16x32_bf16 v[26:29], v[134:137], v[174:177], v[26:29]
	v_mfma_f32_16x16x32_bf16 v[22:25], v[142:145], v[174:177], v[22:25]
	v_mfma_f32_16x16x32_bf16 v[10:13], v[134:137], v[166:169], v[10:13]
	v_mfma_f32_16x16x32_bf16 v[6:9], v[142:145], v[166:169], v[6:9]
	v_mfma_f32_16x16x32_bf16 v[58:61], v[138:141], v[194:197], v[58:61]
	v_mfma_f32_16x16x32_bf16 v[54:57], v[146:149], v[194:197], v[54:57]
	v_mfma_f32_16x16x32_bf16 v[42:45], v[138:141], v[182:185], v[42:45]
	v_mfma_f32_16x16x32_bf16 v[38:41], v[146:149], v[182:185], v[38:41]
	v_mfma_f32_16x16x32_bf16 v[26:29], v[138:141], v[186:189], v[26:29]
	v_mfma_f32_16x16x32_bf16 v[22:25], v[146:149], v[186:189], v[22:25]
	v_mfma_f32_16x16x32_bf16 v[10:13], v[138:141], v[170:173], v[10:13]
	v_mfma_f32_16x16x32_bf16 v[6:9], v[146:149], v[170:173], v[6:9]
	s_setprio 0
	s_branch .LBB0_1005

; #define PG8_STAGE(bufoff, gbase, voff) do { _Pragma("unroll") for (int _i = 0; _i < 2; ++_i) \
;         __builtin_amdgcn_global_load_lds((const unsigned*)((const char*)(gbase) + (voff)[_i]), (LAS unsigned*)(lds + (bufoff) + ldsw + _i * 8192), 16, 0, 0); } while (0)
; #define PG8_LDA(dst, b, h) do { _Pragma("unroll") for (int m = 0; m < 4; ++m) _Pragma("unroll") for (int k = 0; k < 2; ++k) dst[m][k] = *(const LAS bf16x8*)(lds + PG8_SA(b, h) + ((aoff ^ (k * 64)) + m * 2048)); } while (0)
; #define PG8_LDB(dst, b, h) do { _Pragma("unroll") for (int n = 0; n < 2; ++n) _Pragma("unroll") for (int k = 0; k < 2; ++k) dst[n][k] = *(const LAS bf16x8*)(lds + PG8_SB(b, h) + ((boff ^ (k * 64)) + n * 2048)); } while (0)
; #define PG8_MMA(ai, bj, At, Bt) do { __builtin_amdgcn_s_setprio(1); _Pragma("unroll") for (int m = 0; m < 4; ++m) _Pragma("unroll") for (int n = 0; n < 2; ++n) _Pragma("unroll") for (int k = 0; k < 2; ++k) \
;         acc[ai][bj][m][n] = __builtin_amdgcn_mfma_f32_16x16x32_bf16(Bt[n][k], At[m][k], acc[ai][bj][m][n], 0, 0, 0); __builtin_amdgcn_s_setprio(0); } while (0)
; #define PG8_WAIT_V(n) asm volatile("s_waitcnt vmcnt(" #n ")" ::: "memory")
; #define PG8_WAIT_L(n) asm volatile("s_waitcnt lgkmcnt(" #n ")" ::: "memory")
; #define PG8_BAR __builtin_amdgcn_s_barrier()
; #define PG8_SCHED __builtin_amdgcn_sched_barrier(0)
;     ...
;             PG8_LDB(B0, 0, 0); PG8_LDB(B1, 0, 1); PG8_SCHED; PG8_LDA(At, 0, 0); PG8_STAGE(PG8_SA(1, 1), a1, voffA[1]);
;             PG8_WAIT_V(8); PG8_WAIT_L(0); PG8_BAR; if (do0) { PG8_MMA(0, 0, At, B0); PG8_MMA(0, 1, At, B1); } PG8_BAR; PG8_SCHED;
;             PG8_LDA(At, 0, 1); PG8_STAGE(PG8_SB(0, 0), b2, voffB); PG8_STAGE(PG8_SB(0, 1), b2 + hstep, voffB); PG8_STAGE(PG8_SA(0, 0), a2, vs[0]);
;             PG8_WAIT_V(8); PG8_WAIT_L(0); PG8_BAR; if (do1) { PG8_MMA(1, 0, At, B0); PG8_MMA(1, 1, At, B1); } PG8_BAR; PG8_SCHED;
;             PG8_LDB(B0, 1, 0); PG8_LDB(B1, 1, 1); PG8_SCHED; PG8_LDA(At, 1, 0); PG8_STAGE(PG8_SA(0, 1), a2, vs[1]);
;             PG8_WAIT_V(8); PG8_WAIT_L(0); PG8_BAR; if (do0) { PG8_MMA(0, 0, At, B0); PG8_MMA(0, 1, At, B1); } PG8_BAR; PG8_SCHED;
.LBB0_1100:
	ds_read_b128 v[150:153], v218
	ds_read_b128 v[154:157], v219
	ds_read_b128 v[158:161], v220
	ds_read_b128 v[162:165], v221
	ds_read_b128 v[134:137], v222
	ds_read_b128 v[138:141], v223
	ds_read_b128 v[142:145], v224
	ds_read_b128 v[146:149], v225
	v_lshl_add_u64 v[4:5], s[22:23], 0, v[212:213]
	s_add_i32 m0, s28, 0xc000
	s_waitcnt lgkmcnt(0)
	ds_read_b128 v[190:193], v226
	ds_read_b128 v[178:181], v226 offset:2048
	ds_read_b128 v[194:197], v227
	ds_read_b128 v[182:185], v227 offset:2048
	ds_read_b128 v[174:177], v226 offset:4096
	ds_read_b128 v[166:169], v226 offset:6144
	ds_read_b128 v[186:189], v227 offset:4096
	ds_read_b128 v[170:173], v227 offset:6144
	global_load_lds_dwordx4 v[4:5], off
	v_lshl_add_u64 v[4:5], s[22:23], 0, v[214:215]
	s_add_i32 m0, s28, 0xe000
	v_cmp_ne_u32_e64 s[6:7], 1, v228
	global_load_lds_dwordx4 v[4:5], off
	s_waitcnt vmcnt(8)
	s_waitcnt lgkmcnt(0)
	s_andn2_b64 vcc, exec, s[20:21]
	s_barrier
	s_cbranch_vccnz .LBB0_1102
	s_setprio 1
	v_mfma_f32_16x16x32_bf16 v[66:69], v[150:153], v[190:193], v[66:69]
	v_mfma_f32_16x16x32_bf16 v[62:65], v[158:161], v[190:193], v[62:65]
	v_mfma_f32_16x16x32_bf16 v[50:53], v[150:153], v[178:181], v[50:53]
	v_mfma_f32_16x16x32_bf16 v[46:49], v[158:161], v[178:181], v[46:49]
	v_mfma_f32_16x16x32_bf16 v[34:37], v[150:153], v[174:177], v[34:37]
	v_mfma_f32_16x16x32_bf16 v[30:33], v[158:161], v[174:177], v[30:33]
	v_mfma_f32_16x16x32_bf16 v[18:21], v[150:153], v[166:169], v[18:21]
	v_mfma_f32_16x16x32_bf16 v[14:17], v[158:161], v[166:169], v[14:17]
	v_mfma_f32_16x16x32_bf16 v[66:69], v[154:157], v[194:197], v[66:69]
	v_mfma_f32_16x16x32_bf16 v[62:65], v[162:165], v[194:197], v[62:65]
	v_mfma_f32_16x16x32_bf16 v[50:53], v[154:157], v[182:185], v[50:53]
	v_mfma_f32_16x16x32_bf16 v[46:49], v[162:165], v[182:185], v[46:49]
	v_mfma_f32_16x16x32_bf16 v[34:37], v[154:157], v[186:189], v[34:37]
	v_mfma_f32_16x16x32_bf16 v[30:33], v[162:165], v[186:189], v[30:33]
	v_mfma_f32_16x16x32_bf16 v[18:21], v[154:157], v[170:173], v[18:21]
	v_mfma_f32_16x16x32_bf16 v[14:17], v[162:165], v[170:173], v[14:17]
	v_mfma_f32_16x16x32_bf16 v[58:61], v[134:137], v[190:193], v[58:61]
	v_mfma_f32_16x16x32_bf16 v[54:57], v[142:145], v[190:193], v[54:57]
	v_mfma_f32_16x16x32_bf16 v[42:45], v[134:137], v[178:181], v[42:45]
	v_mfma_f32_16x16x32_bf16 v[38:41], v[142:145], v[178:181], v[38:41]
	v_mfma_f32_16x16x32_bf16 v[26:29], v[134:137], v[174:177], v[26:29]
	v_mfma_f32_16x16x32_bf16 v[22:25], v[142:145], v[174:177], v[22:25]
	v_mfma_f32_16x16x32_bf16 v[10:13], v[134:137], v[166:169], v[10:13]
	v_mfma_f32_16x16x32_bf16 v[4:7], v[142:145], v[166:169], v[6:9]
	v_mfma_f32_16x16x32_bf16 v[58:61], v[138:141], v[194:197], v[58:61]
	v_mfma_f32_16x16x32_bf16 v[54:57], v[146:149], v[194:197], v[54:57]
	v_mfma_f32_16x16x32_bf16 v[42:45], v[138:141], v[182:185], v[42:45]
	v_mfma_f32_16x16x32_bf16 v[38:41], v[146:149], v[182:185], v[38:41]
	v_mfma_f32_16x16x32_bf16 v[26:29], v[138:141], v[186:189], v[26:29]
	v_mfma_f32_16x16x32_bf16 v[22:25], v[146:149], v[186:189], v[22:25]
	v_mfma_f32_16x16x32_bf16 v[10:13], v[138:141], v[170:173], v[10:13]
	v_mfma_f32_16x16x32_bf16 v[6:9], v[146:149], v[170:173], v[4:7]
	s_setprio 0
.LBB0_1102:
	s_add_u32 s8, s22, 0x4000
	s_addc_u32 s9, s23, 0
	s_cmp_eq_u32 s61, s59
	s_cselect_b32 s27, s15, s9
	s_cselect_b32 s26, s14, s8
	s_cselect_b32 s25, s17, s63
	s_cselect_b32 s24, s16, s62
	s_barrier
	s_mov_b32 m0, s29
	v_lshl_add_u64 v[4:5], s[24:25], 0, v[208:209]
	s_add_u32 s8, s24, 0xb0000
	s_waitcnt lgkmcnt(0)
	ds_read_b128 v[190:193], v226 offset:16384
	ds_read_b128 v[178:181], v226 offset:18432
	ds_read_b128 v[194:197], v227 offset:16384
	ds_read_b128 v[182:185], v227 offset:18432
	ds_read_b128 v[174:177], v226 offset:20480
	ds_read_b128 v[166:169], v226 offset:22528
	ds_read_b128 v[186:189], v227 offset:20480
	ds_read_b128 v[170:173], v227 offset:22528
	global_load_lds_dwordx4 v[4:5], off
	v_lshl_add_u64 v[4:5], s[24:25], 0, v[210:211]
	s_mov_b32 m0, s30
	s_addc_u32 s9, s25, 0
	global_load_lds_dwordx4 v[4:5], off
	v_lshl_add_u64 v[4:5], s[8:9], 0, v[208:209]
	s_mov_b32 m0, s31
	v_cndmask_b32_e64 v3, 0, 1, s[18:19]
	global_load_lds_dwordx4 v[4:5], off
	v_lshl_add_u64 v[4:5], s[8:9], 0, v[210:211]
	s_mov_b32 m0, s34
	v_cmp_ne_u32_e64 s[8:9], 1, v3
	global_load_lds_dwordx4 v[4:5], off
	v_lshl_add_u64 v[4:5], s[26:27], 0, v[200:201]
	s_mov_b32 m0, s28
	s_andn2_b64 vcc, exec, s[18:19]
	global_load_lds_dwordx4 v[4:5], off
	v_lshl_add_u64 v[4:5], s[26:27], 0, v[202:203]
	s_mov_b32 m0, s35
	s_nop 0
	global_load_lds_dwordx4 v[4:5], off
	s_waitcnt vmcnt(8)
	s_waitcnt lgkmcnt(0)
	s_barrier
	s_cbranch_vccnz .LBB0_1104
	s_setprio 1
	v_mfma_f32_16x16x32_bf16 v[130:133], v[150:153], v[190:193], v[130:133]
	v_mfma_f32_16x16x32_bf16 v[126:129], v[158:161], v[190:193], v[126:129]
	v_mfma_f32_16x16x32_bf16 v[114:117], v[150:153], v[178:181], v[114:117]
	v_mfma_f32_16x16x32_bf16 v[110:113], v[158:161], v[178:181], v[110:113]
	v_mfma_f32_16x16x32_bf16 v[98:101], v[150:153], v[174:177], v[98:101]
	v_mfma_f32_16x16x32_bf16 v[94:97], v[158:161], v[174:177], v[94:97]
	v_mfma_f32_16x16x32_bf16 v[82:85], v[150:153], v[166:169], v[82:85]
	v_mfma_f32_16x16x32_bf16 v[78:81], v[158:161], v[166:169], v[78:81]
	v_mfma_f32_16x16x32_bf16 v[130:133], v[154:157], v[194:197], v[130:133]
	v_mfma_f32_16x16x32_bf16 v[126:129], v[162:165], v[194:197], v[126:129]
	v_mfma_f32_16x16x32_bf16 v[114:117], v[154:157], v[182:185], v[114:117]
	v_mfma_f32_16x16x32_bf16 v[110:113], v[162:165], v[182:185], v[110:113]
	v_mfma_f32_16x16x32_bf16 v[98:101], v[154:157], v[186:189], v[98:101]
	v_mfma_f32_16x16x32_bf16 v[94:97], v[162:165], v[186:189], v[94:97]
	v_mfma_f32_16x16x32_bf16 v[82:85], v[154:157], v[170:173], v[82:85]
	v_mfma_f32_16x16x32_bf16 v[78:81], v[162:165], v[170:173], v[78:81]
	v_mfma_f32_16x16x32_bf16 v[122:125], v[134:137], v[190:193], v[122:125]
	v_mfma_f32_16x16x32_bf16 v[118:121], v[142:145], v[190:193], v[118:121]
	v_mfma_f32_16x16x32_bf16 v[106:109], v[134:137], v[178:181], v[106:109]
	v_mfma_f32_16x16x32_bf16 v[102:105], v[142:145], v[178:181], v[102:105]
	v_mfma_f32_16x16x32_bf16 v[90:93], v[134:137], v[174:177], v[90:93]
	v_mfma_f32_16x16x32_bf16 v[86:89], v[142:145], v[174:177], v[86:89]
	v_mfma_f32_16x16x32_bf16 v[74:77], v[134:137], v[166:169], v[74:77]
	v_mfma_f32_16x16x32_bf16 v[70:73], v[142:145], v[166:169], v[70:73]
	v_mfma_f32_16x16x32_bf16 v[122:125], v[138:141], v[194:197], v[122:125]
	v_mfma_f32_16x16x32_bf16 v[118:121], v[146:149], v[194:197], v[118:121]
	v_mfma_f32_16x16x32_bf16 v[106:109], v[138:141], v[182:185], v[106:109]
	v_mfma_f32_16x16x32_bf16 v[102:105], v[146:149], v[182:185], v[102:105]
	v_mfma_f32_16x16x32_bf16 v[90:93], v[138:141], v[186:189], v[90:93]
	v_mfma_f32_16x16x32_bf16 v[86:89], v[146:149], v[186:189], v[86:89]
	v_mfma_f32_16x16x32_bf16 v[74:77], v[138:141], v[170:173], v[74:77]
	v_mfma_f32_16x16x32_bf16 v[70:73], v[146:149], v[170:173], v[70:73]
	s_setprio 0
; #define PG8_STAGE(bufoff, gbase, voff) do { _Pragma("unroll") for (int _i = 0; _i < 2; ++_i) \
;         __builtin_amdgcn_global_load_lds((const unsigned*)((const char*)(gbase) + (voff)[_i]), (LAS unsigned*)(lds + (bufoff) + ldsw + _i * 8192), 16, 0, 0); } while (0)
; #define PG8_LDA(dst, b, h) do { _Pragma("unroll") for (int m = 0; m < 4; ++m) _Pragma("unroll") for (int k = 0; k < 2; ++k) dst[m][k] = *(const LAS bf16x8*)(lds + PG8_SA(b, h) + ((aoff ^ (k * 64)) + m * 2048)); } while (0)
; #define PG8_LDB(dst, b, h) do { _Pragma("unroll") for (int n = 0; n < 2; ++n) _Pragma("unroll") for (int k = 0; k < 2; ++k) dst[n][k] = *(const LAS bf16x8*)(lds + PG8_SB(b, h) + ((boff ^ (k * 64)) + n * 2048)); } while (0)
; #define PG8_MMA(ai, bj, At, Bt) do { __builtin_amdgcn_s_setprio(1); _Pragma("unroll") for (int m = 0; m < 4; ++m) _Pragma("unroll") for (int n = 0; n < 2; ++n) _Pragma("unroll") for (int k = 0; k < 2; ++k) \
;         acc[ai][bj][m][n] = __builtin_amdgcn_mfma_f32_16x16x32_bf16(Bt[n][k], At[m][k], acc[ai][bj][m][n], 0, 0, 0); __builtin_amdgcn_s_setprio(0); } while (0)
; #define PG8_WAIT_V(n) asm volatile("s_waitcnt vmcnt(" #n ")" ::: "memory")
; #define PG8_WAIT_L(n) asm volatile("s_waitcnt lgkmcnt(" #n ")" ::: "memory")
; #define PG8_BAR __builtin_amdgcn_s_barrier()
; #define PG8_SCHED __builtin_amdgcn_sched_barrier(0)
;     ...
;             PG8_LDB(B0, 1, 0); PG8_LDB(B1, 1, 1); PG8_SCHED; PG8_LDA(At, 1, 0); PG8_STAGE(PG8_SA(0, 1), a2, vs[1]);
;             PG8_WAIT_V(8); PG8_WAIT_L(0); PG8_BAR; if (do0) { PG8_MMA(0, 0, At, B0); PG8_MMA(0, 1, At, B1); } PG8_BAR; PG8_SCHED;
.LBB0_1104:
	s_barrier
	s_add_i32 s64, 0, 0x18000
	v_add_u32_e32 v3, s64, v199
	v_add_u32_e32 v4, s64, v216
	ds_read_b128 v[150:153], v3
	ds_read_b128 v[154:157], v4
	v_add_u32_e32 v3, s48, v199
	s_add_i32 s64, 0, 0x1c000
	v_add_u32_e32 v4, s48, v216
	ds_read_b128 v[158:161], v3
	ds_read_b128 v[162:165], v4
	v_add_u32_e32 v3, s64, v199
	v_add_u32_e32 v4, s64, v216
	ds_read_b128 v[134:137], v3
	ds_read_b128 v[138:141], v4
	v_add_u32_e32 v3, s49, v199
	v_add_u32_e32 v4, s49, v216
	ds_read_b128 v[142:145], v3
	ds_read_b128 v[146:149], v4
	s_mov_b32 m0, s36
	v_lshl_add_u64 v[4:5], s[26:27], 0, v[204:205]
	s_waitcnt lgkmcnt(0)
	ds_read_b128 v[190:193], v226 offset:32768
	ds_read_b128 v[178:181], v226 offset:34816
	ds_read_b128 v[194:197], v227 offset:32768
	ds_read_b128 v[182:185], v227 offset:34816
	ds_read_b128 v[174:177], v226 offset:36864
	ds_read_b128 v[166:169], v226 offset:38912
	ds_read_b128 v[186:189], v227 offset:36864
	ds_read_b128 v[170:173], v227 offset:38912
	global_load_lds_dwordx4 v[4:5], off
	v_lshl_add_u64 v[4:5], s[26:27], 0, v[206:207]
	s_mov_b32 m0, s37
	s_and_b64 vcc, exec, s[6:7]
	global_load_lds_dwordx4 v[4:5], off
	s_waitcnt vmcnt(8)
	s_waitcnt lgkmcnt(0)
	s_barrier
	s_cbranch_vccnz .LBB0_1106
	s_setprio 1
	v_mfma_f32_16x16x32_bf16 v[66:69], v[150:153], v[190:193], v[66:69]
	v_mfma_f32_16x16x32_bf16 v[62:65], v[158:161], v[190:193], v[62:65]
	v_mfma_f32_16x16x32_bf16 v[50:53], v[150:153], v[178:181], v[50:53]
	v_mfma_f32_16x16x32_bf16 v[46:49], v[158:161], v[178:181], v[46:49]
	v_mfma_f32_16x16x32_bf16 v[34:37], v[150:153], v[174:177], v[34:37]
	v_mfma_f32_16x16x32_bf16 v[30:33], v[158:161], v[174:177], v[30:33]
	v_mfma_f32_16x16x32_bf16 v[18:21], v[150:153], v[166:169], v[18:21]
	v_mfma_f32_16x16x32_bf16 v[14:17], v[158:161], v[166:169], v[14:17]
	v_mfma_f32_16x16x32_bf16 v[66:69], v[154:157], v[194:197], v[66:69]
	v_mfma_f32_16x16x32_bf16 v[62:65], v[162:165], v[194:197], v[62:65]
	v_mfma_f32_16x16x32_bf16 v[50:53], v[154:157], v[182:185], v[50:53]
	v_mfma_f32_16x16x32_bf16 v[46:49], v[162:165], v[182:185], v[46:49]
	v_mfma_f32_16x16x32_bf16 v[34:37], v[154:157], v[186:189], v[34:37]
	v_mfma_f32_16x16x32_bf16 v[30:33], v[162:165], v[186:189], v[30:33]
	v_mfma_f32_16x16x32_bf16 v[18:21], v[154:157], v[170:173], v[18:21]
	v_mfma_f32_16x16x32_bf16 v[14:17], v[162:165], v[170:173], v[14:17]
	v_mfma_f32_16x16x32_bf16 v[58:61], v[134:137], v[190:193], v[58:61]
	v_mfma_f32_16x16x32_bf16 v[54:57], v[142:145], v[190:193], v[54:57]
	v_mfma_f32_16x16x32_bf16 v[42:45], v[134:137], v[178:181], v[42:45]
	v_mfma_f32_16x16x32_bf16 v[38:41], v[142:145], v[178:181], v[38:41]
	v_mfma_f32_16x16x32_bf16 v[26:29], v[134:137], v[174:177], v[26:29]
	v_mfma_f32_16x16x32_bf16 v[22:25], v[142:145], v[174:177], v[22:25]
	v_mfma_f32_16x16x32_bf16 v[10:13], v[134:137], v[166:169], v[10:13]
	v_mfma_f32_16x16x32_bf16 v[4:7], v[142:145], v[166:169], v[6:9]
	v_mfma_f32_16x16x32_bf16 v[58:61], v[138:141], v[194:197], v[58:61]
	v_mfma_f32_16x16x32_bf16 v[54:57], v[146:149], v[194:197], v[54:57]
	v_mfma_f32_16x16x32_bf16 v[42:45], v[138:141], v[182:185], v[42:45]
	v_mfma_f32_16x16x32_bf16 v[38:41], v[146:149], v[182:185], v[38:41]
	v_mfma_f32_16x16x32_bf16 v[26:29], v[138:141], v[186:189], v[26:29]
	v_mfma_f32_16x16x32_bf16 v[22:25], v[146:149], v[186:189], v[22:25]
	v_mfma_f32_16x16x32_bf16 v[10:13], v[138:141], v[170:173], v[10:13]
	v_mfma_f32_16x16x32_bf16 v[6:9], v[146:149], v[170:173], v[4:7]
	s_setprio 0
; #define PG8_STAGE(bufoff, gbase, voff) do { _Pragma("unroll") for (int _i = 0; _i < 2; ++_i) \
;         __builtin_amdgcn_global_load_lds((const unsigned*)((const char*)(gbase) + (voff)[_i]), (LAS unsigned*)(lds + (bufoff) + ldsw + _i * 8192), 16, 0, 0); } while (0)
; #define PG8_LDA(dst, b, h) do { _Pragma("unroll") for (int m = 0; m < 4; ++m) _Pragma("unroll") for (int k = 0; k < 2; ++k) dst[m][k] = *(const LAS bf16x8*)(lds + PG8_SA(b, h) + ((aoff ^ (k * 64)) + m * 2048)); } while (0)
; #define PG8_MMA(ai, bj, At, Bt) do { __builtin_amdgcn_s_setprio(1); _Pragma("unroll") for (int m = 0; m < 4; ++m) _Pragma("unroll") for (int n = 0; n < 2; ++n) _Pragma("unroll") for (int k = 0; k < 2; ++k) \
;         acc[ai][bj][m][n] = __builtin_amdgcn_mfma_f32_16x16x32_bf16(Bt[n][k], At[m][k], acc[ai][bj][m][n], 0, 0, 0); __builtin_amdgcn_s_setprio(0); } while (0)
; #define PG8_WAIT_V(n) asm volatile("s_waitcnt vmcnt(" #n ")" ::: "memory")
; #define PG8_WAIT_L(n) asm volatile("s_waitcnt lgkmcnt(" #n ")" ::: "memory")
; #define PG8_BAR __builtin_amdgcn_s_barrier()
; #define PG8_SCHED __builtin_amdgcn_sched_barrier(0)
;     ...
;             PG8_LDA(At, 1, 1); PG8_STAGE(PG8_SB(1, 0), b3, voffB); PG8_STAGE(PG8_SB(1, 1), b3 + hstep, voffB); PG8_STAGE(PG8_SA(1, 0), a3, vs[0]);
;             PG8_WAIT_V(8); PG8_WAIT_L(0); PG8_BAR; if (do1) { PG8_MMA(1, 0, At, B0); PG8_MMA(1, 1, At, B1); } PG8_BAR; PG8_SCHED;
;         }
.LBB0_1106:
	s_add_u32 s6, s26, 0x4000
	s_addc_u32 s7, s27, 0
	s_add_u32 s26, s24, 0x4000
	s_addc_u32 s27, s25, 0
	s_barrier
	s_mov_b32 m0, s39
	v_lshl_add_u64 v[4:5], s[26:27], 0, v[208:209]
	s_add_u32 s24, s24, 0xb4000
	s_waitcnt lgkmcnt(0)
	ds_read_b128 v[190:193], v226 offset:49152
	ds_read_b128 v[178:181], v226 offset:51200
	ds_read_b128 v[194:197], v227 offset:49152
	ds_read_b128 v[182:185], v227 offset:51200
	ds_read_b128 v[174:177], v226 offset:53248
	ds_read_b128 v[166:169], v226 offset:55296
	ds_read_b128 v[186:189], v227 offset:53248
	ds_read_b128 v[170:173], v227 offset:55296
	global_load_lds_dwordx4 v[4:5], off
	v_lshl_add_u64 v[4:5], s[26:27], 0, v[210:211]
	s_mov_b32 m0, s40
	s_addc_u32 s25, s25, 0
	global_load_lds_dwordx4 v[4:5], off
	v_lshl_add_u64 v[4:5], s[24:25], 0, v[208:209]
	s_mov_b32 m0, s43
	s_and_b64 vcc, exec, s[8:9]
	global_load_lds_dwordx4 v[4:5], off
	v_lshl_add_u64 v[4:5], s[24:25], 0, v[210:211]
	s_mov_b32 m0, s44
	s_nop 0
	global_load_lds_dwordx4 v[4:5], off
	v_lshl_add_u64 v[4:5], s[6:7], 0, v[200:201]
	s_mov_b32 m0, s41
	s_nop 0
	global_load_lds_dwordx4 v[4:5], off
	v_lshl_add_u64 v[4:5], s[6:7], 0, v[202:203]
	s_mov_b32 m0, s42
	s_nop 0
	global_load_lds_dwordx4 v[4:5], off
	s_waitcnt vmcnt(8)
	s_waitcnt lgkmcnt(0)
	s_barrier
	s_cbranch_vccnz .LBB0_1099
	s_setprio 1
	v_mfma_f32_16x16x32_bf16 v[130:133], v[150:153], v[190:193], v[130:133]
	v_mfma_f32_16x16x32_bf16 v[126:129], v[158:161], v[190:193], v[126:129]
	v_mfma_f32_16x16x32_bf16 v[114:117], v[150:153], v[178:181], v[114:117]
	v_mfma_f32_16x16x32_bf16 v[110:113], v[158:161], v[178:181], v[110:113]
	v_mfma_f32_16x16x32_bf16 v[98:101], v[150:153], v[174:177], v[98:101]
	v_mfma_f32_16x16x32_bf16 v[94:97], v[158:161], v[174:177], v[94:97]
	v_mfma_f32_16x16x32_bf16 v[82:85], v[150:153], v[166:169], v[82:85]
	v_mfma_f32_16x16x32_bf16 v[78:81], v[158:161], v[166:169], v[78:81]
	v_mfma_f32_16x16x32_bf16 v[130:133], v[154:157], v[194:197], v[130:133]
	v_mfma_f32_16x16x32_bf16 v[126:129], v[162:165], v[194:197], v[126:129]
	v_mfma_f32_16x16x32_bf16 v[114:117], v[154:157], v[182:185], v[114:117]
	v_mfma_f32_16x16x32_bf16 v[110:113], v[162:165], v[182:185], v[110:113]
	v_mfma_f32_16x16x32_bf16 v[98:101], v[154:157], v[186:189], v[98:101]
	v_mfma_f32_16x16x32_bf16 v[94:97], v[162:165], v[186:189], v[94:97]
	v_mfma_f32_16x16x32_bf16 v[82:85], v[154:157], v[170:173], v[82:85]
	v_mfma_f32_16x16x32_bf16 v[78:81], v[162:165], v[170:173], v[78:81]
	v_mfma_f32_16x16x32_bf16 v[122:125], v[134:137], v[190:193], v[122:125]
	v_mfma_f32_16x16x32_bf16 v[118:121], v[142:145], v[190:193], v[118:121]
	v_mfma_f32_16x16x32_bf16 v[106:109], v[134:137], v[178:181], v[106:109]
	v_mfma_f32_16x16x32_bf16 v[102:105], v[142:145], v[178:181], v[102:105]
	v_mfma_f32_16x16x32_bf16 v[90:93], v[134:137], v[174:177], v[90:93]
	v_mfma_f32_16x16x32_bf16 v[86:89], v[142:145], v[174:177], v[86:89]
	v_mfma_f32_16x16x32_bf16 v[74:77], v[134:137], v[166:169], v[74:77]
	v_mfma_f32_16x16x32_bf16 v[70:73], v[142:145], v[166:169], v[70:73]
	v_mfma_f32_16x16x32_bf16 v[122:125], v[138:141], v[194:197], v[122:125]
	v_mfma_f32_16x16x32_bf16 v[118:121], v[146:149], v[194:197], v[118:121]
	v_mfma_f32_16x16x32_bf16 v[106:109], v[138:141], v[182:185], v[106:109]
	v_mfma_f32_16x16x32_bf16 v[102:105], v[146:149], v[182:185], v[102:105]
	v_mfma_f32_16x16x32_bf16 v[90:93], v[138:141], v[186:189], v[90:93]
	v_mfma_f32_16x16x32_bf16 v[86:89], v[146:149], v[186:189], v[86:89]
	v_mfma_f32_16x16x32_bf16 v[74:77], v[138:141], v[170:173], v[74:77]
	v_mfma_f32_16x16x32_bf16 v[70:73], v[146:149], v[170:173], v[70:73]
	s_setprio 0
	s_branch .LBB0_1099

; #define PG8_STAGE(bufoff, gbase, voff) do { _Pragma("unroll") for (int _i = 0; _i < 2; ++_i) \
;         __builtin_amdgcn_global_load_lds((const unsigned*)((const char*)(gbase) + (voff)[_i]), (LAS unsigned*)(lds + (bufoff) + ldsw + _i * 8192), 16, 0, 0); } while (0)
; #define PG8_LDA(dst, b, h) do { _Pragma("unroll") for (int m = 0; m < 4; ++m) _Pragma("unroll") for (int k = 0; k < 2; ++k) dst[m][k] = *(const LAS bf16x8*)(lds + PG8_SA(b, h) + ((aoff ^ (k * 64)) + m * 2048)); } while (0)
; #define PG8_LDB(dst, b, h) do { _Pragma("unroll") for (int n = 0; n < 2; ++n) _Pragma("unroll") for (int k = 0; k < 2; ++k) dst[n][k] = *(const LAS bf16x8*)(lds + PG8_SB(b, h) + ((boff ^ (k * 64)) + n * 2048)); } while (0)
; #define PG8_MMA(ai, bj, At, Bt) do { __builtin_amdgcn_s_setprio(1); _Pragma("unroll") for (int m = 0; m < 4; ++m) _Pragma("unroll") for (int n = 0; n < 2; ++n) _Pragma("unroll") for (int k = 0; k < 2; ++k) \
;         acc[ai][bj][m][n] = __builtin_amdgcn_mfma_f32_16x16x32_bf16(Bt[n][k], At[m][k], acc[ai][bj][m][n], 0, 0, 0); __builtin_amdgcn_s_setprio(0); } while (0)
; #define PG8_WAIT_V(n) asm volatile("s_waitcnt vmcnt(" #n ")" ::: "memory")
; #define PG8_WAIT_L(n) asm volatile("s_waitcnt lgkmcnt(" #n ")" ::: "memory")
; #define PG8_BAR __builtin_amdgcn_s_barrier()
; #define PG8_SCHED __builtin_amdgcn_sched_barrier(0)
;     ...
;             PG8_LDB(B0, 0, 0); PG8_LDB(B1, 0, 1); PG8_SCHED; PG8_LDA(At, 0, 0); PG8_STAGE(PG8_SA(1, 1), a1, voffA[1]);
;             PG8_WAIT_V(8); PG8_WAIT_L(0); PG8_BAR; if (do0) { PG8_MMA(0, 0, At, B0); PG8_MMA(0, 1, At, B1); } PG8_BAR; PG8_SCHED;
;             PG8_LDA(At, 0, 1); PG8_STAGE(PG8_SB(0, 0), b2, voffB); PG8_STAGE(PG8_SB(0, 1), b2 + hstep, voffB); PG8_STAGE(PG8_SA(0, 0), a2, vs[0]);
;             PG8_WAIT_V(8); PG8_WAIT_L(0); PG8_BAR; if (do1) { PG8_MMA(1, 0, At, B0); PG8_MMA(1, 1, At, B1); } PG8_BAR; PG8_SCHED;
.LBB0_1257:
	ds_read_b128 v[156:159], v176
	ds_read_b128 v[160:163], v177
	ds_read_b128 v[164:167], v178
	ds_read_b128 v[192:195], v179
	ds_read_b128 v[200:203], v180
	ds_read_b128 v[204:207], v181
	ds_read_b128 v[208:211], v182
	ds_read_b128 v[212:215], v183
	s_add_u32 s40, s38, 0x80
	s_addc_u32 s41, s39, 0
	s_cmp_eq_u32 s63, 12
	s_cselect_b32 s45, s3, s41
	s_cselect_b32 s44, s11, s40
	s_cselect_b32 s41, s12, s62
	s_cselect_b32 s40, s29, s31
	v_lshl_add_u64 v[168:169], s[38:39], 0, v[150:151]
	s_add_i32 m0, s47, 0xc000
	ds_read_b128 v[216:219], v184
	ds_read_b128 v[220:223], v184 offset:2048
	ds_read_b128 v[224:227], v185
	ds_read_b128 v[228:231], v185 offset:2048
	ds_read_b128 v[232:235], v184 offset:4096
	ds_read_b128 v[236:239], v184 offset:6144
	ds_read_b128 v[240:243], v185 offset:4096
	ds_read_b128 v[244:247], v185 offset:6144
	global_load_lds_dwordx4 v[168:169], off
	v_lshl_add_u64 v[168:169], s[38:39], 0, v[148:149]
	s_add_i32 m0, s47, 0xe000
	s_add_u32 s42, s40, 0x4000
	global_load_lds_dwordx4 v[168:169], off
	s_waitcnt vmcnt(8)
	s_waitcnt lgkmcnt(0)
	s_addc_u32 s43, s41, 0
	s_barrier
	s_setprio 1
	v_mfma_f32_16x16x32_bf16 v[126:129], v[156:159], v[216:219], v[126:129]
	v_mfma_f32_16x16x32_bf16 v[118:121], v[164:167], v[216:219], v[118:121]
	v_mfma_f32_16x16x32_bf16 v[110:113], v[156:159], v[220:223], v[110:113]
	v_mfma_f32_16x16x32_bf16 v[102:105], v[164:167], v[220:223], v[102:105]
	v_mfma_f32_16x16x32_bf16 v[94:97], v[156:159], v[232:235], v[94:97]
	v_mfma_f32_16x16x32_bf16 v[86:89], v[164:167], v[232:235], v[86:89]
	v_mfma_f32_16x16x32_bf16 v[78:81], v[156:159], v[236:239], v[78:81]
	v_mfma_f32_16x16x32_bf16 v[70:73], v[164:167], v[236:239], v[70:73]
	v_mfma_f32_16x16x32_bf16 v[126:129], v[160:163], v[224:227], v[126:129]
	v_mfma_f32_16x16x32_bf16 v[118:121], v[192:195], v[224:227], v[118:121]
	v_mfma_f32_16x16x32_bf16 v[110:113], v[160:163], v[228:231], v[110:113]
	v_mfma_f32_16x16x32_bf16 v[102:105], v[192:195], v[228:231], v[102:105]
	v_mfma_f32_16x16x32_bf16 v[94:97], v[160:163], v[240:243], v[94:97]
	v_mfma_f32_16x16x32_bf16 v[86:89], v[192:195], v[240:243], v[86:89]
	v_mfma_f32_16x16x32_bf16 v[78:81], v[160:163], v[244:247], v[78:81]
	v_mfma_f32_16x16x32_bf16 v[70:73], v[192:195], v[244:247], v[70:73]
	v_mfma_f32_16x16x32_bf16 v[122:125], v[200:203], v[216:219], v[122:125]
	v_mfma_f32_16x16x32_bf16 v[114:117], v[208:211], v[216:219], v[114:117]
	v_mfma_f32_16x16x32_bf16 v[106:109], v[200:203], v[220:223], v[106:109]
	v_mfma_f32_16x16x32_bf16 v[98:101], v[208:211], v[220:223], v[98:101]
	v_mfma_f32_16x16x32_bf16 v[90:93], v[200:203], v[232:235], v[90:93]
	v_mfma_f32_16x16x32_bf16 v[82:85], v[208:211], v[232:235], v[82:85]
	v_mfma_f32_16x16x32_bf16 v[74:77], v[200:203], v[236:239], v[74:77]
	v_mfma_f32_16x16x32_bf16 v[66:69], v[208:211], v[236:239], v[66:69]
	v_mfma_f32_16x16x32_bf16 v[122:125], v[204:207], v[224:227], v[122:125]
	v_mfma_f32_16x16x32_bf16 v[114:117], v[212:215], v[224:227], v[114:117]
	v_mfma_f32_16x16x32_bf16 v[106:109], v[204:207], v[228:231], v[106:109]
	v_mfma_f32_16x16x32_bf16 v[98:101], v[212:215], v[228:231], v[98:101]
	v_mfma_f32_16x16x32_bf16 v[90:93], v[204:207], v[240:243], v[90:93]
	v_mfma_f32_16x16x32_bf16 v[82:85], v[212:215], v[240:243], v[82:85]
	v_mfma_f32_16x16x32_bf16 v[74:77], v[204:207], v[244:247], v[74:77]
	v_mfma_f32_16x16x32_bf16 v[66:69], v[212:215], v[244:247], v[66:69]
	s_setprio 0
	s_barrier
	s_add_i32 s64, s56, s46
	v_lshl_add_u64 v[168:169], s[40:41], 0, v[130:131]
	s_mov_b32 m0, s64
	ds_read_b128 v[216:219], v184 offset:16384
	ds_read_b128 v[220:223], v184 offset:18432
	ds_read_b128 v[224:227], v185 offset:16384
	ds_read_b128 v[228:231], v185 offset:18432
	ds_read_b128 v[232:235], v184 offset:20480
	ds_read_b128 v[236:239], v184 offset:22528
	ds_read_b128 v[240:243], v185 offset:20480
	ds_read_b128 v[244:247], v185 offset:22528
	global_load_lds_dwordx4 v[168:169], off
	s_add_i32 m0, s64, 0x2000
	s_add_u32 s64, s40, 0x40000
	v_lshl_add_u64 v[168:169], s[40:41], 0, v[132:133]
	s_addc_u32 s65, s41, 0
	s_add_i32 s66, s57, s46
	global_load_lds_dwordx4 v[168:169], off
	v_lshl_add_u64 v[168:169], s[64:65], 0, v[130:131]
	s_mov_b32 m0, s66
	v_lshl_add_u64 v[196:197], s[44:45], 0, v[136:137]
	global_load_lds_dwordx4 v[168:169], off
	v_lshl_add_u64 v[168:169], s[64:65], 0, v[132:133]
	s_add_i32 m0, s66, 0x2000
	s_nop 0
	global_load_lds_dwordx4 v[168:169], off
	v_lshl_add_u64 v[168:169], s[44:45], 0, v[134:135]
	s_mov_b32 m0, s47
	s_nop 0
	global_load_lds_dwordx4 v[168:169], off
	s_mov_b32 m0, s48
	s_nop 0
	global_load_lds_dwordx4 v[196:197], off
	s_waitcnt vmcnt(8)
	s_waitcnt lgkmcnt(0)
	s_barrier
; #define PG8_STAGE(bufoff, gbase, voff) do { _Pragma("unroll") for (int _i = 0; _i < 2; ++_i) \
;         __builtin_amdgcn_global_load_lds((const unsigned*)((const char*)(gbase) + (voff)[_i]), (LAS unsigned*)(lds + (bufoff) + ldsw + _i * 8192), 16, 0, 0); } while (0)
; #define PG8_LDA(dst, b, h) do { _Pragma("unroll") for (int m = 0; m < 4; ++m) _Pragma("unroll") for (int k = 0; k < 2; ++k) dst[m][k] = *(const LAS bf16x8*)(lds + PG8_SA(b, h) + ((aoff ^ (k * 64)) + m * 2048)); } while (0)
; #define PG8_LDB(dst, b, h) do { _Pragma("unroll") for (int n = 0; n < 2; ++n) _Pragma("unroll") for (int k = 0; k < 2; ++k) dst[n][k] = *(const LAS bf16x8*)(lds + PG8_SB(b, h) + ((boff ^ (k * 64)) + n * 2048)); } while (0)
; #define PG8_MMA(ai, bj, At, Bt) do { __builtin_amdgcn_s_setprio(1); _Pragma("unroll") for (int m = 0; m < 4; ++m) _Pragma("unroll") for (int n = 0; n < 2; ++n) _Pragma("unroll") for (int k = 0; k < 2; ++k) \
;         acc[ai][bj][m][n] = __builtin_amdgcn_mfma_f32_16x16x32_bf16(Bt[n][k], At[m][k], acc[ai][bj][m][n], 0, 0, 0); __builtin_amdgcn_s_setprio(0); } while (0)
; #define PG8_WAIT_V(n) asm volatile("s_waitcnt vmcnt(" #n ")" ::: "memory")
; #define PG8_WAIT_L(n) asm volatile("s_waitcnt lgkmcnt(" #n ")" ::: "memory")
; #define PG8_BAR __builtin_amdgcn_s_barrier()
; #define PG8_SCHED __builtin_amdgcn_sched_barrier(0)
;     ...
;             PG8_WAIT_V(8); PG8_WAIT_L(0); PG8_BAR; if (do1) { PG8_MMA(1, 0, At, B0); PG8_MMA(1, 1, At, B1); } PG8_BAR; PG8_SCHED;
;             PG8_LDB(B0, 1, 0); PG8_LDB(B1, 1, 1); PG8_SCHED; PG8_LDA(At, 1, 0); PG8_STAGE(PG8_SA(0, 1), a2, vs[1]);
;             PG8_WAIT_V(8); PG8_WAIT_L(0); PG8_BAR; if (do0) { PG8_MMA(0, 0, At, B0); PG8_MMA(0, 1, At, B1); } PG8_BAR; PG8_SCHED;
	s_setprio 1
	v_mfma_f32_16x16x32_bf16 v[62:65], v[156:159], v[216:219], v[62:65]
	v_mfma_f32_16x16x32_bf16 v[54:57], v[164:167], v[216:219], v[54:57]
	v_mfma_f32_16x16x32_bf16 v[46:49], v[156:159], v[220:223], v[46:49]
	v_mfma_f32_16x16x32_bf16 v[38:41], v[164:167], v[220:223], v[38:41]
	v_mfma_f32_16x16x32_bf16 v[30:33], v[156:159], v[232:235], v[30:33]
	v_mfma_f32_16x16x32_bf16 v[22:25], v[164:167], v[232:235], v[22:25]
	v_mfma_f32_16x16x32_bf16 v[14:17], v[156:159], v[236:239], v[14:17]
	v_mfma_f32_16x16x32_bf16 v[6:9], v[164:167], v[236:239], v[6:9]
	v_mfma_f32_16x16x32_bf16 v[62:65], v[160:163], v[224:227], v[62:65]
	v_mfma_f32_16x16x32_bf16 v[54:57], v[192:195], v[224:227], v[54:57]
	v_mfma_f32_16x16x32_bf16 v[46:49], v[160:163], v[228:231], v[46:49]
	v_mfma_f32_16x16x32_bf16 v[38:41], v[192:195], v[228:231], v[38:41]
	v_mfma_f32_16x16x32_bf16 v[30:33], v[160:163], v[240:243], v[30:33]
	v_mfma_f32_16x16x32_bf16 v[22:25], v[192:195], v[240:243], v[22:25]
	v_mfma_f32_16x16x32_bf16 v[14:17], v[160:163], v[244:247], v[14:17]
	v_mfma_f32_16x16x32_bf16 v[6:9], v[192:195], v[244:247], v[6:9]
	v_mfma_f32_16x16x32_bf16 v[58:61], v[200:203], v[216:219], v[58:61]
	v_mfma_f32_16x16x32_bf16 v[50:53], v[208:211], v[216:219], v[50:53]
	v_mfma_f32_16x16x32_bf16 v[42:45], v[200:203], v[220:223], v[42:45]
	v_mfma_f32_16x16x32_bf16 v[34:37], v[208:211], v[220:223], v[34:37]
	v_mfma_f32_16x16x32_bf16 v[26:29], v[200:203], v[232:235], v[26:29]
	v_mfma_f32_16x16x32_bf16 v[18:21], v[208:211], v[232:235], v[18:21]
	v_mfma_f32_16x16x32_bf16 v[10:13], v[200:203], v[236:239], v[10:13]
	v_mfma_f32_16x16x32_bf16 v[2:5], v[208:211], v[236:239], v[2:5]
	v_mfma_f32_16x16x32_bf16 v[58:61], v[204:207], v[224:227], v[58:61]
	v_mfma_f32_16x16x32_bf16 v[50:53], v[212:215], v[224:227], v[50:53]
	v_mfma_f32_16x16x32_bf16 v[42:45], v[204:207], v[228:231], v[42:45]
	v_mfma_f32_16x16x32_bf16 v[34:37], v[212:215], v[228:231], v[34:37]
	v_mfma_f32_16x16x32_bf16 v[26:29], v[204:207], v[240:243], v[26:29]
	v_mfma_f32_16x16x32_bf16 v[18:21], v[212:215], v[240:243], v[18:21]
	v_mfma_f32_16x16x32_bf16 v[10:13], v[204:207], v[244:247], v[10:13]
	v_mfma_f32_16x16x32_bf16 v[2:5], v[212:215], v[244:247], v[2:5]
	s_setprio 0
	s_barrier
	s_add_i32 s64, 0, 0x18000
	v_add_u32_e32 v142, s64, v170
	v_add_u32_e32 v160, s64, v174
	s_add_i32 s65, 0, 0x1c000
	ds_read_b128 v[156:159], v142
	ds_read_b128 v[160:163], v160
	ds_read_b128 v[164:167], v186
	ds_read_b128 v[192:195], v187
	v_add_u32_e32 v142, s65, v170
	v_add_u32_e32 v191, s65, v174
	ds_read_b128 v[200:203], v142
	ds_read_b128 v[204:207], v191
	ds_read_b128 v[208:211], v188
	ds_read_b128 v[212:215], v189
	s_mov_b32 m0, s49
	v_lshl_add_u64 v[248:249], s[44:45], 0, v[138:139]
	ds_read_b128 v[216:219], v184 offset:32768
	ds_read_b128 v[220:223], v184 offset:34816
	ds_read_b128 v[224:227], v185 offset:32768
	ds_read_b128 v[228:231], v185 offset:34816
	ds_read_b128 v[232:235], v184 offset:36864
	ds_read_b128 v[236:239], v184 offset:38912
	ds_read_b128 v[240:243], v185 offset:36864
	ds_read_b128 v[244:247], v185 offset:38912
	global_load_lds_dwordx4 v[248:249], off
	v_lshl_add_u64 v[248:249], s[44:45], 0, v[140:141]
	s_mov_b32 m0, s50
	s_nop 0
	global_load_lds_dwordx4 v[248:249], off
	s_waitcnt vmcnt(8)
	s_waitcnt lgkmcnt(0)
	s_barrier
	s_setprio 1
	v_mfma_f32_16x16x32_bf16 v[126:129], v[156:159], v[216:219], v[126:129]
	v_mfma_f32_16x16x32_bf16 v[118:121], v[164:167], v[216:219], v[118:121]
	v_mfma_f32_16x16x32_bf16 v[110:113], v[156:159], v[220:223], v[110:113]
	v_mfma_f32_16x16x32_bf16 v[102:105], v[164:167], v[220:223], v[102:105]
	v_mfma_f32_16x16x32_bf16 v[94:97], v[156:159], v[232:235], v[94:97]
	v_mfma_f32_16x16x32_bf16 v[86:89], v[164:167], v[232:235], v[86:89]
	v_mfma_f32_16x16x32_bf16 v[78:81], v[156:159], v[236:239], v[78:81]
	v_mfma_f32_16x16x32_bf16 v[70:73], v[164:167], v[236:239], v[70:73]
	v_mfma_f32_16x16x32_bf16 v[126:129], v[160:163], v[224:227], v[126:129]
	v_mfma_f32_16x16x32_bf16 v[118:121], v[192:195], v[224:227], v[118:121]
	v_mfma_f32_16x16x32_bf16 v[110:113], v[160:163], v[228:231], v[110:113]
	v_mfma_f32_16x16x32_bf16 v[102:105], v[192:195], v[228:231], v[102:105]
	v_mfma_f32_16x16x32_bf16 v[94:97], v[160:163], v[240:243], v[94:97]
	v_mfma_f32_16x16x32_bf16 v[86:89], v[192:195], v[240:243], v[86:89]
	v_mfma_f32_16x16x32_bf16 v[78:81], v[160:163], v[244:247], v[78:81]
	v_mfma_f32_16x16x32_bf16 v[70:73], v[192:195], v[244:247], v[70:73]
	v_mfma_f32_16x16x32_bf16 v[122:125], v[200:203], v[216:219], v[122:125]
	v_mfma_f32_16x16x32_bf16 v[114:117], v[208:211], v[216:219], v[114:117]
	v_mfma_f32_16x16x32_bf16 v[106:109], v[200:203], v[220:223], v[106:109]
	v_mfma_f32_16x16x32_bf16 v[98:101], v[208:211], v[220:223], v[98:101]
	v_mfma_f32_16x16x32_bf16 v[90:93], v[200:203], v[232:235], v[90:93]
	v_mfma_f32_16x16x32_bf16 v[82:85], v[208:211], v[232:235], v[82:85]
	v_mfma_f32_16x16x32_bf16 v[74:77], v[200:203], v[236:239], v[74:77]
	v_mfma_f32_16x16x32_bf16 v[66:69], v[208:211], v[236:239], v[66:69]
	v_mfma_f32_16x16x32_bf16 v[122:125], v[204:207], v[224:227], v[122:125]
	v_mfma_f32_16x16x32_bf16 v[114:117], v[212:215], v[224:227], v[114:117]
	v_mfma_f32_16x16x32_bf16 v[106:109], v[204:207], v[228:231], v[106:109]
	v_mfma_f32_16x16x32_bf16 v[98:101], v[212:215], v[228:231], v[98:101]
	v_mfma_f32_16x16x32_bf16 v[90:93], v[204:207], v[240:243], v[90:93]
	v_mfma_f32_16x16x32_bf16 v[82:85], v[212:215], v[240:243], v[82:85]
	v_mfma_f32_16x16x32_bf16 v[74:77], v[204:207], v[244:247], v[74:77]
	v_mfma_f32_16x16x32_bf16 v[66:69], v[212:215], v[244:247], v[66:69]
	s_setprio 0
	s_barrier
; #define PG8_STAGE(bufoff, gbase, voff) do { _Pragma("unroll") for (int _i = 0; _i < 2; ++_i) \
;         __builtin_amdgcn_global_load_lds((const unsigned*)((const char*)(gbase) + (voff)[_i]), (LAS unsigned*)(lds + (bufoff) + ldsw + _i * 8192), 16, 0, 0); } while (0)
; #define PG8_LDA(dst, b, h) do { _Pragma("unroll") for (int m = 0; m < 4; ++m) _Pragma("unroll") for (int k = 0; k < 2; ++k) dst[m][k] = *(const LAS bf16x8*)(lds + PG8_SA(b, h) + ((aoff ^ (k * 64)) + m * 2048)); } while (0)
; #define PG8_MMA(ai, bj, At, Bt) do { __builtin_amdgcn_s_setprio(1); _Pragma("unroll") for (int m = 0; m < 4; ++m) _Pragma("unroll") for (int n = 0; n < 2; ++n) _Pragma("unroll") for (int k = 0; k < 2; ++k) \
;         acc[ai][bj][m][n] = __builtin_amdgcn_mfma_f32_16x16x32_bf16(Bt[n][k], At[m][k], acc[ai][bj][m][n], 0, 0, 0); __builtin_amdgcn_s_setprio(0); } while (0)
; #define PG8_WAIT_V(n) asm volatile("s_waitcnt vmcnt(" #n ")" ::: "memory")
; #define PG8_WAIT_L(n) asm volatile("s_waitcnt lgkmcnt(" #n ")" ::: "memory")
; #define PG8_BAR __builtin_amdgcn_s_barrier()
; #define PG8_SCHED __builtin_amdgcn_sched_barrier(0)
;     ...
;             PG8_LDA(At, 1, 1); PG8_STAGE(PG8_SB(1, 0), b3, voffB); PG8_STAGE(PG8_SB(1, 1), b3 + hstep, voffB); PG8_STAGE(PG8_SA(1, 0), a3, vs[0]);
;             PG8_WAIT_V(8); PG8_WAIT_L(0); PG8_BAR; if (do1) { PG8_MMA(1, 0, At, B0); PG8_MMA(1, 1, At, B1); } PG8_BAR; PG8_SCHED;
;         }
	s_add_i32 s44, s64, s46
	v_lshl_add_u64 v[248:249], s[42:43], 0, v[130:131]
	s_mov_b32 m0, s44
	ds_read_b128 v[216:219], v184 offset:49152
	ds_read_b128 v[220:223], v184 offset:51200
	ds_read_b128 v[224:227], v185 offset:49152
	ds_read_b128 v[228:231], v185 offset:51200
	ds_read_b128 v[232:235], v184 offset:53248
	ds_read_b128 v[236:239], v184 offset:55296
	ds_read_b128 v[240:243], v185 offset:53248
	ds_read_b128 v[244:247], v185 offset:55296
	global_load_lds_dwordx4 v[248:249], off
	s_add_i32 m0, s44, 0x2000
	s_add_u32 s40, s40, 0x44000
	v_lshl_add_u64 v[248:249], s[42:43], 0, v[132:133]
	s_addc_u32 s41, s41, 0
	s_add_i32 s42, s65, s46
	global_load_lds_dwordx4 v[248:249], off
	v_lshl_add_u64 v[248:249], s[40:41], 0, v[130:131]
	s_mov_b32 m0, s42
	v_lshl_add_u64 v[168:169], v[168:169], 0, s[20:21]
	global_load_lds_dwordx4 v[248:249], off
	v_lshl_add_u64 v[248:249], s[40:41], 0, v[132:133]
	s_add_i32 m0, s42, 0x2000
	s_nop 0
	global_load_lds_dwordx4 v[248:249], off
	s_mov_b32 m0, s52
	s_nop 0
	global_load_lds_dwordx4 v[168:169], off
	v_lshl_add_u64 v[168:169], v[196:197], 0, s[20:21]
	s_mov_b32 m0, s53
	s_nop 0
	global_load_lds_dwordx4 v[168:169], off
	s_waitcnt vmcnt(8)
	s_waitcnt lgkmcnt(0)
	s_barrier
	s_setprio 1
	v_mfma_f32_16x16x32_bf16 v[62:65], v[156:159], v[216:219], v[62:65]
	v_mfma_f32_16x16x32_bf16 v[54:57], v[164:167], v[216:219], v[54:57]
	v_mfma_f32_16x16x32_bf16 v[46:49], v[156:159], v[220:223], v[46:49]
	v_mfma_f32_16x16x32_bf16 v[38:41], v[164:167], v[220:223], v[38:41]
	v_mfma_f32_16x16x32_bf16 v[30:33], v[156:159], v[232:235], v[30:33]
	v_mfma_f32_16x16x32_bf16 v[22:25], v[164:167], v[232:235], v[22:25]
	v_mfma_f32_16x16x32_bf16 v[14:17], v[156:159], v[236:239], v[14:17]
	v_mfma_f32_16x16x32_bf16 v[6:9], v[164:167], v[236:239], v[6:9]
	v_mfma_f32_16x16x32_bf16 v[62:65], v[160:163], v[224:227], v[62:65]
	v_mfma_f32_16x16x32_bf16 v[54:57], v[192:195], v[224:227], v[54:57]
	v_mfma_f32_16x16x32_bf16 v[46:49], v[160:163], v[228:231], v[46:49]
	v_mfma_f32_16x16x32_bf16 v[38:41], v[192:195], v[228:231], v[38:41]
	v_mfma_f32_16x16x32_bf16 v[30:33], v[160:163], v[240:243], v[30:33]
	v_mfma_f32_16x16x32_bf16 v[22:25], v[192:195], v[240:243], v[22:25]
	v_mfma_f32_16x16x32_bf16 v[14:17], v[160:163], v[244:247], v[14:17]
	v_mfma_f32_16x16x32_bf16 v[6:9], v[192:195], v[244:247], v[6:9]
	v_mfma_f32_16x16x32_bf16 v[58:61], v[200:203], v[216:219], v[58:61]
	v_mfma_f32_16x16x32_bf16 v[50:53], v[208:211], v[216:219], v[50:53]
	v_mfma_f32_16x16x32_bf16 v[42:45], v[200:203], v[220:223], v[42:45]
	v_mfma_f32_16x16x32_bf16 v[34:37], v[208:211], v[220:223], v[34:37]
	v_mfma_f32_16x16x32_bf16 v[26:29], v[200:203], v[232:235], v[26:29]
	v_mfma_f32_16x16x32_bf16 v[18:21], v[208:211], v[232:235], v[18:21]
	v_mfma_f32_16x16x32_bf16 v[10:13], v[200:203], v[236:239], v[10:13]
	v_mfma_f32_16x16x32_bf16 v[2:5], v[208:211], v[236:239], v[2:5]
	v_mfma_f32_16x16x32_bf16 v[58:61], v[204:207], v[224:227], v[58:61]
	v_mfma_f32_16x16x32_bf16 v[50:53], v[212:215], v[224:227], v[50:53]
	v_mfma_f32_16x16x32_bf16 v[42:45], v[204:207], v[228:231], v[42:45]
	v_mfma_f32_16x16x32_bf16 v[34:37], v[212:215], v[228:231], v[34:37]
	v_mfma_f32_16x16x32_bf16 v[26:29], v[204:207], v[240:243], v[26:29]
	v_mfma_f32_16x16x32_bf16 v[18:21], v[212:215], v[240:243], v[18:21]
	v_mfma_f32_16x16x32_bf16 v[10:13], v[204:207], v[244:247], v[10:13]
	v_mfma_f32_16x16x32_bf16 v[2:5], v[212:215], v[244:247], v[2:5]
	s_setprio 0
	s_barrier
	s_add_i32 s63, s63, 2
	s_add_u32 s31, s31, 0x8000
	s_addc_u32 s62, s62, 0
	s_add_u32 s38, s38, 0x100
	s_addc_u32 s39, s39, 0
	s_cmp_gt_u32 s63, 13
	s_cbranch_scc0 .LBB0_1257
	s_and_b64 vcc, exec, s[22:23]
	s_cbranch_vccz .LBB0_1260
	s_barrier

; #define PG8_STAGE(bufoff, gbase, voff) do { _Pragma("unroll") for (int _i = 0; _i < 2; ++_i) \
;         __builtin_amdgcn_global_load_lds((const unsigned*)((const char*)(gbase) + (voff)[_i]), (LAS unsigned*)(lds + (bufoff) + ldsw + _i * 8192), 16, 0, 0); } while (0)
; #define PG8_LDA(dst, b, h) do { _Pragma("unroll") for (int m = 0; m < 4; ++m) _Pragma("unroll") for (int k = 0; k < 2; ++k) dst[m][k] = *(const LAS bf16x8*)(lds + PG8_SA(b, h) + ((aoff ^ (k * 64)) + m * 2048)); } while (0)
; #define PG8_LDB(dst, b, h) do { _Pragma("unroll") for (int n = 0; n < 2; ++n) _Pragma("unroll") for (int k = 0; k < 2; ++k) dst[n][k] = *(const LAS bf16x8*)(lds + PG8_SB(b, h) + ((boff ^ (k * 64)) + n * 2048)); } while (0)
; #define PG8_MMA(ai, bj, At, Bt) do { __builtin_amdgcn_s_setprio(1); _Pragma("unroll") for (int m = 0; m < 4; ++m) _Pragma("unroll") for (int n = 0; n < 2; ++n) _Pragma("unroll") for (int k = 0; k < 2; ++k) \
;         acc[ai][bj][m][n] = __builtin_amdgcn_mfma_f32_16x16x32_bf16(Bt[n][k], At[m][k], acc[ai][bj][m][n], 0, 0, 0); __builtin_amdgcn_s_setprio(0); } while (0)
; #define PG8_WAIT_V(n) asm volatile("s_waitcnt vmcnt(" #n ")" ::: "memory")
; #define PG8_WAIT_L(n) asm volatile("s_waitcnt lgkmcnt(" #n ")" ::: "memory")
; #define PG8_BAR __builtin_amdgcn_s_barrier()
; #define PG8_SCHED __builtin_amdgcn_sched_barrier(0)
;     ...
;             PG8_LDB(B0, 0, 0); PG8_LDB(B1, 0, 1); PG8_SCHED; PG8_LDA(At, 0, 0); PG8_STAGE(PG8_SA(1, 1), a1, voffA[1]);
;             PG8_WAIT_V(8); PG8_WAIT_L(0); PG8_BAR; if (do0) { PG8_MMA(0, 0, At, B0); PG8_MMA(0, 1, At, B1); } PG8_BAR; PG8_SCHED;
;             PG8_LDA(At, 0, 1); PG8_STAGE(PG8_SB(0, 0), b2, voffB); PG8_STAGE(PG8_SB(0, 1), b2 + hstep, voffB); PG8_STAGE(PG8_SA(0, 0), a2, vs[0]);
;             PG8_WAIT_V(8); PG8_WAIT_L(0); PG8_BAR; if (do1) { PG8_MMA(1, 0, At, B0); PG8_MMA(1, 1, At, B1); } PG8_BAR; PG8_SCHED;
.LBB0_1343:
	v_add_u32_e32 v130, s92, v161
	v_add_u32_e32 v134, s92, v188
	v_add_u32_e32 v138, s93, v161
	v_add_u32_e32 v142, s93, v188
	v_add_u32_e32 v158, s62, v161
	ds_read_b128 v[130:133], v130
	ds_read_b128 v[134:137], v134
	ds_read_b128 v[138:141], v138
	ds_read_b128 v[142:145], v142
	v_add_u32_e32 v184, s62, v188
	ds_read_b128 v[180:183], v158
	ds_read_b128 v[200:203], v184
	v_add_u32_e32 v158, s63, v161
	s_add_u32 s56, s0, 0x4000
	v_add_u32_e32 v184, s63, v188
	ds_read_b128 v[204:207], v158
	ds_read_b128 v[208:211], v184
	s_addc_u32 s57, s1, 0
	s_cmp_eq_u32 s95, 12
	s_cselect_b32 s60, s23, s56
	s_cselect_b32 s61, s3, s57
	s_cselect_b32 s58, s47, s74
	s_cselect_b32 s59, s45, s94
	s_add_u32 s56, s60, 0x4000
	s_addc_u32 s57, s61, 0
	v_lshl_add_u64 v[184:185], s[0:1], 0, v[176:177]
	s_add_i32 m0, s55, 0xc000
	ds_read_b128 v[212:215], v193
	ds_read_b128 v[216:219], v193 offset:2048
	ds_read_b128 v[220:223], v194
	ds_read_b128 v[224:227], v194 offset:2048
	ds_read_b128 v[228:231], v193 offset:4096
	ds_read_b128 v[232:235], v193 offset:6144
	ds_read_b128 v[236:239], v194 offset:4096
	ds_read_b128 v[240:243], v194 offset:6144
	global_load_lds_dwordx4 v[184:185], off
	v_lshl_add_u64 v[184:185], s[0:1], 0, v[178:179]
	s_add_i32 m0, s55, 0xe000
	s_nop 0
	global_load_lds_dwordx4 v[184:185], off
	s_waitcnt vmcnt(8)
	s_waitcnt lgkmcnt(0)
	s_barrier
	s_setprio 1
	v_mfma_f32_16x16x32_bf16 v[126:129], v[130:133], v[212:215], v[126:129]
	v_mfma_f32_16x16x32_bf16 v[122:125], v[138:141], v[212:215], v[122:125]
	v_mfma_f32_16x16x32_bf16 v[94:97], v[130:133], v[216:219], v[94:97]
	v_mfma_f32_16x16x32_bf16 v[90:93], v[138:141], v[216:219], v[90:93]
	v_mfma_f32_16x16x32_bf16 v[62:65], v[130:133], v[228:231], v[62:65]
	v_mfma_f32_16x16x32_bf16 v[58:61], v[138:141], v[228:231], v[58:61]
	v_mfma_f32_16x16x32_bf16 v[30:33], v[130:133], v[232:235], v[30:33]
	v_mfma_f32_16x16x32_bf16 v[26:29], v[138:141], v[232:235], v[26:29]
	v_mfma_f32_16x16x32_bf16 v[126:129], v[134:137], v[220:223], v[126:129]
	v_mfma_f32_16x16x32_bf16 v[122:125], v[142:145], v[220:223], v[122:125]
	v_mfma_f32_16x16x32_bf16 v[94:97], v[134:137], v[224:227], v[94:97]
	v_mfma_f32_16x16x32_bf16 v[90:93], v[142:145], v[224:227], v[90:93]
	v_mfma_f32_16x16x32_bf16 v[62:65], v[134:137], v[236:239], v[62:65]
	v_mfma_f32_16x16x32_bf16 v[58:61], v[142:145], v[236:239], v[58:61]
	v_mfma_f32_16x16x32_bf16 v[30:33], v[134:137], v[240:243], v[30:33]
	v_mfma_f32_16x16x32_bf16 v[26:29], v[142:145], v[240:243], v[26:29]
	v_mfma_f32_16x16x32_bf16 v[110:113], v[180:183], v[212:215], v[110:113]
	v_mfma_f32_16x16x32_bf16 v[106:109], v[204:207], v[212:215], v[106:109]
	v_mfma_f32_16x16x32_bf16 v[78:81], v[180:183], v[216:219], v[78:81]
	v_mfma_f32_16x16x32_bf16 v[74:77], v[204:207], v[216:219], v[74:77]
	v_mfma_f32_16x16x32_bf16 v[46:49], v[180:183], v[228:231], v[46:49]
	v_mfma_f32_16x16x32_bf16 v[42:45], v[204:207], v[228:231], v[42:45]
	v_mfma_f32_16x16x32_bf16 v[14:17], v[180:183], v[232:235], v[14:17]
	v_mfma_f32_16x16x32_bf16 v[10:13], v[204:207], v[232:235], v[10:13]
	v_mfma_f32_16x16x32_bf16 v[110:113], v[200:203], v[220:223], v[110:113]
	v_mfma_f32_16x16x32_bf16 v[106:109], v[208:211], v[220:223], v[106:109]
	v_mfma_f32_16x16x32_bf16 v[78:81], v[200:203], v[224:227], v[78:81]
	v_mfma_f32_16x16x32_bf16 v[74:77], v[208:211], v[224:227], v[74:77]
	v_mfma_f32_16x16x32_bf16 v[46:49], v[200:203], v[236:239], v[46:49]
	v_mfma_f32_16x16x32_bf16 v[42:45], v[208:211], v[236:239], v[42:45]
	v_mfma_f32_16x16x32_bf16 v[14:17], v[200:203], v[240:243], v[14:17]
	v_mfma_f32_16x16x32_bf16 v[10:13], v[208:211], v[240:243], v[10:13]
	s_setprio 0
	s_barrier
	s_add_i32 vcc_lo, s92, s64
	v_lshl_add_u64 v[184:185], s[58:59], 0, v[146:147]
	s_mov_b32 m0, vcc_lo
	ds_read_b128 v[212:215], v193 offset:16384
	ds_read_b128 v[216:219], v193 offset:18432
	ds_read_b128 v[220:223], v194 offset:16384
	ds_read_b128 v[224:227], v194 offset:18432
	ds_read_b128 v[228:231], v193 offset:20480
	ds_read_b128 v[232:235], v193 offset:22528
	ds_read_b128 v[236:239], v194 offset:20480
	ds_read_b128 v[240:243], v194 offset:22528
	global_load_lds_dwordx4 v[184:185], off
	s_add_i32 m0, vcc_lo, 0x2000
	s_add_u32 vcc_lo, s58, 0x40000
	v_lshl_add_u64 v[196:197], s[58:59], 0, v[148:149]
	s_addc_u32 vcc_hi, s59, 0
	s_add_i32 s18, s62, s64
	global_load_lds_dwordx4 v[196:197], off
	v_lshl_add_u64 v[244:245], vcc, 0, v[146:147]
	s_mov_b32 m0, s18
	s_nop 0
	global_load_lds_dwordx4 v[244:245], off
	v_lshl_add_u64 v[244:245], vcc, 0, v[148:149]
	s_add_i32 m0, s18, 0x2000
	s_nop 0
	global_load_lds_dwordx4 v[244:245], off
	v_lshl_add_u64 v[244:245], s[60:61], 0, v[150:151]
	s_mov_b32 m0, s55
	s_nop 0
	global_load_lds_dwordx4 v[244:245], off
	v_lshl_add_u64 v[244:245], s[60:61], 0, v[152:153]
	s_mov_b32 m0, s65
	s_nop 0
	global_load_lds_dwordx4 v[244:245], off
	s_waitcnt vmcnt(8)
	s_waitcnt lgkmcnt(0)
	s_barrier
; #define PG8_STAGE(bufoff, gbase, voff) do { _Pragma("unroll") for (int _i = 0; _i < 2; ++_i) \
;         __builtin_amdgcn_global_load_lds((const unsigned*)((const char*)(gbase) + (voff)[_i]), (LAS unsigned*)(lds + (bufoff) + ldsw + _i * 8192), 16, 0, 0); } while (0)
; #define PG8_LDA(dst, b, h) do { _Pragma("unroll") for (int m = 0; m < 4; ++m) _Pragma("unroll") for (int k = 0; k < 2; ++k) dst[m][k] = *(const LAS bf16x8*)(lds + PG8_SA(b, h) + ((aoff ^ (k * 64)) + m * 2048)); } while (0)
; #define PG8_LDB(dst, b, h) do { _Pragma("unroll") for (int n = 0; n < 2; ++n) _Pragma("unroll") for (int k = 0; k < 2; ++k) dst[n][k] = *(const LAS bf16x8*)(lds + PG8_SB(b, h) + ((boff ^ (k * 64)) + n * 2048)); } while (0)
; #define PG8_MMA(ai, bj, At, Bt) do { __builtin_amdgcn_s_setprio(1); _Pragma("unroll") for (int m = 0; m < 4; ++m) _Pragma("unroll") for (int n = 0; n < 2; ++n) _Pragma("unroll") for (int k = 0; k < 2; ++k) \
;         acc[ai][bj][m][n] = __builtin_amdgcn_mfma_f32_16x16x32_bf16(Bt[n][k], At[m][k], acc[ai][bj][m][n], 0, 0, 0); __builtin_amdgcn_s_setprio(0); } while (0)
; #define PG8_WAIT_V(n) asm volatile("s_waitcnt vmcnt(" #n ")" ::: "memory")
; #define PG8_WAIT_L(n) asm volatile("s_waitcnt lgkmcnt(" #n ")" ::: "memory")
; #define PG8_BAR __builtin_amdgcn_s_barrier()
; #define PG8_SCHED __builtin_amdgcn_sched_barrier(0)
;     ...
;             PG8_WAIT_V(8); PG8_WAIT_L(0); PG8_BAR; if (do1) { PG8_MMA(1, 0, At, B0); PG8_MMA(1, 1, At, B1); } PG8_BAR; PG8_SCHED;
;             PG8_LDB(B0, 1, 0); PG8_LDB(B1, 1, 1); PG8_SCHED; PG8_LDA(At, 1, 0); PG8_STAGE(PG8_SA(0, 1), a2, vs[1]);
;             PG8_WAIT_V(8); PG8_WAIT_L(0); PG8_BAR; if (do0) { PG8_MMA(0, 0, At, B0); PG8_MMA(0, 1, At, B1); } PG8_BAR; PG8_SCHED;
	s_setprio 1
	v_mfma_f32_16x16x32_bf16 v[118:121], v[130:133], v[212:215], v[118:121]
	v_mfma_f32_16x16x32_bf16 v[114:117], v[138:141], v[212:215], v[114:117]
	v_mfma_f32_16x16x32_bf16 v[86:89], v[130:133], v[216:219], v[86:89]
	v_mfma_f32_16x16x32_bf16 v[82:85], v[138:141], v[216:219], v[82:85]
	v_mfma_f32_16x16x32_bf16 v[54:57], v[130:133], v[228:231], v[54:57]
	v_mfma_f32_16x16x32_bf16 v[50:53], v[138:141], v[228:231], v[50:53]
	v_mfma_f32_16x16x32_bf16 v[22:25], v[130:133], v[232:235], v[22:25]
	v_mfma_f32_16x16x32_bf16 v[18:21], v[138:141], v[232:235], v[18:21]
	v_mfma_f32_16x16x32_bf16 v[118:121], v[134:137], v[220:223], v[118:121]
	v_mfma_f32_16x16x32_bf16 v[114:117], v[142:145], v[220:223], v[114:117]
	v_mfma_f32_16x16x32_bf16 v[86:89], v[134:137], v[224:227], v[86:89]
	v_mfma_f32_16x16x32_bf16 v[82:85], v[142:145], v[224:227], v[82:85]
	v_mfma_f32_16x16x32_bf16 v[54:57], v[134:137], v[236:239], v[54:57]
	v_mfma_f32_16x16x32_bf16 v[50:53], v[142:145], v[236:239], v[50:53]
	v_mfma_f32_16x16x32_bf16 v[22:25], v[134:137], v[240:243], v[22:25]
	v_mfma_f32_16x16x32_bf16 v[18:21], v[142:145], v[240:243], v[18:21]
	v_mfma_f32_16x16x32_bf16 v[102:105], v[180:183], v[212:215], v[102:105]
	v_mfma_f32_16x16x32_bf16 v[98:101], v[204:207], v[212:215], v[98:101]
	v_mfma_f32_16x16x32_bf16 v[70:73], v[180:183], v[216:219], v[70:73]
	v_mfma_f32_16x16x32_bf16 v[66:69], v[204:207], v[216:219], v[66:69]
	v_mfma_f32_16x16x32_bf16 v[38:41], v[180:183], v[228:231], v[38:41]
	v_mfma_f32_16x16x32_bf16 v[34:37], v[204:207], v[228:231], v[34:37]
	v_mfma_f32_16x16x32_bf16 v[6:9], v[180:183], v[232:235], v[6:9]
	v_mfma_f32_16x16x32_bf16 v[2:5], v[204:207], v[232:235], v[2:5]
	v_mfma_f32_16x16x32_bf16 v[102:105], v[200:203], v[220:223], v[102:105]
	v_mfma_f32_16x16x32_bf16 v[98:101], v[208:211], v[220:223], v[98:101]
	v_mfma_f32_16x16x32_bf16 v[70:73], v[200:203], v[224:227], v[70:73]
	v_mfma_f32_16x16x32_bf16 v[66:69], v[208:211], v[224:227], v[66:69]
	v_mfma_f32_16x16x32_bf16 v[38:41], v[200:203], v[236:239], v[38:41]
	v_mfma_f32_16x16x32_bf16 v[34:37], v[208:211], v[236:239], v[34:37]
	v_mfma_f32_16x16x32_bf16 v[6:9], v[200:203], v[240:243], v[6:9]
	v_mfma_f32_16x16x32_bf16 v[2:5], v[208:211], v[240:243], v[2:5]
	s_setprio 0
	s_barrier
	s_add_i32 s18, 0, 0x18000
	s_add_i32 s19, 0, 0x1c000
	v_add_u32_e32 v130, s18, v161
	v_add_u32_e32 v134, s18, v188
	v_add_u32_e32 v138, s72, v161
	v_add_u32_e32 v142, s72, v188
	v_add_u32_e32 v158, s19, v161
	ds_read_b128 v[130:133], v130
	ds_read_b128 v[134:137], v134
	ds_read_b128 v[138:141], v138
	ds_read_b128 v[142:145], v142
	v_add_u32_e32 v195, s19, v188
	ds_read_b128 v[180:183], v158
	ds_read_b128 v[200:203], v195
	v_add_u32_e32 v158, s73, v161
	v_add_u32_e32 v195, s73, v188
	ds_read_b128 v[204:207], v158
	ds_read_b128 v[208:211], v195
	s_mov_b32 m0, s66
	v_lshl_add_u64 v[244:245], s[60:61], 0, v[154:155]
	ds_read_b128 v[212:215], v193 offset:32768
	ds_read_b128 v[216:219], v193 offset:34816
	ds_read_b128 v[220:223], v194 offset:32768
	ds_read_b128 v[224:227], v194 offset:34816
	ds_read_b128 v[228:231], v193 offset:36864
	ds_read_b128 v[232:235], v193 offset:38912
	ds_read_b128 v[236:239], v194 offset:36864
	ds_read_b128 v[240:243], v194 offset:38912
	global_load_lds_dwordx4 v[244:245], off
	v_lshl_add_u64 v[244:245], s[60:61], 0, v[156:157]
	s_mov_b32 m0, s67
	s_nop 0
	global_load_lds_dwordx4 v[244:245], off
	s_waitcnt vmcnt(8)
	s_waitcnt lgkmcnt(0)
	s_barrier
	s_setprio 1
	v_mfma_f32_16x16x32_bf16 v[126:129], v[130:133], v[212:215], v[126:129]
	v_mfma_f32_16x16x32_bf16 v[122:125], v[138:141], v[212:215], v[122:125]
	v_mfma_f32_16x16x32_bf16 v[94:97], v[130:133], v[216:219], v[94:97]
	v_mfma_f32_16x16x32_bf16 v[90:93], v[138:141], v[216:219], v[90:93]
	v_mfma_f32_16x16x32_bf16 v[62:65], v[130:133], v[228:231], v[62:65]
	v_mfma_f32_16x16x32_bf16 v[58:61], v[138:141], v[228:231], v[58:61]
	v_mfma_f32_16x16x32_bf16 v[30:33], v[130:133], v[232:235], v[30:33]
	v_mfma_f32_16x16x32_bf16 v[26:29], v[138:141], v[232:235], v[26:29]
	v_mfma_f32_16x16x32_bf16 v[126:129], v[134:137], v[220:223], v[126:129]
	v_mfma_f32_16x16x32_bf16 v[122:125], v[142:145], v[220:223], v[122:125]
	v_mfma_f32_16x16x32_bf16 v[94:97], v[134:137], v[224:227], v[94:97]
	v_mfma_f32_16x16x32_bf16 v[90:93], v[142:145], v[224:227], v[90:93]
	v_mfma_f32_16x16x32_bf16 v[62:65], v[134:137], v[236:239], v[62:65]
	v_mfma_f32_16x16x32_bf16 v[58:61], v[142:145], v[236:239], v[58:61]
	v_mfma_f32_16x16x32_bf16 v[30:33], v[134:137], v[240:243], v[30:33]
	v_mfma_f32_16x16x32_bf16 v[26:29], v[142:145], v[240:243], v[26:29]
	v_mfma_f32_16x16x32_bf16 v[110:113], v[180:183], v[212:215], v[110:113]
	v_mfma_f32_16x16x32_bf16 v[106:109], v[204:207], v[212:215], v[106:109]
	v_mfma_f32_16x16x32_bf16 v[78:81], v[180:183], v[216:219], v[78:81]
	v_mfma_f32_16x16x32_bf16 v[74:77], v[204:207], v[216:219], v[74:77]
	v_mfma_f32_16x16x32_bf16 v[46:49], v[180:183], v[228:231], v[46:49]
	v_mfma_f32_16x16x32_bf16 v[42:45], v[204:207], v[228:231], v[42:45]
	v_mfma_f32_16x16x32_bf16 v[14:17], v[180:183], v[232:235], v[14:17]
	v_mfma_f32_16x16x32_bf16 v[10:13], v[204:207], v[232:235], v[10:13]
	v_mfma_f32_16x16x32_bf16 v[110:113], v[200:203], v[220:223], v[110:113]
	v_mfma_f32_16x16x32_bf16 v[106:109], v[208:211], v[220:223], v[106:109]
	v_mfma_f32_16x16x32_bf16 v[78:81], v[200:203], v[224:227], v[78:81]
	v_mfma_f32_16x16x32_bf16 v[74:77], v[208:211], v[224:227], v[74:77]
	v_mfma_f32_16x16x32_bf16 v[46:49], v[200:203], v[236:239], v[46:49]
	v_mfma_f32_16x16x32_bf16 v[42:45], v[208:211], v[236:239], v[42:45]
	v_mfma_f32_16x16x32_bf16 v[14:17], v[200:203], v[240:243], v[14:17]
	v_mfma_f32_16x16x32_bf16 v[10:13], v[208:211], v[240:243], v[10:13]
	s_setprio 0
	s_barrier
; #define PG8_STAGE(bufoff, gbase, voff) do { _Pragma("unroll") for (int _i = 0; _i < 2; ++_i) \
;         __builtin_amdgcn_global_load_lds((const unsigned*)((const char*)(gbase) + (voff)[_i]), (LAS unsigned*)(lds + (bufoff) + ldsw + _i * 8192), 16, 0, 0); } while (0)
; #define PG8_LDA(dst, b, h) do { _Pragma("unroll") for (int m = 0; m < 4; ++m) _Pragma("unroll") for (int k = 0; k < 2; ++k) dst[m][k] = *(const LAS bf16x8*)(lds + PG8_SA(b, h) + ((aoff ^ (k * 64)) + m * 2048)); } while (0)
; #define PG8_MMA(ai, bj, At, Bt) do { __builtin_amdgcn_s_setprio(1); _Pragma("unroll") for (int m = 0; m < 4; ++m) _Pragma("unroll") for (int n = 0; n < 2; ++n) _Pragma("unroll") for (int k = 0; k < 2; ++k) \
;         acc[ai][bj][m][n] = __builtin_amdgcn_mfma_f32_16x16x32_bf16(Bt[n][k], At[m][k], acc[ai][bj][m][n], 0, 0, 0); __builtin_amdgcn_s_setprio(0); } while (0)
; #define PG8_WAIT_V(n) asm volatile("s_waitcnt vmcnt(" #n ")" ::: "memory")
; #define PG8_WAIT_L(n) asm volatile("s_waitcnt lgkmcnt(" #n ")" ::: "memory")
; #define PG8_BAR __builtin_amdgcn_s_barrier()
; #define PG8_SCHED __builtin_amdgcn_sched_barrier(0)
;     ...
;             PG8_LDA(At, 1, 1); PG8_STAGE(PG8_SB(1, 0), b3, voffB); PG8_STAGE(PG8_SB(1, 1), b3 + hstep, voffB); PG8_STAGE(PG8_SA(1, 0), a3, vs[0]);
;             PG8_WAIT_V(8); PG8_WAIT_L(0); PG8_BAR; if (do1) { PG8_MMA(1, 0, At, B0); PG8_MMA(1, 1, At, B1); } PG8_BAR; PG8_SCHED;
;         }
	s_add_i32 s18, s18, s64
	v_lshl_add_u64 v[184:185], v[184:185], 0, s[10:11]
	s_mov_b32 m0, s18
	ds_read_b128 v[212:215], v193 offset:49152
	ds_read_b128 v[216:219], v193 offset:51200
	ds_read_b128 v[220:223], v194 offset:49152
	ds_read_b128 v[224:227], v194 offset:51200
	ds_read_b128 v[228:231], v193 offset:53248
	ds_read_b128 v[232:235], v193 offset:55296
	ds_read_b128 v[236:239], v194 offset:53248
	ds_read_b128 v[240:243], v194 offset:55296
	global_load_lds_dwordx4 v[184:185], off
	s_add_i32 m0, s18, 0x2000
	s_add_u32 s58, s58, 0x40080
	v_lshl_add_u64 v[184:185], v[196:197], 0, s[10:11]
	s_addc_u32 s59, s59, 0
	s_add_i32 s18, s19, s64
	global_load_lds_dwordx4 v[184:185], off
	v_lshl_add_u64 v[184:185], s[58:59], 0, v[146:147]
	s_mov_b32 m0, s18
	s_nop 0
	global_load_lds_dwordx4 v[184:185], off
	v_lshl_add_u64 v[184:185], s[58:59], 0, v[148:149]
	s_add_i32 m0, s18, 0x2000
	s_nop 0
	global_load_lds_dwordx4 v[184:185], off
	v_lshl_add_u64 v[184:185], s[56:57], 0, v[150:151]
	s_mov_b32 m0, s70
	s_nop 0
	global_load_lds_dwordx4 v[184:185], off
	v_lshl_add_u64 v[184:185], s[56:57], 0, v[152:153]
	s_mov_b32 m0, s71
	s_nop 0
	global_load_lds_dwordx4 v[184:185], off
	s_waitcnt vmcnt(8)
	s_waitcnt lgkmcnt(0)
	s_barrier
	s_setprio 1
	v_mfma_f32_16x16x32_bf16 v[118:121], v[130:133], v[212:215], v[118:121]
	v_mfma_f32_16x16x32_bf16 v[114:117], v[138:141], v[212:215], v[114:117]
	v_mfma_f32_16x16x32_bf16 v[86:89], v[130:133], v[216:219], v[86:89]
	v_mfma_f32_16x16x32_bf16 v[82:85], v[138:141], v[216:219], v[82:85]
	v_mfma_f32_16x16x32_bf16 v[54:57], v[130:133], v[228:231], v[54:57]
	v_mfma_f32_16x16x32_bf16 v[50:53], v[138:141], v[228:231], v[50:53]
	v_mfma_f32_16x16x32_bf16 v[22:25], v[130:133], v[232:235], v[22:25]
	v_mfma_f32_16x16x32_bf16 v[18:21], v[138:141], v[232:235], v[18:21]
	v_mfma_f32_16x16x32_bf16 v[118:121], v[134:137], v[220:223], v[118:121]
	v_mfma_f32_16x16x32_bf16 v[114:117], v[142:145], v[220:223], v[114:117]
	v_mfma_f32_16x16x32_bf16 v[86:89], v[134:137], v[224:227], v[86:89]
	v_mfma_f32_16x16x32_bf16 v[82:85], v[142:145], v[224:227], v[82:85]
	v_mfma_f32_16x16x32_bf16 v[54:57], v[134:137], v[236:239], v[54:57]
	v_mfma_f32_16x16x32_bf16 v[50:53], v[142:145], v[236:239], v[50:53]
	v_mfma_f32_16x16x32_bf16 v[22:25], v[134:137], v[240:243], v[22:25]
	v_mfma_f32_16x16x32_bf16 v[18:21], v[142:145], v[240:243], v[18:21]
	v_mfma_f32_16x16x32_bf16 v[102:105], v[180:183], v[212:215], v[102:105]
	v_mfma_f32_16x16x32_bf16 v[98:101], v[204:207], v[212:215], v[98:101]
	v_mfma_f32_16x16x32_bf16 v[70:73], v[180:183], v[216:219], v[70:73]
	v_mfma_f32_16x16x32_bf16 v[66:69], v[204:207], v[216:219], v[66:69]
	v_mfma_f32_16x16x32_bf16 v[38:41], v[180:183], v[228:231], v[38:41]
	v_mfma_f32_16x16x32_bf16 v[34:37], v[204:207], v[228:231], v[34:37]
	v_mfma_f32_16x16x32_bf16 v[6:9], v[180:183], v[232:235], v[6:9]
	v_mfma_f32_16x16x32_bf16 v[2:5], v[204:207], v[232:235], v[2:5]
	v_mfma_f32_16x16x32_bf16 v[102:105], v[200:203], v[220:223], v[102:105]
	v_mfma_f32_16x16x32_bf16 v[98:101], v[208:211], v[220:223], v[98:101]
	v_mfma_f32_16x16x32_bf16 v[70:73], v[200:203], v[224:227], v[70:73]
	v_mfma_f32_16x16x32_bf16 v[66:69], v[208:211], v[224:227], v[66:69]
	v_mfma_f32_16x16x32_bf16 v[38:41], v[200:203], v[236:239], v[38:41]
	v_mfma_f32_16x16x32_bf16 v[34:37], v[208:211], v[236:239], v[34:37]
	v_mfma_f32_16x16x32_bf16 v[6:9], v[200:203], v[240:243], v[6:9]
	v_mfma_f32_16x16x32_bf16 v[2:5], v[208:211], v[240:243], v[2:5]
	s_setprio 0
	s_barrier
	s_add_i32 s95, s95, 2
	s_add_u32 s74, s74, 0x100
	s_addc_u32 s94, s94, 0
	s_add_u32 s0, s0, 0x8000
	s_addc_u32 s1, s1, 0
	s_cmp_gt_u32 s95, 13
	s_cbranch_scc0 .LBB0_1343
	s_and_b64 vcc, exec, s[12:13]
	s_cbranch_vccz .LBB0_1346
	s_barrier

; #define PG8_STAGE(bufoff, gbase, voff) do { _Pragma("unroll") for (int _i = 0; _i < 2; ++_i) \
;         __builtin_amdgcn_global_load_lds((const unsigned*)((const char*)(gbase) + (voff)[_i]), (LAS unsigned*)(lds + (bufoff) + ldsw + _i * 8192), 16, 0, 0); } while (0)
; #define PG8_LDA(dst, b, h) do { _Pragma("unroll") for (int m = 0; m < 4; ++m) _Pragma("unroll") for (int k = 0; k < 2; ++k) dst[m][k] = *(const LAS bf16x8*)(lds + PG8_SA(b, h) + ((aoff ^ (k * 64)) + m * 2048)); } while (0)
; #define PG8_LDB(dst, b, h) do { _Pragma("unroll") for (int n = 0; n < 2; ++n) _Pragma("unroll") for (int k = 0; k < 2; ++k) dst[n][k] = *(const LAS bf16x8*)(lds + PG8_SB(b, h) + ((boff ^ (k * 64)) + n * 2048)); } while (0)
; #define PG8_MMA(ai, bj, At, Bt) do { __builtin_amdgcn_s_setprio(1); _Pragma("unroll") for (int m = 0; m < 4; ++m) _Pragma("unroll") for (int n = 0; n < 2; ++n) _Pragma("unroll") for (int k = 0; k < 2; ++k) \
;         acc[ai][bj][m][n] = __builtin_amdgcn_mfma_f32_16x16x32_bf16(Bt[n][k], At[m][k], acc[ai][bj][m][n], 0, 0, 0); __builtin_amdgcn_s_setprio(0); } while (0)
; #define PG8_WAIT_V(n) asm volatile("s_waitcnt vmcnt(" #n ")" ::: "memory")
; #define PG8_WAIT_L(n) asm volatile("s_waitcnt lgkmcnt(" #n ")" ::: "memory")
; #define PG8_BAR __builtin_amdgcn_s_barrier()
; #define PG8_SCHED __builtin_amdgcn_sched_barrier(0)
;     ...
;             PG8_LDB(B0, 0, 0); PG8_LDB(B1, 0, 1); PG8_SCHED; PG8_LDA(At, 0, 0); PG8_STAGE(PG8_SA(1, 1), a1, voffA[1]);
;             PG8_WAIT_V(8); PG8_WAIT_L(0); PG8_BAR; if (do0) { PG8_MMA(0, 0, At, B0); PG8_MMA(0, 1, At, B1); } PG8_BAR; PG8_SCHED;
;             PG8_LDA(At, 0, 1); PG8_STAGE(PG8_SB(0, 0), b2, voffB); PG8_STAGE(PG8_SB(0, 1), b2 + hstep, voffB); PG8_STAGE(PG8_SA(0, 0), a2, vs[0]);
;             PG8_WAIT_V(8); PG8_WAIT_L(0); PG8_BAR; if (do1) { PG8_MMA(1, 0, At, B0); PG8_MMA(1, 1, At, B1); } PG8_BAR; PG8_SCHED;
.LBB0_1498:
	v_add_u32_e32 v130, s70, v153
	v_add_u32_e32 v134, s70, v184
	v_add_u32_e32 v150, s71, v153
	v_add_u32_e32 v176, s71, v184
	ds_read_b128 v[130:133], v130
	ds_read_b128 v[134:137], v134
	ds_read_b128 v[172:175], v150
	ds_read_b128 v[176:179], v176
	v_add_u32_e32 v150, s92, v153
	v_add_u32_e32 v180, s92, v184
	ds_read_b128 v[192:195], v150
	ds_read_b128 v[200:203], v180
	v_add_u32_e32 v150, s93, v153
	s_add_u32 s6, s0, 0x4000
	v_add_u32_e32 v180, s93, v184
	ds_read_b128 v[204:207], v150
	ds_read_b128 v[208:211], v180
	s_addc_u32 s7, s1, 0
	s_cmp_eq_u32 s63, 12
	s_cselect_b32 s58, s9, s6
	s_cselect_b32 s59, s3, s7
	s_cselect_b32 s56, s37, s49
	s_cselect_b32 s57, s23, s62
	s_add_u32 s6, s58, 0x4000
	s_addc_u32 s7, s59, 0
	v_lshl_add_u64 v[180:181], s[0:1], 0, v[168:169]
	s_add_i32 m0, s61, 0xc000
	ds_read_b128 v[212:215], v189
	ds_read_b128 v[216:219], v189 offset:2048
	ds_read_b128 v[220:223], v190
	ds_read_b128 v[224:227], v190 offset:2048
	ds_read_b128 v[228:231], v189 offset:4096
	ds_read_b128 v[232:235], v189 offset:6144
	ds_read_b128 v[236:239], v190 offset:4096
	ds_read_b128 v[240:243], v190 offset:6144
	global_load_lds_dwordx4 v[180:181], off
	v_lshl_add_u64 v[180:181], s[0:1], 0, v[170:171]
	s_add_i32 m0, s61, 0xe000
	s_nop 0
	global_load_lds_dwordx4 v[180:181], off
	s_waitcnt vmcnt(8)
	s_waitcnt lgkmcnt(0)
	s_barrier
	s_setprio 1
	v_mfma_f32_16x16x32_bf16 v[126:129], v[130:133], v[212:215], v[126:129]
	v_mfma_f32_16x16x32_bf16 v[122:125], v[172:175], v[212:215], v[122:125]
	v_mfma_f32_16x16x32_bf16 v[94:97], v[130:133], v[216:219], v[94:97]
	v_mfma_f32_16x16x32_bf16 v[90:93], v[172:175], v[216:219], v[90:93]
	v_mfma_f32_16x16x32_bf16 v[62:65], v[130:133], v[228:231], v[62:65]
	v_mfma_f32_16x16x32_bf16 v[58:61], v[172:175], v[228:231], v[58:61]
	v_mfma_f32_16x16x32_bf16 v[30:33], v[130:133], v[232:235], v[30:33]
	v_mfma_f32_16x16x32_bf16 v[26:29], v[172:175], v[232:235], v[26:29]
	v_mfma_f32_16x16x32_bf16 v[126:129], v[134:137], v[220:223], v[126:129]
	v_mfma_f32_16x16x32_bf16 v[122:125], v[176:179], v[220:223], v[122:125]
	v_mfma_f32_16x16x32_bf16 v[94:97], v[134:137], v[224:227], v[94:97]
	v_mfma_f32_16x16x32_bf16 v[90:93], v[176:179], v[224:227], v[90:93]
	v_mfma_f32_16x16x32_bf16 v[62:65], v[134:137], v[236:239], v[62:65]
	v_mfma_f32_16x16x32_bf16 v[58:61], v[176:179], v[236:239], v[58:61]
	v_mfma_f32_16x16x32_bf16 v[30:33], v[134:137], v[240:243], v[30:33]
	v_mfma_f32_16x16x32_bf16 v[26:29], v[176:179], v[240:243], v[26:29]
	v_mfma_f32_16x16x32_bf16 v[110:113], v[192:195], v[212:215], v[110:113]
	v_mfma_f32_16x16x32_bf16 v[106:109], v[204:207], v[212:215], v[106:109]
	v_mfma_f32_16x16x32_bf16 v[78:81], v[192:195], v[216:219], v[78:81]
	v_mfma_f32_16x16x32_bf16 v[74:77], v[204:207], v[216:219], v[74:77]
	v_mfma_f32_16x16x32_bf16 v[46:49], v[192:195], v[228:231], v[46:49]
	v_mfma_f32_16x16x32_bf16 v[42:45], v[204:207], v[228:231], v[42:45]
	v_mfma_f32_16x16x32_bf16 v[14:17], v[192:195], v[232:235], v[14:17]
	v_mfma_f32_16x16x32_bf16 v[10:13], v[204:207], v[232:235], v[10:13]
	v_mfma_f32_16x16x32_bf16 v[110:113], v[200:203], v[220:223], v[110:113]
	v_mfma_f32_16x16x32_bf16 v[106:109], v[208:211], v[220:223], v[106:109]
	v_mfma_f32_16x16x32_bf16 v[78:81], v[200:203], v[224:227], v[78:81]
	v_mfma_f32_16x16x32_bf16 v[74:77], v[208:211], v[224:227], v[74:77]
	v_mfma_f32_16x16x32_bf16 v[46:49], v[200:203], v[236:239], v[46:49]
	v_mfma_f32_16x16x32_bf16 v[42:45], v[208:211], v[236:239], v[42:45]
	v_mfma_f32_16x16x32_bf16 v[14:17], v[200:203], v[240:243], v[14:17]
	v_mfma_f32_16x16x32_bf16 v[10:13], v[208:211], v[240:243], v[10:13]
	s_setprio 0
	s_barrier
	s_add_i32 s18, s70, s60
	v_lshl_add_u64 v[180:181], s[56:57], 0, v[138:139]
	s_mov_b32 m0, s18
	ds_read_b128 v[212:215], v189 offset:16384
	ds_read_b128 v[216:219], v189 offset:18432
	ds_read_b128 v[220:223], v190 offset:16384
	ds_read_b128 v[224:227], v190 offset:18432
	ds_read_b128 v[228:231], v189 offset:20480
	ds_read_b128 v[232:235], v189 offset:22528
	ds_read_b128 v[236:239], v190 offset:20480
	ds_read_b128 v[240:243], v190 offset:22528
	global_load_lds_dwordx4 v[180:181], off
	s_add_i32 m0, s18, 0x2000
	s_add_u32 s72, s56, 0x40000
	v_lshl_add_u64 v[196:197], s[56:57], 0, v[140:141]
	s_addc_u32 s73, s57, 0
	s_add_i32 s18, s92, s60
	global_load_lds_dwordx4 v[196:197], off
	v_lshl_add_u64 v[244:245], s[72:73], 0, v[138:139]
	s_mov_b32 m0, s18
	s_nop 0
	global_load_lds_dwordx4 v[244:245], off
	v_lshl_add_u64 v[244:245], s[72:73], 0, v[140:141]
	s_add_i32 m0, s18, 0x2000
	s_nop 0
	global_load_lds_dwordx4 v[244:245], off
	v_lshl_add_u64 v[244:245], s[58:59], 0, v[142:143]
	s_mov_b32 m0, s61
	s_nop 0
	global_load_lds_dwordx4 v[244:245], off
	v_lshl_add_u64 v[244:245], s[58:59], 0, v[144:145]
	s_mov_b32 m0, s64
	s_nop 0
	global_load_lds_dwordx4 v[244:245], off
	s_waitcnt vmcnt(8)
	s_waitcnt lgkmcnt(0)
	s_barrier
; #define PG8_STAGE(bufoff, gbase, voff) do { _Pragma("unroll") for (int _i = 0; _i < 2; ++_i) \
;         __builtin_amdgcn_global_load_lds((const unsigned*)((const char*)(gbase) + (voff)[_i]), (LAS unsigned*)(lds + (bufoff) + ldsw + _i * 8192), 16, 0, 0); } while (0)
; #define PG8_LDA(dst, b, h) do { _Pragma("unroll") for (int m = 0; m < 4; ++m) _Pragma("unroll") for (int k = 0; k < 2; ++k) dst[m][k] = *(const LAS bf16x8*)(lds + PG8_SA(b, h) + ((aoff ^ (k * 64)) + m * 2048)); } while (0)
; #define PG8_LDB(dst, b, h) do { _Pragma("unroll") for (int n = 0; n < 2; ++n) _Pragma("unroll") for (int k = 0; k < 2; ++k) dst[n][k] = *(const LAS bf16x8*)(lds + PG8_SB(b, h) + ((boff ^ (k * 64)) + n * 2048)); } while (0)
; #define PG8_MMA(ai, bj, At, Bt) do { __builtin_amdgcn_s_setprio(1); _Pragma("unroll") for (int m = 0; m < 4; ++m) _Pragma("unroll") for (int n = 0; n < 2; ++n) _Pragma("unroll") for (int k = 0; k < 2; ++k) \
;         acc[ai][bj][m][n] = __builtin_amdgcn_mfma_f32_16x16x32_bf16(Bt[n][k], At[m][k], acc[ai][bj][m][n], 0, 0, 0); __builtin_amdgcn_s_setprio(0); } while (0)
; #define PG8_WAIT_V(n) asm volatile("s_waitcnt vmcnt(" #n ")" ::: "memory")
; #define PG8_WAIT_L(n) asm volatile("s_waitcnt lgkmcnt(" #n ")" ::: "memory")
; #define PG8_BAR __builtin_amdgcn_s_barrier()
; #define PG8_SCHED __builtin_amdgcn_sched_barrier(0)
;     ...
;             PG8_WAIT_V(8); PG8_WAIT_L(0); PG8_BAR; if (do1) { PG8_MMA(1, 0, At, B0); PG8_MMA(1, 1, At, B1); } PG8_BAR; PG8_SCHED;
;             PG8_LDB(B0, 1, 0); PG8_LDB(B1, 1, 1); PG8_SCHED; PG8_LDA(At, 1, 0); PG8_STAGE(PG8_SA(0, 1), a2, vs[1]);
;             PG8_WAIT_V(8); PG8_WAIT_L(0); PG8_BAR; if (do0) { PG8_MMA(0, 0, At, B0); PG8_MMA(0, 1, At, B1); } PG8_BAR; PG8_SCHED;
	s_setprio 1
	v_mfma_f32_16x16x32_bf16 v[118:121], v[130:133], v[212:215], v[118:121]
	v_mfma_f32_16x16x32_bf16 v[114:117], v[172:175], v[212:215], v[114:117]
	v_mfma_f32_16x16x32_bf16 v[86:89], v[130:133], v[216:219], v[86:89]
	v_mfma_f32_16x16x32_bf16 v[82:85], v[172:175], v[216:219], v[82:85]
	v_mfma_f32_16x16x32_bf16 v[54:57], v[130:133], v[228:231], v[54:57]
	v_mfma_f32_16x16x32_bf16 v[50:53], v[172:175], v[228:231], v[50:53]
	v_mfma_f32_16x16x32_bf16 v[22:25], v[130:133], v[232:235], v[22:25]
	v_mfma_f32_16x16x32_bf16 v[18:21], v[172:175], v[232:235], v[18:21]
	v_mfma_f32_16x16x32_bf16 v[118:121], v[134:137], v[220:223], v[118:121]
	v_mfma_f32_16x16x32_bf16 v[114:117], v[176:179], v[220:223], v[114:117]
	v_mfma_f32_16x16x32_bf16 v[86:89], v[134:137], v[224:227], v[86:89]
	v_mfma_f32_16x16x32_bf16 v[82:85], v[176:179], v[224:227], v[82:85]
	v_mfma_f32_16x16x32_bf16 v[54:57], v[134:137], v[236:239], v[54:57]
	v_mfma_f32_16x16x32_bf16 v[50:53], v[176:179], v[236:239], v[50:53]
	v_mfma_f32_16x16x32_bf16 v[22:25], v[134:137], v[240:243], v[22:25]
	v_mfma_f32_16x16x32_bf16 v[18:21], v[176:179], v[240:243], v[18:21]
	v_mfma_f32_16x16x32_bf16 v[102:105], v[192:195], v[212:215], v[102:105]
	v_mfma_f32_16x16x32_bf16 v[98:101], v[204:207], v[212:215], v[98:101]
	v_mfma_f32_16x16x32_bf16 v[70:73], v[192:195], v[216:219], v[70:73]
	v_mfma_f32_16x16x32_bf16 v[66:69], v[204:207], v[216:219], v[66:69]
	v_mfma_f32_16x16x32_bf16 v[38:41], v[192:195], v[228:231], v[38:41]
	v_mfma_f32_16x16x32_bf16 v[34:37], v[204:207], v[228:231], v[34:37]
	v_mfma_f32_16x16x32_bf16 v[6:9], v[192:195], v[232:235], v[6:9]
	v_mfma_f32_16x16x32_bf16 v[2:5], v[204:207], v[232:235], v[2:5]
	v_mfma_f32_16x16x32_bf16 v[102:105], v[200:203], v[220:223], v[102:105]
	v_mfma_f32_16x16x32_bf16 v[98:101], v[208:211], v[220:223], v[98:101]
	v_mfma_f32_16x16x32_bf16 v[70:73], v[200:203], v[224:227], v[70:73]
	v_mfma_f32_16x16x32_bf16 v[66:69], v[208:211], v[224:227], v[66:69]
	v_mfma_f32_16x16x32_bf16 v[38:41], v[200:203], v[236:239], v[38:41]
	v_mfma_f32_16x16x32_bf16 v[34:37], v[208:211], v[236:239], v[34:37]
	v_mfma_f32_16x16x32_bf16 v[6:9], v[200:203], v[240:243], v[6:9]
	v_mfma_f32_16x16x32_bf16 v[2:5], v[208:211], v[240:243], v[2:5]
	s_setprio 0
	s_barrier
	s_add_i32 s18, 0, 0x18000
	v_add_u32_e32 v130, s18, v153
	v_add_u32_e32 v134, s18, v184
	v_add_u32_e32 v150, s12, v153
	v_add_u32_e32 v176, s12, v184
	s_add_i32 s19, 0, 0x1c000
	ds_read_b128 v[130:133], v130
	ds_read_b128 v[134:137], v134
	ds_read_b128 v[172:175], v150
	ds_read_b128 v[176:179], v176
	v_add_u32_e32 v150, s19, v153
	v_add_u32_e32 v191, s19, v184
	ds_read_b128 v[192:195], v150
	ds_read_b128 v[200:203], v191
	v_add_u32_e32 v150, s13, v153
	v_add_u32_e32 v191, s13, v184
	ds_read_b128 v[204:207], v150
	ds_read_b128 v[208:211], v191
	s_mov_b32 m0, s65
	v_lshl_add_u64 v[244:245], s[58:59], 0, v[146:147]
	ds_read_b128 v[212:215], v189 offset:32768
	ds_read_b128 v[216:219], v189 offset:34816
	ds_read_b128 v[220:223], v190 offset:32768
	ds_read_b128 v[224:227], v190 offset:34816
	ds_read_b128 v[228:231], v189 offset:36864
	ds_read_b128 v[232:235], v189 offset:38912
	ds_read_b128 v[236:239], v190 offset:36864
	ds_read_b128 v[240:243], v190 offset:38912
	global_load_lds_dwordx4 v[244:245], off
	v_lshl_add_u64 v[244:245], s[58:59], 0, v[148:149]
	s_mov_b32 m0, s66
	s_nop 0
	global_load_lds_dwordx4 v[244:245], off
	s_waitcnt vmcnt(8)
	s_waitcnt lgkmcnt(0)
	s_barrier
	s_setprio 1
	v_mfma_f32_16x16x32_bf16 v[126:129], v[130:133], v[212:215], v[126:129]
	v_mfma_f32_16x16x32_bf16 v[122:125], v[172:175], v[212:215], v[122:125]
	v_mfma_f32_16x16x32_bf16 v[94:97], v[130:133], v[216:219], v[94:97]
	v_mfma_f32_16x16x32_bf16 v[90:93], v[172:175], v[216:219], v[90:93]
	v_mfma_f32_16x16x32_bf16 v[62:65], v[130:133], v[228:231], v[62:65]
	v_mfma_f32_16x16x32_bf16 v[58:61], v[172:175], v[228:231], v[58:61]
	v_mfma_f32_16x16x32_bf16 v[30:33], v[130:133], v[232:235], v[30:33]
	v_mfma_f32_16x16x32_bf16 v[26:29], v[172:175], v[232:235], v[26:29]
	v_mfma_f32_16x16x32_bf16 v[126:129], v[134:137], v[220:223], v[126:129]
	v_mfma_f32_16x16x32_bf16 v[122:125], v[176:179], v[220:223], v[122:125]
	v_mfma_f32_16x16x32_bf16 v[94:97], v[134:137], v[224:227], v[94:97]
	v_mfma_f32_16x16x32_bf16 v[90:93], v[176:179], v[224:227], v[90:93]
	v_mfma_f32_16x16x32_bf16 v[62:65], v[134:137], v[236:239], v[62:65]
	v_mfma_f32_16x16x32_bf16 v[58:61], v[176:179], v[236:239], v[58:61]
	v_mfma_f32_16x16x32_bf16 v[30:33], v[134:137], v[240:243], v[30:33]
	v_mfma_f32_16x16x32_bf16 v[26:29], v[176:179], v[240:243], v[26:29]
	v_mfma_f32_16x16x32_bf16 v[110:113], v[192:195], v[212:215], v[110:113]
	v_mfma_f32_16x16x32_bf16 v[106:109], v[204:207], v[212:215], v[106:109]
	v_mfma_f32_16x16x32_bf16 v[78:81], v[192:195], v[216:219], v[78:81]
	v_mfma_f32_16x16x32_bf16 v[74:77], v[204:207], v[216:219], v[74:77]
	v_mfma_f32_16x16x32_bf16 v[46:49], v[192:195], v[228:231], v[46:49]
	v_mfma_f32_16x16x32_bf16 v[42:45], v[204:207], v[228:231], v[42:45]
	v_mfma_f32_16x16x32_bf16 v[14:17], v[192:195], v[232:235], v[14:17]
	v_mfma_f32_16x16x32_bf16 v[10:13], v[204:207], v[232:235], v[10:13]
	v_mfma_f32_16x16x32_bf16 v[110:113], v[200:203], v[220:223], v[110:113]
	v_mfma_f32_16x16x32_bf16 v[106:109], v[208:211], v[220:223], v[106:109]
	v_mfma_f32_16x16x32_bf16 v[78:81], v[200:203], v[224:227], v[78:81]
	v_mfma_f32_16x16x32_bf16 v[74:77], v[208:211], v[224:227], v[74:77]
	v_mfma_f32_16x16x32_bf16 v[46:49], v[200:203], v[236:239], v[46:49]
	v_mfma_f32_16x16x32_bf16 v[42:45], v[208:211], v[236:239], v[42:45]
	v_mfma_f32_16x16x32_bf16 v[14:17], v[200:203], v[240:243], v[14:17]
	v_mfma_f32_16x16x32_bf16 v[10:13], v[208:211], v[240:243], v[10:13]
	s_setprio 0
	s_barrier
; #define PG8_STAGE(bufoff, gbase, voff) do { _Pragma("unroll") for (int _i = 0; _i < 2; ++_i) \
;         __builtin_amdgcn_global_load_lds((const unsigned*)((const char*)(gbase) + (voff)[_i]), (LAS unsigned*)(lds + (bufoff) + ldsw + _i * 8192), 16, 0, 0); } while (0)
; #define PG8_LDA(dst, b, h) do { _Pragma("unroll") for (int m = 0; m < 4; ++m) _Pragma("unroll") for (int k = 0; k < 2; ++k) dst[m][k] = *(const LAS bf16x8*)(lds + PG8_SA(b, h) + ((aoff ^ (k * 64)) + m * 2048)); } while (0)
; #define PG8_MMA(ai, bj, At, Bt) do { __builtin_amdgcn_s_setprio(1); _Pragma("unroll") for (int m = 0; m < 4; ++m) _Pragma("unroll") for (int n = 0; n < 2; ++n) _Pragma("unroll") for (int k = 0; k < 2; ++k) \
;         acc[ai][bj][m][n] = __builtin_amdgcn_mfma_f32_16x16x32_bf16(Bt[n][k], At[m][k], acc[ai][bj][m][n], 0, 0, 0); __builtin_amdgcn_s_setprio(0); } while (0)
; #define PG8_WAIT_V(n) asm volatile("s_waitcnt vmcnt(" #n ")" ::: "memory")
; #define PG8_WAIT_L(n) asm volatile("s_waitcnt lgkmcnt(" #n ")" ::: "memory")
; #define PG8_BAR __builtin_amdgcn_s_barrier()
; #define PG8_SCHED __builtin_amdgcn_sched_barrier(0)
;     ...
;             PG8_LDA(At, 1, 1); PG8_STAGE(PG8_SB(1, 0), b3, voffB); PG8_STAGE(PG8_SB(1, 1), b3 + hstep, voffB); PG8_STAGE(PG8_SA(1, 0), a3, vs[0]);
;             PG8_WAIT_V(8); PG8_WAIT_L(0); PG8_BAR; if (do1) { PG8_MMA(1, 0, At, B0); PG8_MMA(1, 1, At, B1); } PG8_BAR; PG8_SCHED;
;         }
;         if (wr == 0) PG8_BAR;
	s_add_i32 s18, s18, s60
	v_lshl_add_u64 v[180:181], v[180:181], 0, s[24:25]
	s_mov_b32 m0, s18
	ds_read_b128 v[212:215], v189 offset:49152
	ds_read_b128 v[216:219], v189 offset:51200
	ds_read_b128 v[220:223], v190 offset:49152
	ds_read_b128 v[224:227], v190 offset:51200
	ds_read_b128 v[228:231], v189 offset:53248
	ds_read_b128 v[232:235], v189 offset:55296
	ds_read_b128 v[236:239], v190 offset:53248
	ds_read_b128 v[240:243], v190 offset:55296
	global_load_lds_dwordx4 v[180:181], off
	s_add_i32 m0, s18, 0x2000
	s_add_u32 s56, s56, 0x40080
	v_lshl_add_u64 v[180:181], v[196:197], 0, s[24:25]
	s_addc_u32 s57, s57, 0
	s_add_i32 s18, s19, s60
	global_load_lds_dwordx4 v[180:181], off
	v_lshl_add_u64 v[180:181], s[56:57], 0, v[138:139]
	s_mov_b32 m0, s18
	s_nop 0
	global_load_lds_dwordx4 v[180:181], off
	v_lshl_add_u64 v[180:181], s[56:57], 0, v[140:141]
	s_add_i32 m0, s18, 0x2000
	s_nop 0
	global_load_lds_dwordx4 v[180:181], off
	v_lshl_add_u64 v[180:181], s[6:7], 0, v[142:143]
	s_mov_b32 m0, s68
	s_nop 0
	global_load_lds_dwordx4 v[180:181], off
	v_lshl_add_u64 v[180:181], s[6:7], 0, v[144:145]
	s_mov_b32 m0, s69
	s_nop 0
	global_load_lds_dwordx4 v[180:181], off
	s_waitcnt vmcnt(8)
	s_waitcnt lgkmcnt(0)
	s_barrier
	s_setprio 1
	v_mfma_f32_16x16x32_bf16 v[118:121], v[130:133], v[212:215], v[118:121]
	v_mfma_f32_16x16x32_bf16 v[114:117], v[172:175], v[212:215], v[114:117]
	v_mfma_f32_16x16x32_bf16 v[86:89], v[130:133], v[216:219], v[86:89]
	v_mfma_f32_16x16x32_bf16 v[82:85], v[172:175], v[216:219], v[82:85]
	v_mfma_f32_16x16x32_bf16 v[54:57], v[130:133], v[228:231], v[54:57]
	v_mfma_f32_16x16x32_bf16 v[50:53], v[172:175], v[228:231], v[50:53]
	v_mfma_f32_16x16x32_bf16 v[22:25], v[130:133], v[232:235], v[22:25]
	v_mfma_f32_16x16x32_bf16 v[18:21], v[172:175], v[232:235], v[18:21]
	v_mfma_f32_16x16x32_bf16 v[118:121], v[134:137], v[220:223], v[118:121]
	v_mfma_f32_16x16x32_bf16 v[114:117], v[176:179], v[220:223], v[114:117]
	v_mfma_f32_16x16x32_bf16 v[86:89], v[134:137], v[224:227], v[86:89]
	v_mfma_f32_16x16x32_bf16 v[82:85], v[176:179], v[224:227], v[82:85]
	v_mfma_f32_16x16x32_bf16 v[54:57], v[134:137], v[236:239], v[54:57]
	v_mfma_f32_16x16x32_bf16 v[50:53], v[176:179], v[236:239], v[50:53]
	v_mfma_f32_16x16x32_bf16 v[22:25], v[134:137], v[240:243], v[22:25]
	v_mfma_f32_16x16x32_bf16 v[18:21], v[176:179], v[240:243], v[18:21]
	v_mfma_f32_16x16x32_bf16 v[102:105], v[192:195], v[212:215], v[102:105]
	v_mfma_f32_16x16x32_bf16 v[98:101], v[204:207], v[212:215], v[98:101]
	v_mfma_f32_16x16x32_bf16 v[70:73], v[192:195], v[216:219], v[70:73]
	v_mfma_f32_16x16x32_bf16 v[66:69], v[204:207], v[216:219], v[66:69]
	v_mfma_f32_16x16x32_bf16 v[38:41], v[192:195], v[228:231], v[38:41]
	v_mfma_f32_16x16x32_bf16 v[34:37], v[204:207], v[228:231], v[34:37]
	v_mfma_f32_16x16x32_bf16 v[6:9], v[192:195], v[232:235], v[6:9]
	v_mfma_f32_16x16x32_bf16 v[2:5], v[204:207], v[232:235], v[2:5]
	v_mfma_f32_16x16x32_bf16 v[102:105], v[200:203], v[220:223], v[102:105]
	v_mfma_f32_16x16x32_bf16 v[98:101], v[208:211], v[220:223], v[98:101]
	v_mfma_f32_16x16x32_bf16 v[70:73], v[200:203], v[224:227], v[70:73]
	v_mfma_f32_16x16x32_bf16 v[66:69], v[208:211], v[224:227], v[66:69]
	v_mfma_f32_16x16x32_bf16 v[38:41], v[200:203], v[236:239], v[38:41]
	v_mfma_f32_16x16x32_bf16 v[34:37], v[208:211], v[236:239], v[34:37]
	v_mfma_f32_16x16x32_bf16 v[6:9], v[200:203], v[240:243], v[6:9]
	v_mfma_f32_16x16x32_bf16 v[2:5], v[208:211], v[240:243], v[2:5]
	s_setprio 0
	s_barrier
	s_add_i32 s63, s63, 2
	s_add_u32 s49, s49, 0x100
	s_addc_u32 s62, s62, 0
	s_add_u32 s0, s0, 0x8000
	s_addc_u32 s1, s1, 0
	s_cmp_gt_u32 s63, 13
	s_cbranch_scc0 .LBB0_1498
	s_and_b64 vcc, exec, s[26:27]
	s_cbranch_vccz .LBB0_1502
	s_barrier
	s_cmp_gt_i32 s8, 7
	s_mov_b64 s[0:1], -1
	s_cbranch_scc1 .LBB0_1503

; #define PG8_STAGE(bufoff, gbase, voff) do { _Pragma("unroll") for (int _i = 0; _i < 2; ++_i) \
;         __builtin_amdgcn_global_load_lds((const unsigned*)((const char*)(gbase) + (voff)[_i]), (LAS unsigned*)(lds + (bufoff) + ldsw + _i * 8192), 16, 0, 0); } while (0)
; #define PG8_LDA(dst, b, h) do { _Pragma("unroll") for (int m = 0; m < 4; ++m) _Pragma("unroll") for (int k = 0; k < 2; ++k) dst[m][k] = *(const LAS bf16x8*)(lds + PG8_SA(b, h) + ((aoff ^ (k * 64)) + m * 2048)); } while (0)
; #define PG8_LDB(dst, b, h) do { _Pragma("unroll") for (int n = 0; n < 2; ++n) _Pragma("unroll") for (int k = 0; k < 2; ++k) dst[n][k] = *(const LAS bf16x8*)(lds + PG8_SB(b, h) + ((boff ^ (k * 64)) + n * 2048)); } while (0)
; #define PG8_MMA(ai, bj, At, Bt) do { __builtin_amdgcn_s_setprio(1); _Pragma("unroll") for (int m = 0; m < 4; ++m) _Pragma("unroll") for (int n = 0; n < 2; ++n) _Pragma("unroll") for (int k = 0; k < 2; ++k) \
;         acc[ai][bj][m][n] = __builtin_amdgcn_mfma_f32_16x16x32_bf16(Bt[n][k], At[m][k], acc[ai][bj][m][n], 0, 0, 0); __builtin_amdgcn_s_setprio(0); } while (0)
; #define PG8_WAIT_V(n) asm volatile("s_waitcnt vmcnt(" #n ")" ::: "memory")
; #define PG8_WAIT_L(n) asm volatile("s_waitcnt lgkmcnt(" #n ")" ::: "memory")
; #define PG8_BAR __builtin_amdgcn_s_barrier()
; #define PG8_SCHED __builtin_amdgcn_sched_barrier(0)
;     ...
;             PG8_LDB(B0, 0, 0); PG8_LDB(B1, 0, 1); PG8_SCHED; PG8_LDA(At, 0, 0); PG8_STAGE(PG8_SA(1, 1), a1, voffA[1]);
;             PG8_WAIT_V(8); PG8_WAIT_L(0); PG8_BAR; if (do0) { PG8_MMA(0, 0, At, B0); PG8_MMA(0, 1, At, B1); } PG8_BAR; PG8_SCHED;
;             PG8_LDA(At, 0, 1); PG8_STAGE(PG8_SB(0, 0), b2, voffB); PG8_STAGE(PG8_SB(0, 1), b2 + hstep, voffB); PG8_STAGE(PG8_SA(0, 0), a2, vs[0]);
;             PG8_WAIT_V(8); PG8_WAIT_L(0); PG8_BAR; if (do1) { PG8_MMA(1, 0, At, B0); PG8_MMA(1, 1, At, B1); } PG8_BAR; PG8_SCHED;
;             PG8_LDB(B0, 1, 0); PG8_LDB(B1, 1, 1); PG8_SCHED; PG8_LDA(At, 1, 0); PG8_STAGE(PG8_SA(0, 1), a2, vs[1]);
;             PG8_WAIT_V(8); PG8_WAIT_L(0); PG8_BAR; if (do0) { PG8_MMA(0, 0, At, B0); PG8_MMA(0, 1, At, B1); } PG8_BAR; PG8_SCHED;
.LBB0_1659:
	ds_read_b128 v[146:149], v218
	ds_read_b128 v[150:153], v219
	ds_read_b128 v[154:157], v220
	ds_read_b128 v[158:161], v221
	ds_read_b128 v[130:133], v222
	ds_read_b128 v[134:137], v223
	ds_read_b128 v[138:141], v224
	ds_read_b128 v[142:145], v225
	s_mov_b32 m0, s54
	v_lshl_add_u64 v[212:213], s[90:91], 0, v[208:209]
	s_waitcnt lgkmcnt(0)
	ds_read_b128 v[186:189], v226
	ds_read_b128 v[174:177], v226 offset:2048
	ds_read_b128 v[190:193], v227
	ds_read_b128 v[178:181], v227 offset:2048
	ds_read_b128 v[170:173], v226 offset:4096
	ds_read_b128 v[162:165], v226 offset:6144
	ds_read_b128 v[182:185], v227 offset:4096
	ds_read_b128 v[166:169], v227 offset:6144
	global_load_lds_dwordx4 v[212:213], off
	v_lshl_add_u64 v[212:213], s[90:91], 0, v[210:211]
	s_mov_b32 m0, s55
	s_and_b64 vcc, exec, s[0:1]
	global_load_lds_dwordx4 v[212:213], off
	s_waitcnt vmcnt(8)
	s_waitcnt lgkmcnt(0)
	s_barrier
	s_cbranch_vccnz .LBB0_1661
	s_setprio 1
	v_mfma_f32_16x16x32_bf16 v[114:117], v[146:149], v[186:189], v[114:117]
	v_mfma_f32_16x16x32_bf16 v[118:121], v[154:157], v[186:189], v[118:121]
	v_mfma_f32_16x16x32_bf16 v[82:85], v[146:149], v[174:177], v[82:85]
	v_mfma_f32_16x16x32_bf16 v[86:89], v[154:157], v[174:177], v[86:89]
	v_mfma_f32_16x16x32_bf16 v[50:53], v[146:149], v[170:173], v[50:53]
	v_mfma_f32_16x16x32_bf16 v[54:57], v[154:157], v[170:173], v[54:57]
	v_mfma_f32_16x16x32_bf16 v[18:21], v[146:149], v[162:165], v[18:21]
	v_mfma_f32_16x16x32_bf16 v[22:25], v[154:157], v[162:165], v[22:25]
	v_mfma_f32_16x16x32_bf16 v[114:117], v[150:153], v[190:193], v[114:117]
	v_mfma_f32_16x16x32_bf16 v[118:121], v[158:161], v[190:193], v[118:121]
	v_mfma_f32_16x16x32_bf16 v[82:85], v[150:153], v[178:181], v[82:85]
	v_mfma_f32_16x16x32_bf16 v[86:89], v[158:161], v[178:181], v[86:89]
	v_mfma_f32_16x16x32_bf16 v[50:53], v[150:153], v[182:185], v[50:53]
	v_mfma_f32_16x16x32_bf16 v[54:57], v[158:161], v[182:185], v[54:57]
	v_mfma_f32_16x16x32_bf16 v[18:21], v[150:153], v[166:169], v[18:21]
	v_mfma_f32_16x16x32_bf16 v[22:25], v[158:161], v[166:169], v[22:25]
	v_mfma_f32_16x16x32_bf16 v[98:101], v[130:133], v[186:189], v[98:101]
	v_mfma_f32_16x16x32_bf16 v[102:105], v[138:141], v[186:189], v[102:105]
	v_mfma_f32_16x16x32_bf16 v[66:69], v[130:133], v[174:177], v[66:69]
	v_mfma_f32_16x16x32_bf16 v[70:73], v[138:141], v[174:177], v[70:73]
	v_mfma_f32_16x16x32_bf16 v[34:37], v[130:133], v[170:173], v[34:37]
	v_mfma_f32_16x16x32_bf16 v[38:41], v[138:141], v[170:173], v[38:41]
	v_mfma_f32_16x16x32_bf16 v[6:9], v[130:133], v[162:165], v[6:9]
	v_mfma_f32_16x16x32_bf16 v[10:13], v[138:141], v[162:165], v[10:13]
	v_mfma_f32_16x16x32_bf16 v[98:101], v[134:137], v[190:193], v[98:101]
	v_mfma_f32_16x16x32_bf16 v[102:105], v[142:145], v[190:193], v[102:105]
	v_mfma_f32_16x16x32_bf16 v[66:69], v[134:137], v[178:181], v[66:69]
	v_mfma_f32_16x16x32_bf16 v[70:73], v[142:145], v[178:181], v[70:73]
	v_mfma_f32_16x16x32_bf16 v[34:37], v[134:137], v[182:185], v[34:37]
	v_mfma_f32_16x16x32_bf16 v[38:41], v[142:145], v[182:185], v[38:41]
	v_mfma_f32_16x16x32_bf16 v[6:9], v[134:137], v[166:169], v[6:9]
	v_mfma_f32_16x16x32_bf16 v[10:13], v[142:145], v[166:169], v[10:13]
	s_setprio 0
.LBB0_1661:
	s_add_u32 s6, s90, s51
	s_addc_u32 s7, s91, s52
	s_add_u32 s18, s90, s50
	s_addc_u32 s19, s91, s41
	s_cmp_eq_u32 s53, 12
	s_cselect_b32 s27, s13, s7
	s_cselect_b32 s26, s12, s6
	s_cselect_b32 s25, s11, s19
	s_cselect_b32 s24, s10, s18
	s_barrier
	s_mov_b32 m0, s34
	v_lshl_add_u64 v[212:213], s[24:25], 0, v[196:197]
	s_add_u32 s6, s24, 0x40000
	s_waitcnt lgkmcnt(0)
	ds_read_b128 v[186:189], v226 offset:16384
	ds_read_b128 v[174:177], v226 offset:18432
	ds_read_b128 v[190:193], v227 offset:16384
	ds_read_b128 v[178:181], v227 offset:18432
	ds_read_b128 v[170:173], v226 offset:20480
	ds_read_b128 v[162:165], v226 offset:22528
	ds_read_b128 v[182:185], v227 offset:20480
	ds_read_b128 v[166:169], v227 offset:22528
	global_load_lds_dwordx4 v[212:213], off
	v_lshl_add_u64 v[214:215], s[24:25], 0, v[194:195]
	s_mov_b32 m0, s35
	s_addc_u32 s7, s25, 0
	global_load_lds_dwordx4 v[214:215], off
	v_lshl_add_u64 v[228:229], s[6:7], 0, v[196:197]
	s_mov_b32 m0, s36
	s_andn2_b64 vcc, exec, s[2:3]
	global_load_lds_dwordx4 v[228:229], off
	v_lshl_add_u64 v[228:229], s[6:7], 0, v[194:195]
	s_mov_b32 m0, s37
	s_nop 0
	global_load_lds_dwordx4 v[228:229], off
	v_lshl_add_u64 v[228:229], s[26:27], 0, v[200:201]
	s_mov_b32 m0, s31
	s_nop 0
	global_load_lds_dwordx4 v[228:229], off
	v_lshl_add_u64 v[228:229], s[26:27], 0, v[202:203]
	s_mov_b32 m0, s38
	s_nop 0
	global_load_lds_dwordx4 v[228:229], off
	s_waitcnt vmcnt(8)
	s_waitcnt lgkmcnt(0)
	v_cndmask_b32_e64 v228, 0, 1, s[2:3]
	v_cmp_ne_u32_e64 s[6:7], 1, v228
	s_barrier
	s_cbranch_vccnz .LBB0_1663
	s_setprio 1
	v_mfma_f32_16x16x32_bf16 v[126:129], v[146:149], v[186:189], v[126:129]
	v_mfma_f32_16x16x32_bf16 v[122:125], v[154:157], v[186:189], v[122:125]
	v_mfma_f32_16x16x32_bf16 v[94:97], v[146:149], v[174:177], v[94:97]
	v_mfma_f32_16x16x32_bf16 v[90:93], v[154:157], v[174:177], v[90:93]
	v_mfma_f32_16x16x32_bf16 v[62:65], v[146:149], v[170:173], v[62:65]
	v_mfma_f32_16x16x32_bf16 v[58:61], v[154:157], v[170:173], v[58:61]
	v_mfma_f32_16x16x32_bf16 v[30:33], v[146:149], v[162:165], v[30:33]
	v_mfma_f32_16x16x32_bf16 v[26:29], v[154:157], v[162:165], v[26:29]
	v_mfma_f32_16x16x32_bf16 v[126:129], v[150:153], v[190:193], v[126:129]
	v_mfma_f32_16x16x32_bf16 v[122:125], v[158:161], v[190:193], v[122:125]
	v_mfma_f32_16x16x32_bf16 v[94:97], v[150:153], v[178:181], v[94:97]
	v_mfma_f32_16x16x32_bf16 v[90:93], v[158:161], v[178:181], v[90:93]
	v_mfma_f32_16x16x32_bf16 v[62:65], v[150:153], v[182:185], v[62:65]
	v_mfma_f32_16x16x32_bf16 v[58:61], v[158:161], v[182:185], v[58:61]
	v_mfma_f32_16x16x32_bf16 v[30:33], v[150:153], v[166:169], v[30:33]
	v_mfma_f32_16x16x32_bf16 v[26:29], v[158:161], v[166:169], v[26:29]
	v_mfma_f32_16x16x32_bf16 v[110:113], v[130:133], v[186:189], v[110:113]
	v_mfma_f32_16x16x32_bf16 v[106:109], v[138:141], v[186:189], v[106:109]
	v_mfma_f32_16x16x32_bf16 v[78:81], v[130:133], v[174:177], v[78:81]
	v_mfma_f32_16x16x32_bf16 v[74:77], v[138:141], v[174:177], v[74:77]
	v_mfma_f32_16x16x32_bf16 v[46:49], v[130:133], v[170:173], v[46:49]
	v_mfma_f32_16x16x32_bf16 v[42:45], v[138:141], v[170:173], v[42:45]
	v_mfma_f32_16x16x32_bf16 v[14:17], v[130:133], v[162:165], v[14:17]
	v_mfma_f32_16x16x32_bf16 v[2:5], v[138:141], v[162:165], v[2:5]
	v_mfma_f32_16x16x32_bf16 v[110:113], v[134:137], v[190:193], v[110:113]
	v_mfma_f32_16x16x32_bf16 v[106:109], v[142:145], v[190:193], v[106:109]
	v_mfma_f32_16x16x32_bf16 v[78:81], v[134:137], v[178:181], v[78:81]
	v_mfma_f32_16x16x32_bf16 v[74:77], v[142:145], v[178:181], v[74:77]
	v_mfma_f32_16x16x32_bf16 v[46:49], v[134:137], v[182:185], v[46:49]
	v_mfma_f32_16x16x32_bf16 v[42:45], v[142:145], v[182:185], v[42:45]
	v_mfma_f32_16x16x32_bf16 v[14:17], v[134:137], v[166:169], v[14:17]
	v_mfma_f32_16x16x32_bf16 v[2:5], v[142:145], v[166:169], v[2:5]
	s_setprio 0
; #define PG8_STAGE(bufoff, gbase, voff) do { _Pragma("unroll") for (int _i = 0; _i < 2; ++_i) \
;         __builtin_amdgcn_global_load_lds((const unsigned*)((const char*)(gbase) + (voff)[_i]), (LAS unsigned*)(lds + (bufoff) + ldsw + _i * 8192), 16, 0, 0); } while (0)
; #define PG8_LDA(dst, b, h) do { _Pragma("unroll") for (int m = 0; m < 4; ++m) _Pragma("unroll") for (int k = 0; k < 2; ++k) dst[m][k] = *(const LAS bf16x8*)(lds + PG8_SA(b, h) + ((aoff ^ (k * 64)) + m * 2048)); } while (0)
; #define PG8_LDB(dst, b, h) do { _Pragma("unroll") for (int n = 0; n < 2; ++n) _Pragma("unroll") for (int k = 0; k < 2; ++k) dst[n][k] = *(const LAS bf16x8*)(lds + PG8_SB(b, h) + ((boff ^ (k * 64)) + n * 2048)); } while (0)
; #define PG8_MMA(ai, bj, At, Bt) do { __builtin_amdgcn_s_setprio(1); _Pragma("unroll") for (int m = 0; m < 4; ++m) _Pragma("unroll") for (int n = 0; n < 2; ++n) _Pragma("unroll") for (int k = 0; k < 2; ++k) \
;         acc[ai][bj][m][n] = __builtin_amdgcn_mfma_f32_16x16x32_bf16(Bt[n][k], At[m][k], acc[ai][bj][m][n], 0, 0, 0); __builtin_amdgcn_s_setprio(0); } while (0)
; #define PG8_WAIT_V(n) asm volatile("s_waitcnt vmcnt(" #n ")" ::: "memory")
; #define PG8_WAIT_L(n) asm volatile("s_waitcnt lgkmcnt(" #n ")" ::: "memory")
; #define PG8_BAR __builtin_amdgcn_s_barrier()
; #define PG8_SCHED __builtin_amdgcn_sched_barrier(0)
;     ...
;             PG8_LDB(B0, 1, 0); PG8_LDB(B1, 1, 1); PG8_SCHED; PG8_LDA(At, 1, 0); PG8_STAGE(PG8_SA(0, 1), a2, vs[1]);
;             PG8_WAIT_V(8); PG8_WAIT_L(0); PG8_BAR; if (do0) { PG8_MMA(0, 0, At, B0); PG8_MMA(0, 1, At, B1); } PG8_BAR; PG8_SCHED;
.LBB0_1663:
	s_barrier
	v_add_u32_e32 v130, s58, v216
	v_add_u32_e32 v131, s58, v217
	ds_read_b128 v[146:149], v130
	ds_read_b128 v[150:153], v131
	v_add_u32_e32 v130, s56, v216
	v_add_u32_e32 v131, s56, v217
	ds_read_b128 v[154:157], v130
	ds_read_b128 v[158:161], v131
	v_add_u32_e32 v130, s59, v216
	v_add_u32_e32 v134, s59, v217
	v_add_u32_e32 v138, s57, v216
	v_add_u32_e32 v142, s57, v217
	ds_read_b128 v[130:133], v130
	ds_read_b128 v[134:137], v134
	ds_read_b128 v[138:141], v138
	ds_read_b128 v[142:145], v142
	s_mov_b32 m0, s39
	v_lshl_add_u64 v[228:229], s[26:27], 0, v[204:205]
	s_waitcnt lgkmcnt(0)
	ds_read_b128 v[186:189], v226 offset:32768
	ds_read_b128 v[174:177], v226 offset:34816
	ds_read_b128 v[190:193], v227 offset:32768
	ds_read_b128 v[178:181], v227 offset:34816
	ds_read_b128 v[170:173], v226 offset:36864
	ds_read_b128 v[162:165], v226 offset:38912
	ds_read_b128 v[182:185], v227 offset:36864
	ds_read_b128 v[166:169], v227 offset:38912
	global_load_lds_dwordx4 v[228:229], off
	v_lshl_add_u64 v[228:229], s[26:27], 0, v[206:207]
	s_mov_b32 m0, s40
	s_and_b64 vcc, exec, s[0:1]
	global_load_lds_dwordx4 v[228:229], off
	s_waitcnt vmcnt(8)
	s_waitcnt lgkmcnt(0)
	s_barrier
	s_cbranch_vccnz .LBB0_1665
	s_setprio 1
	v_mfma_f32_16x16x32_bf16 v[114:117], v[146:149], v[186:189], v[114:117]
	v_mfma_f32_16x16x32_bf16 v[118:121], v[154:157], v[186:189], v[118:121]
	v_mfma_f32_16x16x32_bf16 v[82:85], v[146:149], v[174:177], v[82:85]
	v_mfma_f32_16x16x32_bf16 v[86:89], v[154:157], v[174:177], v[86:89]
	v_mfma_f32_16x16x32_bf16 v[50:53], v[146:149], v[170:173], v[50:53]
	v_mfma_f32_16x16x32_bf16 v[54:57], v[154:157], v[170:173], v[54:57]
	v_mfma_f32_16x16x32_bf16 v[18:21], v[146:149], v[162:165], v[18:21]
	v_mfma_f32_16x16x32_bf16 v[22:25], v[154:157], v[162:165], v[22:25]
	v_mfma_f32_16x16x32_bf16 v[114:117], v[150:153], v[190:193], v[114:117]
	v_mfma_f32_16x16x32_bf16 v[118:121], v[158:161], v[190:193], v[118:121]
	v_mfma_f32_16x16x32_bf16 v[82:85], v[150:153], v[178:181], v[82:85]
	v_mfma_f32_16x16x32_bf16 v[86:89], v[158:161], v[178:181], v[86:89]
	v_mfma_f32_16x16x32_bf16 v[50:53], v[150:153], v[182:185], v[50:53]
	v_mfma_f32_16x16x32_bf16 v[54:57], v[158:161], v[182:185], v[54:57]
	v_mfma_f32_16x16x32_bf16 v[18:21], v[150:153], v[166:169], v[18:21]
	v_mfma_f32_16x16x32_bf16 v[22:25], v[158:161], v[166:169], v[22:25]
	v_mfma_f32_16x16x32_bf16 v[98:101], v[130:133], v[186:189], v[98:101]
	v_mfma_f32_16x16x32_bf16 v[102:105], v[138:141], v[186:189], v[102:105]
	v_mfma_f32_16x16x32_bf16 v[66:69], v[130:133], v[174:177], v[66:69]
	v_mfma_f32_16x16x32_bf16 v[70:73], v[138:141], v[174:177], v[70:73]
	v_mfma_f32_16x16x32_bf16 v[34:37], v[130:133], v[170:173], v[34:37]
	v_mfma_f32_16x16x32_bf16 v[38:41], v[138:141], v[170:173], v[38:41]
	v_mfma_f32_16x16x32_bf16 v[6:9], v[130:133], v[162:165], v[6:9]
	v_mfma_f32_16x16x32_bf16 v[10:13], v[138:141], v[162:165], v[10:13]
	v_mfma_f32_16x16x32_bf16 v[98:101], v[134:137], v[190:193], v[98:101]
	v_mfma_f32_16x16x32_bf16 v[102:105], v[142:145], v[190:193], v[102:105]
	v_mfma_f32_16x16x32_bf16 v[66:69], v[134:137], v[178:181], v[66:69]
	v_mfma_f32_16x16x32_bf16 v[70:73], v[142:145], v[178:181], v[70:73]
	v_mfma_f32_16x16x32_bf16 v[34:37], v[134:137], v[182:185], v[34:37]
	v_mfma_f32_16x16x32_bf16 v[38:41], v[142:145], v[182:185], v[38:41]
	v_mfma_f32_16x16x32_bf16 v[6:9], v[134:137], v[166:169], v[6:9]
	v_mfma_f32_16x16x32_bf16 v[10:13], v[142:145], v[166:169], v[10:13]
	s_setprio 0
; #define PG8_STAGE(bufoff, gbase, voff) do { _Pragma("unroll") for (int _i = 0; _i < 2; ++_i) \
;         __builtin_amdgcn_global_load_lds((const unsigned*)((const char*)(gbase) + (voff)[_i]), (LAS unsigned*)(lds + (bufoff) + ldsw + _i * 8192), 16, 0, 0); } while (0)
; #define PG8_LDA(dst, b, h) do { _Pragma("unroll") for (int m = 0; m < 4; ++m) _Pragma("unroll") for (int k = 0; k < 2; ++k) dst[m][k] = *(const LAS bf16x8*)(lds + PG8_SA(b, h) + ((aoff ^ (k * 64)) + m * 2048)); } while (0)
; #define PG8_MMA(ai, bj, At, Bt) do { __builtin_amdgcn_s_setprio(1); _Pragma("unroll") for (int m = 0; m < 4; ++m) _Pragma("unroll") for (int n = 0; n < 2; ++n) _Pragma("unroll") for (int k = 0; k < 2; ++k) \
;         acc[ai][bj][m][n] = __builtin_amdgcn_mfma_f32_16x16x32_bf16(Bt[n][k], At[m][k], acc[ai][bj][m][n], 0, 0, 0); __builtin_amdgcn_s_setprio(0); } while (0)
; #define PG8_WAIT_V(n) asm volatile("s_waitcnt vmcnt(" #n ")" ::: "memory")
; #define PG8_WAIT_L(n) asm volatile("s_waitcnt lgkmcnt(" #n ")" ::: "memory")
; #define PG8_BAR __builtin_amdgcn_s_barrier()
; #define PG8_SCHED __builtin_amdgcn_sched_barrier(0)
;     ...
;             PG8_LDA(At, 1, 1); PG8_STAGE(PG8_SB(1, 0), b3, voffB); PG8_STAGE(PG8_SB(1, 1), b3 + hstep, voffB); PG8_STAGE(PG8_SA(1, 0), a3, vs[0]);
;             PG8_WAIT_V(8); PG8_WAIT_L(0); PG8_BAR; if (do1) { PG8_MMA(1, 0, At, B0); PG8_MMA(1, 1, At, B1); } PG8_BAR; PG8_SCHED;
;         }
.LBB0_1665:
	s_add_u32 s26, s26, 0x4000
	s_addc_u32 s27, s27, 0
	s_barrier
	s_mov_b32 m0, s44
	v_lshl_add_u64 v[212:213], v[212:213], 0, s[14:15]
	s_add_u32 s24, s24, 0x40080
	s_waitcnt lgkmcnt(0)
	ds_read_b128 v[186:189], v226 offset:49152
	ds_read_b128 v[174:177], v226 offset:51200
	ds_read_b128 v[190:193], v227 offset:49152
	ds_read_b128 v[178:181], v227 offset:51200
	ds_read_b128 v[170:173], v226 offset:53248
	ds_read_b128 v[162:165], v226 offset:55296
	ds_read_b128 v[182:185], v227 offset:53248
	ds_read_b128 v[166:169], v227 offset:55296
	global_load_lds_dwordx4 v[212:213], off
	v_lshl_add_u64 v[212:213], v[214:215], 0, s[14:15]
	s_mov_b32 m0, s45
	s_addc_u32 s25, s25, 0
	global_load_lds_dwordx4 v[212:213], off
	v_lshl_add_u64 v[212:213], s[24:25], 0, v[196:197]
	s_mov_b32 m0, s48
	s_and_b64 vcc, exec, s[6:7]
	global_load_lds_dwordx4 v[212:213], off
	v_lshl_add_u64 v[212:213], s[24:25], 0, v[194:195]
	s_mov_b32 m0, s49
	s_nop 0
	global_load_lds_dwordx4 v[212:213], off
	v_lshl_add_u64 v[212:213], s[26:27], 0, v[200:201]
	s_mov_b32 m0, s46
	s_nop 0
	global_load_lds_dwordx4 v[212:213], off
	v_lshl_add_u64 v[212:213], s[26:27], 0, v[202:203]
	s_mov_b32 m0, s47
	s_nop 0
	global_load_lds_dwordx4 v[212:213], off
	s_waitcnt vmcnt(8)
	s_waitcnt lgkmcnt(0)
	s_barrier
	s_cbranch_vccnz .LBB0_1658
	s_setprio 1
	v_mfma_f32_16x16x32_bf16 v[126:129], v[146:149], v[186:189], v[126:129]
	v_mfma_f32_16x16x32_bf16 v[122:125], v[154:157], v[186:189], v[122:125]
	v_mfma_f32_16x16x32_bf16 v[94:97], v[146:149], v[174:177], v[94:97]
	v_mfma_f32_16x16x32_bf16 v[90:93], v[154:157], v[174:177], v[90:93]
	v_mfma_f32_16x16x32_bf16 v[62:65], v[146:149], v[170:173], v[62:65]
	v_mfma_f32_16x16x32_bf16 v[58:61], v[154:157], v[170:173], v[58:61]
	v_mfma_f32_16x16x32_bf16 v[30:33], v[146:149], v[162:165], v[30:33]
	v_mfma_f32_16x16x32_bf16 v[26:29], v[154:157], v[162:165], v[26:29]
	v_mfma_f32_16x16x32_bf16 v[126:129], v[150:153], v[190:193], v[126:129]
	v_mfma_f32_16x16x32_bf16 v[122:125], v[158:161], v[190:193], v[122:125]
	v_mfma_f32_16x16x32_bf16 v[94:97], v[150:153], v[178:181], v[94:97]
	v_mfma_f32_16x16x32_bf16 v[90:93], v[158:161], v[178:181], v[90:93]
	v_mfma_f32_16x16x32_bf16 v[62:65], v[150:153], v[182:185], v[62:65]
	v_mfma_f32_16x16x32_bf16 v[58:61], v[158:161], v[182:185], v[58:61]
	v_mfma_f32_16x16x32_bf16 v[30:33], v[150:153], v[166:169], v[30:33]
	v_mfma_f32_16x16x32_bf16 v[26:29], v[158:161], v[166:169], v[26:29]
	v_mfma_f32_16x16x32_bf16 v[110:113], v[130:133], v[186:189], v[110:113]
	v_mfma_f32_16x16x32_bf16 v[106:109], v[138:141], v[186:189], v[106:109]
	v_mfma_f32_16x16x32_bf16 v[78:81], v[130:133], v[174:177], v[78:81]
	v_mfma_f32_16x16x32_bf16 v[74:77], v[138:141], v[174:177], v[74:77]
	v_mfma_f32_16x16x32_bf16 v[46:49], v[130:133], v[170:173], v[46:49]
	v_mfma_f32_16x16x32_bf16 v[42:45], v[138:141], v[170:173], v[42:45]
	v_mfma_f32_16x16x32_bf16 v[14:17], v[130:133], v[162:165], v[14:17]
	v_mfma_f32_16x16x32_bf16 v[2:5], v[138:141], v[162:165], v[2:5]
	v_mfma_f32_16x16x32_bf16 v[110:113], v[134:137], v[190:193], v[110:113]
	v_mfma_f32_16x16x32_bf16 v[106:109], v[142:145], v[190:193], v[106:109]
	v_mfma_f32_16x16x32_bf16 v[78:81], v[134:137], v[178:181], v[78:81]
	v_mfma_f32_16x16x32_bf16 v[74:77], v[142:145], v[178:181], v[74:77]
	v_mfma_f32_16x16x32_bf16 v[46:49], v[134:137], v[182:185], v[46:49]
	v_mfma_f32_16x16x32_bf16 v[42:45], v[142:145], v[182:185], v[42:45]
	v_mfma_f32_16x16x32_bf16 v[14:17], v[134:137], v[166:169], v[14:17]
	v_mfma_f32_16x16x32_bf16 v[2:5], v[142:145], v[166:169], v[2:5]
	s_setprio 0
	s_branch .LBB0_1658

; #define PG8_STAGE(bufoff, gbase, voff) do { _Pragma("unroll") for (int _i = 0; _i < 2; ++_i) \
;         __builtin_amdgcn_global_load_lds((const unsigned*)((const char*)(gbase) + (voff)[_i]), (LAS unsigned*)(lds + (bufoff) + ldsw + _i * 8192), 16, 0, 0); } while (0)
; #define PG8_LDA(dst, b, h) do { _Pragma("unroll") for (int m = 0; m < 4; ++m) _Pragma("unroll") for (int k = 0; k < 2; ++k) dst[m][k] = *(const LAS bf16x8*)(lds + PG8_SA(b, h) + ((aoff ^ (k * 64)) + m * 2048)); } while (0)
; #define PG8_LDB(dst, b, h) do { _Pragma("unroll") for (int n = 0; n < 2; ++n) _Pragma("unroll") for (int k = 0; k < 2; ++k) dst[n][k] = *(const LAS bf16x8*)(lds + PG8_SB(b, h) + ((boff ^ (k * 64)) + n * 2048)); } while (0)
; #define PG8_MMA(ai, bj, At, Bt) do { __builtin_amdgcn_s_setprio(1); _Pragma("unroll") for (int m = 0; m < 4; ++m) _Pragma("unroll") for (int n = 0; n < 2; ++n) _Pragma("unroll") for (int k = 0; k < 2; ++k) \
;         acc[ai][bj][m][n] = __builtin_amdgcn_mfma_f32_16x16x32_bf16(Bt[n][k], At[m][k], acc[ai][bj][m][n], 0, 0, 0); __builtin_amdgcn_s_setprio(0); } while (0)
; #define PG8_WAIT_V(n) asm volatile("s_waitcnt vmcnt(" #n ")" ::: "memory")
; #define PG8_WAIT_L(n) asm volatile("s_waitcnt lgkmcnt(" #n ")" ::: "memory")
; #define PG8_BAR __builtin_amdgcn_s_barrier()
; #define PG8_SCHED __builtin_amdgcn_sched_barrier(0)
;     ...
;             PG8_LDB(B0, 0, 0); PG8_LDB(B1, 0, 1); PG8_SCHED; PG8_LDA(At, 0, 0); PG8_STAGE(PG8_SA(1, 1), a1, voffA[1]);
;             PG8_WAIT_V(8); PG8_WAIT_L(0); PG8_BAR; if (do0) { PG8_MMA(0, 0, At, B0); PG8_MMA(0, 1, At, B1); } PG8_BAR; PG8_SCHED;
;             PG8_LDA(At, 0, 1); PG8_STAGE(PG8_SB(0, 0), b2, voffB); PG8_STAGE(PG8_SB(0, 1), b2 + hstep, voffB); PG8_STAGE(PG8_SA(0, 0), a2, vs[0]);
;             PG8_WAIT_V(8); PG8_WAIT_L(0); PG8_BAR; if (do1) { PG8_MMA(1, 0, At, B0); PG8_MMA(1, 1, At, B1); } PG8_BAR; PG8_SCHED;
.LBB0_1934:
	ds_read_b128 v[74:77], v191
	ds_read_b128 v[78:81], v192
	ds_read_b128 v[102:105], v193
	ds_read_b128 v[106:109], v194
	ds_read_b128 v[168:171], v195
	ds_read_b128 v[172:175], v196
	ds_read_b128 v[176:179], v197
	ds_read_b128 v[180:183], v199
	s_add_u32 s38, s0, 0x80
	s_addc_u32 s39, s1, 0
	s_cmp_eq_u32 s45, 28
	s_cselect_b32 s43, s7, s39
	s_cselect_b32 s42, s8, s38
	s_cselect_b32 s39, s27, s44
	s_cselect_b32 s38, s29, s37
	v_lshl_add_u64 v[184:185], s[0:1], 0, v[162:163]
	s_add_i32 m0, s52, 0xc000
	ds_read_b128 v[210:213], v200
	ds_read_b128 v[214:217], v200 offset:2048
	ds_read_b128 v[218:221], v201
	ds_read_b128 v[222:225], v201 offset:2048
	ds_read_b128 v[226:229], v200 offset:4096
	ds_read_b128 v[230:233], v200 offset:6144
	ds_read_b128 v[234:237], v201 offset:4096
	ds_read_b128 v[238:241], v201 offset:6144
	global_load_lds_dwordx4 v[184:185], off
	v_lshl_add_u64 v[184:185], s[0:1], 0, v[160:161]
	s_add_i32 m0, s52, 0xe000
	s_add_u32 s40, s38, 0x4000
	global_load_lds_dwordx4 v[184:185], off
	s_waitcnt vmcnt(8)
	s_waitcnt lgkmcnt(0)
	s_addc_u32 s41, s39, 0
	s_barrier
	s_setprio 1
	v_mfma_f32_16x16x32_bf16 v[142:145], v[74:77], v[210:213], v[142:145]
	v_mfma_f32_16x16x32_bf16 v[10:13], v[102:105], v[210:213], v[10:13]
	v_mfma_f32_16x16x32_bf16 v[134:137], v[74:77], v[214:217], v[134:137]
	v_mfma_f32_16x16x32_bf16 v[18:21], v[102:105], v[214:217], v[18:21]
	v_mfma_f32_16x16x32_bf16 v[126:129], v[74:77], v[226:229], v[126:129]
	v_mfma_f32_16x16x32_bf16 v[22:25], v[102:105], v[226:229], v[22:25]
	v_mfma_f32_16x16x32_bf16 v[118:121], v[74:77], v[230:233], v[118:121]
	v_mfma_f32_16x16x32_bf16 v[34:37], v[102:105], v[230:233], v[34:37]
	v_mfma_f32_16x16x32_bf16 v[142:145], v[78:81], v[218:221], v[142:145]
	v_mfma_f32_16x16x32_bf16 v[10:13], v[106:109], v[218:221], v[10:13]
	v_mfma_f32_16x16x32_bf16 v[134:137], v[78:81], v[222:225], v[134:137]
	v_mfma_f32_16x16x32_bf16 v[18:21], v[106:109], v[222:225], v[18:21]
	v_mfma_f32_16x16x32_bf16 v[126:129], v[78:81], v[234:237], v[126:129]
	v_mfma_f32_16x16x32_bf16 v[22:25], v[106:109], v[234:237], v[22:25]
	v_mfma_f32_16x16x32_bf16 v[118:121], v[78:81], v[238:241], v[118:121]
	v_mfma_f32_16x16x32_bf16 v[34:37], v[106:109], v[238:241], v[34:37]
	v_mfma_f32_16x16x32_bf16 v[138:141], v[168:171], v[210:213], v[138:141]
	v_mfma_f32_16x16x32_bf16 v[14:17], v[176:179], v[210:213], v[14:17]
	v_mfma_f32_16x16x32_bf16 v[130:133], v[168:171], v[214:217], v[130:133]
	v_mfma_f32_16x16x32_bf16 v[30:33], v[176:179], v[214:217], v[30:33]
	v_mfma_f32_16x16x32_bf16 v[122:125], v[168:171], v[226:229], v[122:125]
	v_mfma_f32_16x16x32_bf16 v[26:29], v[176:179], v[226:229], v[26:29]
	v_mfma_f32_16x16x32_bf16 v[114:117], v[168:171], v[230:233], v[114:117]
	v_mfma_f32_16x16x32_bf16 v[46:49], v[176:179], v[230:233], v[46:49]
	v_mfma_f32_16x16x32_bf16 v[138:141], v[172:175], v[218:221], v[138:141]
	v_mfma_f32_16x16x32_bf16 v[14:17], v[180:183], v[218:221], v[14:17]
	v_mfma_f32_16x16x32_bf16 v[130:133], v[172:175], v[222:225], v[130:133]
	v_mfma_f32_16x16x32_bf16 v[30:33], v[180:183], v[222:225], v[30:33]
	v_mfma_f32_16x16x32_bf16 v[122:125], v[172:175], v[234:237], v[122:125]
	v_mfma_f32_16x16x32_bf16 v[26:29], v[180:183], v[234:237], v[26:29]
	v_mfma_f32_16x16x32_bf16 v[114:117], v[172:175], v[238:241], v[114:117]
	v_mfma_f32_16x16x32_bf16 v[46:49], v[180:183], v[238:241], v[46:49]
	s_setprio 0
	s_barrier
	s_add_i32 s46, s67, s51
	v_lshl_add_u64 v[184:185], s[38:39], 0, v[146:147]
	s_mov_b32 m0, s46
	ds_read_b128 v[210:213], v200 offset:16384
	ds_read_b128 v[214:217], v200 offset:18432
	ds_read_b128 v[218:221], v201 offset:16384
	ds_read_b128 v[222:225], v201 offset:18432
	ds_read_b128 v[226:229], v200 offset:20480
	ds_read_b128 v[230:233], v200 offset:22528
	ds_read_b128 v[234:237], v201 offset:20480
	ds_read_b128 v[238:241], v201 offset:22528
	global_load_lds_dwordx4 v[184:185], off
	s_add_i32 m0, s46, 0x2000
	s_add_u32 s46, s38, 0x80000
	v_lshl_add_u64 v[184:185], s[38:39], 0, v[148:149]
	s_addc_u32 s47, s39, 0
	s_add_i32 s72, s68, s51
	global_load_lds_dwordx4 v[184:185], off
	v_lshl_add_u64 v[184:185], s[46:47], 0, v[146:147]
	s_mov_b32 m0, s72
	v_lshl_add_u64 v[242:243], s[42:43], 0, v[152:153]
	global_load_lds_dwordx4 v[184:185], off
	v_lshl_add_u64 v[184:185], s[46:47], 0, v[148:149]
	s_add_i32 m0, s72, 0x2000
	s_nop 0
	global_load_lds_dwordx4 v[184:185], off
	v_lshl_add_u64 v[184:185], s[42:43], 0, v[150:151]
	s_mov_b32 m0, s52
	s_nop 0
	global_load_lds_dwordx4 v[184:185], off
	s_mov_b32 m0, s53
	s_nop 0
	global_load_lds_dwordx4 v[242:243], off
	s_waitcnt vmcnt(8)
	s_waitcnt lgkmcnt(0)
	s_barrier
; #define PG8_STAGE(bufoff, gbase, voff) do { _Pragma("unroll") for (int _i = 0; _i < 2; ++_i) \
;         __builtin_amdgcn_global_load_lds((const unsigned*)((const char*)(gbase) + (voff)[_i]), (LAS unsigned*)(lds + (bufoff) + ldsw + _i * 8192), 16, 0, 0); } while (0)
; #define PG8_LDA(dst, b, h) do { _Pragma("unroll") for (int m = 0; m < 4; ++m) _Pragma("unroll") for (int k = 0; k < 2; ++k) dst[m][k] = *(const LAS bf16x8*)(lds + PG8_SA(b, h) + ((aoff ^ (k * 64)) + m * 2048)); } while (0)
; #define PG8_LDB(dst, b, h) do { _Pragma("unroll") for (int n = 0; n < 2; ++n) _Pragma("unroll") for (int k = 0; k < 2; ++k) dst[n][k] = *(const LAS bf16x8*)(lds + PG8_SB(b, h) + ((boff ^ (k * 64)) + n * 2048)); } while (0)
; #define PG8_MMA(ai, bj, At, Bt) do { __builtin_amdgcn_s_setprio(1); _Pragma("unroll") for (int m = 0; m < 4; ++m) _Pragma("unroll") for (int n = 0; n < 2; ++n) _Pragma("unroll") for (int k = 0; k < 2; ++k) \
;         acc[ai][bj][m][n] = __builtin_amdgcn_mfma_f32_16x16x32_bf16(Bt[n][k], At[m][k], acc[ai][bj][m][n], 0, 0, 0); __builtin_amdgcn_s_setprio(0); } while (0)
; #define PG8_WAIT_V(n) asm volatile("s_waitcnt vmcnt(" #n ")" ::: "memory")
; #define PG8_WAIT_L(n) asm volatile("s_waitcnt lgkmcnt(" #n ")" ::: "memory")
; #define PG8_BAR __builtin_amdgcn_s_barrier()
; #define PG8_SCHED __builtin_amdgcn_sched_barrier(0)
;     ...
;             PG8_WAIT_V(8); PG8_WAIT_L(0); PG8_BAR; if (do1) { PG8_MMA(1, 0, At, B0); PG8_MMA(1, 1, At, B1); } PG8_BAR; PG8_SCHED;
;             PG8_LDB(B0, 1, 0); PG8_LDB(B1, 1, 1); PG8_SCHED; PG8_LDA(At, 1, 0); PG8_STAGE(PG8_SA(0, 1), a2, vs[1]);
;             PG8_WAIT_V(8); PG8_WAIT_L(0); PG8_BAR; if (do0) { PG8_MMA(0, 0, At, B0); PG8_MMA(0, 1, At, B1); } PG8_BAR; PG8_SCHED;
	s_setprio 1
	v_mfma_f32_16x16x32_bf16 v[110:113], v[74:77], v[210:213], v[110:113]
	v_mfma_f32_16x16x32_bf16 v[58:61], v[102:105], v[210:213], v[58:61]
	v_mfma_f32_16x16x32_bf16 v[94:97], v[74:77], v[214:217], v[94:97]
	v_mfma_f32_16x16x32_bf16 v[82:85], v[102:105], v[214:217], v[82:85]
	v_mfma_f32_16x16x32_bf16 v[66:69], v[74:77], v[226:229], v[66:69]
	v_mfma_f32_16x16x32_bf16 v[62:65], v[102:105], v[226:229], v[62:65]
	v_mfma_f32_16x16x32_bf16 v[42:45], v[74:77], v[230:233], v[42:45]
	v_mfma_f32_16x16x32_bf16 v[38:41], v[102:105], v[230:233], v[38:41]
	v_mfma_f32_16x16x32_bf16 v[110:113], v[78:81], v[218:221], v[110:113]
	v_mfma_f32_16x16x32_bf16 v[58:61], v[106:109], v[218:221], v[58:61]
	v_mfma_f32_16x16x32_bf16 v[94:97], v[78:81], v[222:225], v[94:97]
	v_mfma_f32_16x16x32_bf16 v[82:85], v[106:109], v[222:225], v[82:85]
	v_mfma_f32_16x16x32_bf16 v[66:69], v[78:81], v[234:237], v[66:69]
	v_mfma_f32_16x16x32_bf16 v[62:65], v[106:109], v[234:237], v[62:65]
	v_mfma_f32_16x16x32_bf16 v[42:45], v[78:81], v[238:241], v[42:45]
	v_mfma_f32_16x16x32_bf16 v[38:41], v[106:109], v[238:241], v[38:41]
	v_mfma_f32_16x16x32_bf16 v[70:73], v[176:179], v[210:213], v[70:73]
	v_mfma_f32_16x16x32_bf16 v[86:89], v[176:179], v[214:217], v[86:89]
	v_mfma_f32_16x16x32_bf16 v[54:57], v[168:171], v[226:229], v[54:57]
	v_mfma_f32_16x16x32_bf16 v[50:53], v[176:179], v[226:229], v[50:53]
	v_mfma_f32_16x16x32_bf16 v[6:9], v[168:171], v[230:233], v[6:9]
	v_mfma_f32_16x16x32_bf16 v[2:5], v[176:179], v[230:233], v[2:5]
	v_mfma_f32_16x16x32_bf16 v[74:77], v[168:171], v[210:213], v[98:101]
	v_mfma_f32_16x16x32_bf16 v[70:73], v[180:183], v[218:221], v[70:73]
	v_mfma_f32_16x16x32_bf16 v[78:81], v[168:171], v[214:217], v[90:93]
	v_mfma_f32_16x16x32_bf16 v[86:89], v[180:183], v[222:225], v[86:89]
	v_mfma_f32_16x16x32_bf16 v[54:57], v[172:175], v[234:237], v[54:57]
	v_mfma_f32_16x16x32_bf16 v[50:53], v[180:183], v[234:237], v[50:53]
	v_mfma_f32_16x16x32_bf16 v[6:9], v[172:175], v[238:241], v[6:9]
	v_mfma_f32_16x16x32_bf16 v[2:5], v[180:183], v[238:241], v[2:5]
	v_mfma_f32_16x16x32_bf16 v[74:77], v[172:175], v[218:221], v[74:77]
	v_mfma_f32_16x16x32_bf16 v[78:81], v[172:175], v[222:225], v[78:81]
	s_setprio 0
	s_barrier
	s_add_i32 s46, 0, 0x18000
	s_add_i32 s47, 0, 0x1c000
	v_add_u32_e32 v90, s46, v189
	v_add_u32_e32 v98, s46, v190
	v_add_u32_e32 v158, s47, v189
	v_add_u32_e32 v172, s47, v190
	ds_read_b128 v[90:93], v90
	ds_read_b128 v[98:101], v98
	ds_read_b128 v[102:105], v202
	ds_read_b128 v[106:109], v203
	ds_read_b128 v[168:171], v158
	ds_read_b128 v[172:175], v172
	ds_read_b128 v[176:179], v204
	ds_read_b128 v[180:183], v205
	s_mov_b32 m0, s54
	v_lshl_add_u64 v[244:245], s[42:43], 0, v[154:155]
	ds_read_b128 v[210:213], v200 offset:32768
	ds_read_b128 v[214:217], v200 offset:34816
	ds_read_b128 v[218:221], v201 offset:32768
	ds_read_b128 v[222:225], v201 offset:34816
	ds_read_b128 v[226:229], v200 offset:36864
	ds_read_b128 v[230:233], v200 offset:38912
	ds_read_b128 v[234:237], v201 offset:36864
	ds_read_b128 v[238:241], v201 offset:38912
	global_load_lds_dwordx4 v[244:245], off
	v_lshl_add_u64 v[244:245], s[42:43], 0, v[156:157]
	s_mov_b32 m0, s55
	s_nop 0
	global_load_lds_dwordx4 v[244:245], off
	s_waitcnt vmcnt(8)
	s_waitcnt lgkmcnt(0)
	s_barrier
	s_setprio 1
	v_mfma_f32_16x16x32_bf16 v[142:145], v[90:93], v[210:213], v[142:145]
	v_mfma_f32_16x16x32_bf16 v[10:13], v[102:105], v[210:213], v[10:13]
	v_mfma_f32_16x16x32_bf16 v[134:137], v[90:93], v[214:217], v[134:137]
	v_mfma_f32_16x16x32_bf16 v[18:21], v[102:105], v[214:217], v[18:21]
	v_mfma_f32_16x16x32_bf16 v[126:129], v[90:93], v[226:229], v[126:129]
	v_mfma_f32_16x16x32_bf16 v[22:25], v[102:105], v[226:229], v[22:25]
	v_mfma_f32_16x16x32_bf16 v[118:121], v[90:93], v[230:233], v[118:121]
	v_mfma_f32_16x16x32_bf16 v[34:37], v[102:105], v[230:233], v[34:37]
	v_mfma_f32_16x16x32_bf16 v[142:145], v[98:101], v[218:221], v[142:145]
	v_mfma_f32_16x16x32_bf16 v[10:13], v[106:109], v[218:221], v[10:13]
	v_mfma_f32_16x16x32_bf16 v[134:137], v[98:101], v[222:225], v[134:137]
	v_mfma_f32_16x16x32_bf16 v[18:21], v[106:109], v[222:225], v[18:21]
	v_mfma_f32_16x16x32_bf16 v[126:129], v[98:101], v[234:237], v[126:129]
	v_mfma_f32_16x16x32_bf16 v[22:25], v[106:109], v[234:237], v[22:25]
	v_mfma_f32_16x16x32_bf16 v[118:121], v[98:101], v[238:241], v[118:121]
	v_mfma_f32_16x16x32_bf16 v[34:37], v[106:109], v[238:241], v[34:37]
	v_mfma_f32_16x16x32_bf16 v[138:141], v[168:171], v[210:213], v[138:141]
	v_mfma_f32_16x16x32_bf16 v[14:17], v[176:179], v[210:213], v[14:17]
	v_mfma_f32_16x16x32_bf16 v[130:133], v[168:171], v[214:217], v[130:133]
	v_mfma_f32_16x16x32_bf16 v[30:33], v[176:179], v[214:217], v[30:33]
	v_mfma_f32_16x16x32_bf16 v[122:125], v[168:171], v[226:229], v[122:125]
	v_mfma_f32_16x16x32_bf16 v[26:29], v[176:179], v[226:229], v[26:29]
	v_mfma_f32_16x16x32_bf16 v[114:117], v[168:171], v[230:233], v[114:117]
	v_mfma_f32_16x16x32_bf16 v[46:49], v[176:179], v[230:233], v[46:49]
	v_mfma_f32_16x16x32_bf16 v[138:141], v[172:175], v[218:221], v[138:141]
	v_mfma_f32_16x16x32_bf16 v[14:17], v[180:183], v[218:221], v[14:17]
	v_mfma_f32_16x16x32_bf16 v[130:133], v[172:175], v[222:225], v[130:133]
	v_mfma_f32_16x16x32_bf16 v[30:33], v[180:183], v[222:225], v[30:33]
	v_mfma_f32_16x16x32_bf16 v[122:125], v[172:175], v[234:237], v[122:125]
	v_mfma_f32_16x16x32_bf16 v[26:29], v[180:183], v[234:237], v[26:29]
	v_mfma_f32_16x16x32_bf16 v[114:117], v[172:175], v[238:241], v[114:117]
	v_mfma_f32_16x16x32_bf16 v[46:49], v[180:183], v[238:241], v[46:49]
	s_setprio 0
	s_barrier
; #define PG8_STAGE(bufoff, gbase, voff) do { _Pragma("unroll") for (int _i = 0; _i < 2; ++_i) \
;         __builtin_amdgcn_global_load_lds((const unsigned*)((const char*)(gbase) + (voff)[_i]), (LAS unsigned*)(lds + (bufoff) + ldsw + _i * 8192), 16, 0, 0); } while (0)
; #define PG8_LDA(dst, b, h) do { _Pragma("unroll") for (int m = 0; m < 4; ++m) _Pragma("unroll") for (int k = 0; k < 2; ++k) dst[m][k] = *(const LAS bf16x8*)(lds + PG8_SA(b, h) + ((aoff ^ (k * 64)) + m * 2048)); } while (0)
; #define PG8_MMA(ai, bj, At, Bt) do { __builtin_amdgcn_s_setprio(1); _Pragma("unroll") for (int m = 0; m < 4; ++m) _Pragma("unroll") for (int n = 0; n < 2; ++n) _Pragma("unroll") for (int k = 0; k < 2; ++k) \
;         acc[ai][bj][m][n] = __builtin_amdgcn_mfma_f32_16x16x32_bf16(Bt[n][k], At[m][k], acc[ai][bj][m][n], 0, 0, 0); __builtin_amdgcn_s_setprio(0); } while (0)
; #define PG8_WAIT_V(n) asm volatile("s_waitcnt vmcnt(" #n ")" ::: "memory")
; #define PG8_WAIT_L(n) asm volatile("s_waitcnt lgkmcnt(" #n ")" ::: "memory")
; #define PG8_BAR __builtin_amdgcn_s_barrier()
; #define PG8_SCHED __builtin_amdgcn_sched_barrier(0)
;     ...
;             PG8_LDA(At, 1, 1); PG8_STAGE(PG8_SB(1, 0), b3, voffB); PG8_STAGE(PG8_SB(1, 1), b3 + hstep, voffB); PG8_STAGE(PG8_SA(1, 0), a3, vs[0]);
;             PG8_WAIT_V(8); PG8_WAIT_L(0); PG8_BAR; if (do1) { PG8_MMA(1, 0, At, B0); PG8_MMA(1, 1, At, B1); } PG8_BAR; PG8_SCHED;
;         }
;         if (wr == 0) PG8_BAR;
	s_add_i32 s42, s46, s51
	v_lshl_add_u64 v[244:245], s[40:41], 0, v[146:147]
	s_mov_b32 m0, s42
	ds_read_b128 v[210:213], v200 offset:49152
	ds_read_b128 v[214:217], v200 offset:51200
	ds_read_b128 v[218:221], v201 offset:49152
	ds_read_b128 v[222:225], v201 offset:51200
	ds_read_b128 v[226:229], v200 offset:53248
	ds_read_b128 v[230:233], v200 offset:55296
	ds_read_b128 v[234:237], v201 offset:53248
	ds_read_b128 v[238:241], v201 offset:55296
	global_load_lds_dwordx4 v[244:245], off
	s_add_i32 m0, s42, 0x2000
	s_add_u32 s38, s38, 0x84000
	v_lshl_add_u64 v[244:245], s[40:41], 0, v[148:149]
	s_addc_u32 s39, s39, 0
	s_add_i32 s40, s47, s51
	global_load_lds_dwordx4 v[244:245], off
	v_lshl_add_u64 v[244:245], s[38:39], 0, v[146:147]
	s_mov_b32 m0, s40
	v_lshl_add_u64 v[184:185], v[184:185], 0, s[16:17]
	global_load_lds_dwordx4 v[244:245], off
	v_lshl_add_u64 v[244:245], s[38:39], 0, v[148:149]
	s_add_i32 m0, s40, 0x2000
	s_nop 0
	global_load_lds_dwordx4 v[244:245], off
	s_mov_b32 m0, s57
	s_nop 0
	global_load_lds_dwordx4 v[184:185], off
	v_lshl_add_u64 v[184:185], v[242:243], 0, s[16:17]
	s_mov_b32 m0, s58
	s_nop 0
	global_load_lds_dwordx4 v[184:185], off
	s_waitcnt vmcnt(8)
	s_waitcnt lgkmcnt(0)
	s_barrier
	s_setprio 1
	v_mfma_f32_16x16x32_bf16 v[110:113], v[90:93], v[210:213], v[110:113]
	v_mfma_f32_16x16x32_bf16 v[58:61], v[102:105], v[210:213], v[58:61]
	v_mfma_f32_16x16x32_bf16 v[94:97], v[90:93], v[214:217], v[94:97]
	v_mfma_f32_16x16x32_bf16 v[82:85], v[102:105], v[214:217], v[82:85]
	v_mfma_f32_16x16x32_bf16 v[66:69], v[90:93], v[226:229], v[66:69]
	v_mfma_f32_16x16x32_bf16 v[62:65], v[102:105], v[226:229], v[62:65]
	v_mfma_f32_16x16x32_bf16 v[42:45], v[90:93], v[230:233], v[42:45]
	v_mfma_f32_16x16x32_bf16 v[38:41], v[102:105], v[230:233], v[38:41]
	v_mfma_f32_16x16x32_bf16 v[110:113], v[98:101], v[218:221], v[110:113]
	v_mfma_f32_16x16x32_bf16 v[58:61], v[106:109], v[218:221], v[58:61]
	v_mfma_f32_16x16x32_bf16 v[94:97], v[98:101], v[222:225], v[94:97]
	v_mfma_f32_16x16x32_bf16 v[82:85], v[106:109], v[222:225], v[82:85]
	v_mfma_f32_16x16x32_bf16 v[66:69], v[98:101], v[234:237], v[66:69]
	v_mfma_f32_16x16x32_bf16 v[62:65], v[106:109], v[234:237], v[62:65]
	v_mfma_f32_16x16x32_bf16 v[42:45], v[98:101], v[238:241], v[42:45]
	v_mfma_f32_16x16x32_bf16 v[38:41], v[106:109], v[238:241], v[38:41]
	v_mfma_f32_16x16x32_bf16 v[74:77], v[168:171], v[210:213], v[74:77]
	v_mfma_f32_16x16x32_bf16 v[98:101], v[172:175], v[218:221], v[74:77]
	v_mfma_f32_16x16x32_bf16 v[74:77], v[168:171], v[214:217], v[78:81]
	v_mfma_f32_16x16x32_bf16 v[70:73], v[176:179], v[210:213], v[70:73]
	v_mfma_f32_16x16x32_bf16 v[90:93], v[172:175], v[222:225], v[74:77]
	v_mfma_f32_16x16x32_bf16 v[74:77], v[176:179], v[214:217], v[86:89]
	v_mfma_f32_16x16x32_bf16 v[54:57], v[168:171], v[226:229], v[54:57]
	v_mfma_f32_16x16x32_bf16 v[50:53], v[176:179], v[226:229], v[50:53]
	v_mfma_f32_16x16x32_bf16 v[6:9], v[168:171], v[230:233], v[6:9]
	v_mfma_f32_16x16x32_bf16 v[2:5], v[176:179], v[230:233], v[2:5]
	v_mfma_f32_16x16x32_bf16 v[70:73], v[180:183], v[218:221], v[70:73]
	v_mfma_f32_16x16x32_bf16 v[86:89], v[180:183], v[222:225], v[74:77]
	v_mfma_f32_16x16x32_bf16 v[54:57], v[172:175], v[234:237], v[54:57]
	v_mfma_f32_16x16x32_bf16 v[50:53], v[180:183], v[234:237], v[50:53]
	v_mfma_f32_16x16x32_bf16 v[6:9], v[172:175], v[238:241], v[6:9]
	v_mfma_f32_16x16x32_bf16 v[2:5], v[180:183], v[238:241], v[2:5]
	s_setprio 0
	s_barrier
	s_add_i32 s45, s45, 2
	s_add_u32 s37, s37, 0x8000
	s_addc_u32 s44, s44, 0
	s_add_u32 s0, s0, 0x100
	s_addc_u32 s1, s1, 0
	s_cmp_gt_u32 s45, 29
	s_cbranch_scc0 .LBB0_1934
	s_and_b64 vcc, exec, s[18:19]
	s_cbranch_vccz .LBB0_1937
	s_barrier

; #define PG8_STAGE(bufoff, gbase, voff) do { _Pragma("unroll") for (int _i = 0; _i < 2; ++_i) \
;         __builtin_amdgcn_global_load_lds((const unsigned*)((const char*)(gbase) + (voff)[_i]), (LAS unsigned*)(lds + (bufoff) + ldsw + _i * 8192), 16, 0, 0); } while (0)
; #define PG8_LDA(dst, b, h) do { _Pragma("unroll") for (int m = 0; m < 4; ++m) _Pragma("unroll") for (int k = 0; k < 2; ++k) dst[m][k] = *(const LAS bf16x8*)(lds + PG8_SA(b, h) + ((aoff ^ (k * 64)) + m * 2048)); } while (0)
; #define PG8_LDB(dst, b, h) do { _Pragma("unroll") for (int n = 0; n < 2; ++n) _Pragma("unroll") for (int k = 0; k < 2; ++k) dst[n][k] = *(const LAS bf16x8*)(lds + PG8_SB(b, h) + ((boff ^ (k * 64)) + n * 2048)); } while (0)
; #define PG8_MMA(ai, bj, At, Bt) do { __builtin_amdgcn_s_setprio(1); _Pragma("unroll") for (int m = 0; m < 4; ++m) _Pragma("unroll") for (int n = 0; n < 2; ++n) _Pragma("unroll") for (int k = 0; k < 2; ++k) \
;         acc[ai][bj][m][n] = __builtin_amdgcn_mfma_f32_16x16x32_bf16(Bt[n][k], At[m][k], acc[ai][bj][m][n], 0, 0, 0); __builtin_amdgcn_s_setprio(0); } while (0)
; #define PG8_WAIT_V(n) asm volatile("s_waitcnt vmcnt(" #n ")" ::: "memory")
; #define PG8_WAIT_L(n) asm volatile("s_waitcnt lgkmcnt(" #n ")" ::: "memory")
; #define PG8_BAR __builtin_amdgcn_s_barrier()
; #define PG8_SCHED __builtin_amdgcn_sched_barrier(0)
;     ...
;             PG8_LDB(B0, 0, 0); PG8_LDB(B1, 0, 1); PG8_SCHED; PG8_LDA(At, 0, 0); PG8_STAGE(PG8_SA(1, 1), a1, voffA[1]);
;             PG8_WAIT_V(8); PG8_WAIT_L(0); PG8_BAR; if (do0) { PG8_MMA(0, 0, At, B0); PG8_MMA(0, 1, At, B1); } PG8_BAR; PG8_SCHED;
;             PG8_LDA(At, 0, 1); PG8_STAGE(PG8_SB(0, 0), b2, voffB); PG8_STAGE(PG8_SB(0, 1), b2 + hstep, voffB); PG8_STAGE(PG8_SA(0, 0), a2, vs[0]);
;             PG8_WAIT_V(8); PG8_WAIT_L(0); PG8_BAR; if (do1) { PG8_MMA(1, 0, At, B0); PG8_MMA(1, 1, At, B1); } PG8_BAR; PG8_SCHED;
.LBB0_2337:
	v_add_u32_e32 v136, s43, v159
	v_add_u32_e32 v145, s43, v160
	ds_read_b128 v[166:169], v136
	ds_read_b128 v[170:173], v145
	v_add_u32_e32 v136, s44, v159
	s_add_u32 s22, s90, s20
	v_add_u32_e32 v145, s44, v160
	ds_read_b128 v[174:177], v136
	ds_read_b128 v[178:181], v145
	v_add_u32_e32 v136, s45, v159
	s_addc_u32 s23, s91, s21
	v_add_u32_e32 v145, s45, v160
	ds_read_b128 v[182:185], v136
	ds_read_b128 v[186:189], v145
	v_add_u32_e32 v136, s46, v159
	s_add_u32 s24, s22, 0x4213700
	v_add_u32_e32 v145, s46, v160
	ds_read_b128 v[190:193], v136
	ds_read_b128 v[194:197], v145
	s_addc_u32 s25, s23, 0
	s_and_b64 s[22:23], s[2:3], exec
	s_cselect_b32 s22, s14, s13
	s_cselect_b32 s27, s83, s25
	s_cselect_b32 s26, s82, s24
	s_cselect_b32 s23, s15, s53
	s_add_u32 s24, s22, 0x4000
	s_addc_u32 s25, s23, 0
	v_cndmask_b32_e64 v136, v152, v146, s[2:3]
	v_cndmask_b32_e64 v232, v153, v147, s[2:3]
	v_cndmask_b32_e64 v145, v148, v164, s[2:3]
	v_cndmask_b32_e64 v149, v150, v165, s[2:3]
	v_lshl_add_u64 v[234:235], v[156:157], 0, s[20:21]
	s_add_i32 m0, s17, 0xc000
	ds_read_b128 v[200:203], v161
	ds_read_b128 v[204:207], v161 offset:2048
	ds_read_b128 v[208:211], v162
	ds_read_b128 v[212:215], v162 offset:2048
	ds_read_b128 v[216:219], v161 offset:4096
	ds_read_b128 v[220:223], v161 offset:6144
	ds_read_b128 v[224:227], v162 offset:4096
	ds_read_b128 v[228:231], v162 offset:6144
	global_load_lds_dwordx4 v[234:235], off
	v_lshl_add_u64 v[234:235], v[154:155], 0, s[20:21]
	s_add_i32 m0, s17, 0xe000
	s_nop 0
	global_load_lds_dwordx4 v[234:235], off
	s_waitcnt vmcnt(8)
	s_waitcnt lgkmcnt(0)
	s_barrier
	s_setprio 1
	v_mfma_f32_16x16x32_bf16 v[126:129], v[166:169], v[200:203], v[126:129]
	v_mfma_f32_16x16x32_bf16 v[122:125], v[174:177], v[200:203], v[122:125]
	v_mfma_f32_16x16x32_bf16 v[110:113], v[166:169], v[204:207], v[110:113]
	v_mfma_f32_16x16x32_bf16 v[106:109], v[174:177], v[204:207], v[106:109]
	v_mfma_f32_16x16x32_bf16 v[94:97], v[166:169], v[216:219], v[94:97]
	v_mfma_f32_16x16x32_bf16 v[90:93], v[174:177], v[216:219], v[90:93]
	v_mfma_f32_16x16x32_bf16 v[78:81], v[166:169], v[220:223], v[78:81]
	v_mfma_f32_16x16x32_bf16 v[74:77], v[174:177], v[220:223], v[74:77]
	v_mfma_f32_16x16x32_bf16 v[126:129], v[170:173], v[208:211], v[126:129]
	v_mfma_f32_16x16x32_bf16 v[122:125], v[178:181], v[208:211], v[122:125]
	v_mfma_f32_16x16x32_bf16 v[110:113], v[170:173], v[212:215], v[110:113]
	v_mfma_f32_16x16x32_bf16 v[106:109], v[178:181], v[212:215], v[106:109]
	v_mfma_f32_16x16x32_bf16 v[94:97], v[170:173], v[224:227], v[94:97]
	v_mfma_f32_16x16x32_bf16 v[90:93], v[178:181], v[224:227], v[90:93]
	v_mfma_f32_16x16x32_bf16 v[78:81], v[170:173], v[228:231], v[78:81]
	v_mfma_f32_16x16x32_bf16 v[74:77], v[178:181], v[228:231], v[74:77]
	v_mfma_f32_16x16x32_bf16 v[118:121], v[182:185], v[200:203], v[118:121]
	v_mfma_f32_16x16x32_bf16 v[114:117], v[190:193], v[200:203], v[114:117]
	v_mfma_f32_16x16x32_bf16 v[102:105], v[182:185], v[204:207], v[102:105]
	v_mfma_f32_16x16x32_bf16 v[98:101], v[190:193], v[204:207], v[98:101]
	v_mfma_f32_16x16x32_bf16 v[86:89], v[182:185], v[216:219], v[86:89]
	v_mfma_f32_16x16x32_bf16 v[82:85], v[190:193], v[216:219], v[82:85]
	v_mfma_f32_16x16x32_bf16 v[70:73], v[182:185], v[220:223], v[70:73]
	v_mfma_f32_16x16x32_bf16 v[66:69], v[190:193], v[220:223], v[66:69]
	v_mfma_f32_16x16x32_bf16 v[118:121], v[186:189], v[208:211], v[118:121]
	v_mfma_f32_16x16x32_bf16 v[114:117], v[194:197], v[208:211], v[114:117]
	v_mfma_f32_16x16x32_bf16 v[102:105], v[186:189], v[212:215], v[102:105]
	v_mfma_f32_16x16x32_bf16 v[98:101], v[194:197], v[212:215], v[98:101]
	v_mfma_f32_16x16x32_bf16 v[86:89], v[186:189], v[224:227], v[86:89]
	v_mfma_f32_16x16x32_bf16 v[82:85], v[194:197], v[224:227], v[82:85]
	v_mfma_f32_16x16x32_bf16 v[70:73], v[186:189], v[228:231], v[70:73]
	v_mfma_f32_16x16x32_bf16 v[66:69], v[194:197], v[228:231], v[66:69]
	s_setprio 0
	s_barrier
	s_add_i32 s2, s43, s34
	v_lshl_add_u64 v[234:235], s[22:23], 0, v[132:133]
	s_mov_b32 m0, s2
	ds_read_b128 v[200:203], v161 offset:16384
	ds_read_b128 v[204:207], v161 offset:18432
	ds_read_b128 v[208:211], v162 offset:16384
	ds_read_b128 v[212:215], v162 offset:18432
	ds_read_b128 v[216:219], v161 offset:20480
	ds_read_b128 v[220:223], v161 offset:22528
	ds_read_b128 v[224:227], v162 offset:20480
	ds_read_b128 v[228:231], v162 offset:22528
	global_load_lds_dwordx4 v[234:235], off
	s_add_i32 m0, s2, 0x2000
	s_add_u32 s2, s22, 0x40000
	v_lshl_add_u64 v[234:235], s[22:23], 0, v[134:135]
	s_addc_u32 s3, s23, 0
	s_add_i32 s55, s45, s34
	global_load_lds_dwordx4 v[234:235], off
	v_lshl_add_u64 v[234:235], s[2:3], 0, v[132:133]
	s_mov_b32 m0, s55
	v_mov_b32_e32 v233, v137
	global_load_lds_dwordx4 v[234:235], off
	v_lshl_add_u64 v[234:235], s[2:3], 0, v[134:135]
	s_add_i32 m0, s55, 0x2000
	s_nop 0
	global_load_lds_dwordx4 v[234:235], off
	s_mov_b32 m0, s17
	v_lshl_add_u64 v[234:235], s[26:27], 0, v[136:137]
	global_load_lds_dwordx4 v136, s[26:27]
	s_mov_b32 m0, s35
	s_nop 0
	global_load_lds_dwordx4 v232, s[26:27]
	s_waitcnt vmcnt(8)
	s_waitcnt lgkmcnt(0)
	v_lshl_add_u64 v[232:233], s[26:27], 0, v[232:233]
	s_barrier
; #define PG8_STAGE(bufoff, gbase, voff) do { _Pragma("unroll") for (int _i = 0; _i < 2; ++_i) \
;         __builtin_amdgcn_global_load_lds((const unsigned*)((const char*)(gbase) + (voff)[_i]), (LAS unsigned*)(lds + (bufoff) + ldsw + _i * 8192), 16, 0, 0); } while (0)
; #define PG8_LDA(dst, b, h) do { _Pragma("unroll") for (int m = 0; m < 4; ++m) _Pragma("unroll") for (int k = 0; k < 2; ++k) dst[m][k] = *(const LAS bf16x8*)(lds + PG8_SA(b, h) + ((aoff ^ (k * 64)) + m * 2048)); } while (0)
; #define PG8_LDB(dst, b, h) do { _Pragma("unroll") for (int n = 0; n < 2; ++n) _Pragma("unroll") for (int k = 0; k < 2; ++k) dst[n][k] = *(const LAS bf16x8*)(lds + PG8_SB(b, h) + ((boff ^ (k * 64)) + n * 2048)); } while (0)
; #define PG8_MMA(ai, bj, At, Bt) do { __builtin_amdgcn_s_setprio(1); _Pragma("unroll") for (int m = 0; m < 4; ++m) _Pragma("unroll") for (int n = 0; n < 2; ++n) _Pragma("unroll") for (int k = 0; k < 2; ++k) \
;         acc[ai][bj][m][n] = __builtin_amdgcn_mfma_f32_16x16x32_bf16(Bt[n][k], At[m][k], acc[ai][bj][m][n], 0, 0, 0); __builtin_amdgcn_s_setprio(0); } while (0)
; #define PG8_WAIT_V(n) asm volatile("s_waitcnt vmcnt(" #n ")" ::: "memory")
; #define PG8_WAIT_L(n) asm volatile("s_waitcnt lgkmcnt(" #n ")" ::: "memory")
; #define PG8_BAR __builtin_amdgcn_s_barrier()
; #define PG8_SCHED __builtin_amdgcn_sched_barrier(0)
;     ...
;             PG8_WAIT_V(8); PG8_WAIT_L(0); PG8_BAR; if (do1) { PG8_MMA(1, 0, At, B0); PG8_MMA(1, 1, At, B1); } PG8_BAR; PG8_SCHED;
;             PG8_LDB(B0, 1, 0); PG8_LDB(B1, 1, 1); PG8_SCHED; PG8_LDA(At, 1, 0); PG8_STAGE(PG8_SA(0, 1), a2, vs[1]);
;             PG8_WAIT_V(8); PG8_WAIT_L(0); PG8_BAR; if (do0) { PG8_MMA(0, 0, At, B0); PG8_MMA(0, 1, At, B1); } PG8_BAR; PG8_SCHED;
	s_setprio 1
	v_mfma_f32_16x16x32_bf16 v[62:65], v[166:169], v[200:203], v[62:65]
	v_mfma_f32_16x16x32_bf16 v[58:61], v[174:177], v[200:203], v[58:61]
	v_mfma_f32_16x16x32_bf16 v[46:49], v[166:169], v[204:207], v[46:49]
	v_mfma_f32_16x16x32_bf16 v[42:45], v[174:177], v[204:207], v[42:45]
	v_mfma_f32_16x16x32_bf16 v[30:33], v[166:169], v[216:219], v[30:33]
	v_mfma_f32_16x16x32_bf16 v[26:29], v[174:177], v[216:219], v[26:29]
	v_mfma_f32_16x16x32_bf16 v[14:17], v[166:169], v[220:223], v[14:17]
	v_mfma_f32_16x16x32_bf16 v[10:13], v[174:177], v[220:223], v[10:13]
	v_mfma_f32_16x16x32_bf16 v[62:65], v[170:173], v[208:211], v[62:65]
	v_mfma_f32_16x16x32_bf16 v[58:61], v[178:181], v[208:211], v[58:61]
	v_mfma_f32_16x16x32_bf16 v[46:49], v[170:173], v[212:215], v[46:49]
	v_mfma_f32_16x16x32_bf16 v[42:45], v[178:181], v[212:215], v[42:45]
	v_mfma_f32_16x16x32_bf16 v[30:33], v[170:173], v[224:227], v[30:33]
	v_mfma_f32_16x16x32_bf16 v[26:29], v[178:181], v[224:227], v[26:29]
	v_mfma_f32_16x16x32_bf16 v[14:17], v[170:173], v[228:231], v[14:17]
	v_mfma_f32_16x16x32_bf16 v[10:13], v[178:181], v[228:231], v[10:13]
	v_mfma_f32_16x16x32_bf16 v[54:57], v[182:185], v[200:203], v[54:57]
	v_mfma_f32_16x16x32_bf16 v[50:53], v[190:193], v[200:203], v[50:53]
	v_mfma_f32_16x16x32_bf16 v[38:41], v[182:185], v[204:207], v[38:41]
	v_mfma_f32_16x16x32_bf16 v[34:37], v[190:193], v[204:207], v[34:37]
	v_mfma_f32_16x16x32_bf16 v[22:25], v[182:185], v[216:219], v[22:25]
	v_mfma_f32_16x16x32_bf16 v[18:21], v[190:193], v[216:219], v[18:21]
	v_mfma_f32_16x16x32_bf16 v[6:9], v[182:185], v[220:223], v[6:9]
	v_mfma_f32_16x16x32_bf16 v[2:5], v[190:193], v[220:223], v[2:5]
	v_mfma_f32_16x16x32_bf16 v[54:57], v[186:189], v[208:211], v[54:57]
	v_mfma_f32_16x16x32_bf16 v[50:53], v[194:197], v[208:211], v[50:53]
	v_mfma_f32_16x16x32_bf16 v[38:41], v[186:189], v[212:215], v[38:41]
	v_mfma_f32_16x16x32_bf16 v[34:37], v[194:197], v[212:215], v[34:37]
	v_mfma_f32_16x16x32_bf16 v[22:25], v[186:189], v[224:227], v[22:25]
	v_mfma_f32_16x16x32_bf16 v[18:21], v[194:197], v[224:227], v[18:21]
	v_mfma_f32_16x16x32_bf16 v[6:9], v[186:189], v[228:231], v[6:9]
	v_mfma_f32_16x16x32_bf16 v[2:5], v[194:197], v[228:231], v[2:5]
	s_setprio 0
	s_barrier
	s_add_i32 s2, 0, 0x18000
	v_add_u32_e32 v136, s2, v159
	v_add_u32_e32 v151, s2, v160
	ds_read_b128 v[166:169], v136
	ds_read_b128 v[170:173], v151
	v_add_u32_e32 v136, s47, v159
	s_add_i32 s55, 0, 0x1c000
	v_add_u32_e32 v151, s47, v160
	ds_read_b128 v[174:177], v136
	ds_read_b128 v[178:181], v151
	v_add_u32_e32 v136, s55, v159
	v_add_u32_e32 v151, s55, v160
	ds_read_b128 v[182:185], v136
	ds_read_b128 v[186:189], v151
	v_add_u32_e32 v136, s48, v159
	v_add_u32_e32 v151, s48, v160
	ds_read_b128 v[190:193], v136
	ds_read_b128 v[194:197], v151
	s_mov_b32 m0, s36
	ds_read_b128 v[200:203], v161 offset:32768
	ds_read_b128 v[204:207], v161 offset:34816
	ds_read_b128 v[208:211], v162 offset:32768
	ds_read_b128 v[212:215], v162 offset:34816
	ds_read_b128 v[216:219], v161 offset:36864
	ds_read_b128 v[220:223], v161 offset:38912
	ds_read_b128 v[224:227], v162 offset:36864
	ds_read_b128 v[228:231], v162 offset:38912
	global_load_lds_dwordx4 v145, s[26:27]
	s_mov_b32 m0, s37
	s_nop 0
	global_load_lds_dwordx4 v149, s[26:27]
	s_waitcnt vmcnt(8)
	s_waitcnt lgkmcnt(0)
	s_barrier
	s_setprio 1
	v_mfma_f32_16x16x32_bf16 v[126:129], v[166:169], v[200:203], v[126:129]
	v_mfma_f32_16x16x32_bf16 v[122:125], v[174:177], v[200:203], v[122:125]
	v_mfma_f32_16x16x32_bf16 v[110:113], v[166:169], v[204:207], v[110:113]
	v_mfma_f32_16x16x32_bf16 v[106:109], v[174:177], v[204:207], v[106:109]
	v_mfma_f32_16x16x32_bf16 v[94:97], v[166:169], v[216:219], v[94:97]
	v_mfma_f32_16x16x32_bf16 v[90:93], v[174:177], v[216:219], v[90:93]
	v_mfma_f32_16x16x32_bf16 v[78:81], v[166:169], v[220:223], v[78:81]
	v_mfma_f32_16x16x32_bf16 v[74:77], v[174:177], v[220:223], v[74:77]
	v_mfma_f32_16x16x32_bf16 v[126:129], v[170:173], v[208:211], v[126:129]
	v_mfma_f32_16x16x32_bf16 v[122:125], v[178:181], v[208:211], v[122:125]
	v_mfma_f32_16x16x32_bf16 v[110:113], v[170:173], v[212:215], v[110:113]
	v_mfma_f32_16x16x32_bf16 v[106:109], v[178:181], v[212:215], v[106:109]
	v_mfma_f32_16x16x32_bf16 v[94:97], v[170:173], v[224:227], v[94:97]
	v_mfma_f32_16x16x32_bf16 v[90:93], v[178:181], v[224:227], v[90:93]
	v_mfma_f32_16x16x32_bf16 v[78:81], v[170:173], v[228:231], v[78:81]
	v_mfma_f32_16x16x32_bf16 v[74:77], v[178:181], v[228:231], v[74:77]
	v_mfma_f32_16x16x32_bf16 v[118:121], v[182:185], v[200:203], v[118:121]
	v_mfma_f32_16x16x32_bf16 v[114:117], v[190:193], v[200:203], v[114:117]
	v_mfma_f32_16x16x32_bf16 v[102:105], v[182:185], v[204:207], v[102:105]
	v_mfma_f32_16x16x32_bf16 v[98:101], v[190:193], v[204:207], v[98:101]
	v_mfma_f32_16x16x32_bf16 v[86:89], v[182:185], v[216:219], v[86:89]
	v_mfma_f32_16x16x32_bf16 v[82:85], v[190:193], v[216:219], v[82:85]
	v_mfma_f32_16x16x32_bf16 v[70:73], v[182:185], v[220:223], v[70:73]
	v_mfma_f32_16x16x32_bf16 v[66:69], v[190:193], v[220:223], v[66:69]
	v_mfma_f32_16x16x32_bf16 v[118:121], v[186:189], v[208:211], v[118:121]
	v_mfma_f32_16x16x32_bf16 v[114:117], v[194:197], v[208:211], v[114:117]
	v_mfma_f32_16x16x32_bf16 v[102:105], v[186:189], v[212:215], v[102:105]
	v_mfma_f32_16x16x32_bf16 v[98:101], v[194:197], v[212:215], v[98:101]
	v_mfma_f32_16x16x32_bf16 v[86:89], v[186:189], v[224:227], v[86:89]
	v_mfma_f32_16x16x32_bf16 v[82:85], v[194:197], v[224:227], v[82:85]
	v_mfma_f32_16x16x32_bf16 v[70:73], v[186:189], v[228:231], v[70:73]
	v_mfma_f32_16x16x32_bf16 v[66:69], v[194:197], v[228:231], v[66:69]
	s_setprio 0
	s_barrier
; #define PG8_STAGE(bufoff, gbase, voff) do { _Pragma("unroll") for (int _i = 0; _i < 2; ++_i) \
;         __builtin_amdgcn_global_load_lds((const unsigned*)((const char*)(gbase) + (voff)[_i]), (LAS unsigned*)(lds + (bufoff) + ldsw + _i * 8192), 16, 0, 0); } while (0)
; #define PG8_LDA(dst, b, h) do { _Pragma("unroll") for (int m = 0; m < 4; ++m) _Pragma("unroll") for (int k = 0; k < 2; ++k) dst[m][k] = *(const LAS bf16x8*)(lds + PG8_SA(b, h) + ((aoff ^ (k * 64)) + m * 2048)); } while (0)
; #define PG8_MMA(ai, bj, At, Bt) do { __builtin_amdgcn_s_setprio(1); _Pragma("unroll") for (int m = 0; m < 4; ++m) _Pragma("unroll") for (int n = 0; n < 2; ++n) _Pragma("unroll") for (int k = 0; k < 2; ++k) \
;         acc[ai][bj][m][n] = __builtin_amdgcn_mfma_f32_16x16x32_bf16(Bt[n][k], At[m][k], acc[ai][bj][m][n], 0, 0, 0); __builtin_amdgcn_s_setprio(0); } while (0)
; #define PG8_WAIT_V(n) asm volatile("s_waitcnt vmcnt(" #n ")" ::: "memory")
; #define PG8_WAIT_L(n) asm volatile("s_waitcnt lgkmcnt(" #n ")" ::: "memory")
; #define PG8_BAR __builtin_amdgcn_s_barrier()
; #define PG8_SCHED __builtin_amdgcn_sched_barrier(0)
;     ...
;             PG8_LDA(At, 1, 1); PG8_STAGE(PG8_SB(1, 0), b3, voffB); PG8_STAGE(PG8_SB(1, 1), b3 + hstep, voffB); PG8_STAGE(PG8_SA(1, 0), a3, vs[0]);
;             PG8_WAIT_V(8); PG8_WAIT_L(0); PG8_BAR; if (do1) { PG8_MMA(1, 0, At, B0); PG8_MMA(1, 1, At, B1); } PG8_BAR; PG8_SCHED;
;         }
;         if (wr == 0) PG8_BAR;
	s_add_i32 s2, s2, s34
	v_lshl_add_u64 v[236:237], s[24:25], 0, v[132:133]
	s_mov_b32 m0, s2
	ds_read_b128 v[200:203], v161 offset:49152
	ds_read_b128 v[204:207], v161 offset:51200
	ds_read_b128 v[208:211], v162 offset:49152
	ds_read_b128 v[212:215], v162 offset:51200
	ds_read_b128 v[216:219], v161 offset:53248
	ds_read_b128 v[220:223], v161 offset:55296
	ds_read_b128 v[224:227], v162 offset:53248
	ds_read_b128 v[228:231], v162 offset:55296
	global_load_lds_dwordx4 v[236:237], off
	s_add_i32 m0, s2, 0x2000
	s_add_u32 s2, s22, 0x44000
	v_lshl_add_u64 v[236:237], s[24:25], 0, v[134:135]
	s_addc_u32 s3, s23, 0
	s_add_i32 s22, s55, s34
	global_load_lds_dwordx4 v[236:237], off
	v_lshl_add_u64 v[236:237], s[2:3], 0, v[132:133]
	s_mov_b32 m0, s22
	v_lshl_add_u64 v[234:235], v[234:235], 0, s[10:11]
	global_load_lds_dwordx4 v[236:237], off
	v_lshl_add_u64 v[236:237], s[2:3], 0, v[134:135]
	s_add_i32 m0, s22, 0x2000
	v_lshl_add_u64 v[232:233], v[232:233], 0, s[10:11]
	global_load_lds_dwordx4 v[236:237], off
	s_mov_b32 m0, s41
	s_nop 0
	global_load_lds_dwordx4 v[234:235], off
	s_mov_b32 m0, s42
	s_nop 0
	global_load_lds_dwordx4 v[232:233], off
	s_waitcnt vmcnt(8)
	s_waitcnt lgkmcnt(0)
	s_barrier
	s_setprio 1
	v_mfma_f32_16x16x32_bf16 v[62:65], v[166:169], v[200:203], v[62:65]
	v_mfma_f32_16x16x32_bf16 v[58:61], v[174:177], v[200:203], v[58:61]
	v_mfma_f32_16x16x32_bf16 v[46:49], v[166:169], v[204:207], v[46:49]
	v_mfma_f32_16x16x32_bf16 v[42:45], v[174:177], v[204:207], v[42:45]
	v_mfma_f32_16x16x32_bf16 v[30:33], v[166:169], v[216:219], v[30:33]
	v_mfma_f32_16x16x32_bf16 v[26:29], v[174:177], v[216:219], v[26:29]
	v_mfma_f32_16x16x32_bf16 v[14:17], v[166:169], v[220:223], v[14:17]
	v_mfma_f32_16x16x32_bf16 v[10:13], v[174:177], v[220:223], v[10:13]
	v_mfma_f32_16x16x32_bf16 v[62:65], v[170:173], v[208:211], v[62:65]
	v_mfma_f32_16x16x32_bf16 v[58:61], v[178:181], v[208:211], v[58:61]
	v_mfma_f32_16x16x32_bf16 v[46:49], v[170:173], v[212:215], v[46:49]
	v_mfma_f32_16x16x32_bf16 v[42:45], v[178:181], v[212:215], v[42:45]
	v_mfma_f32_16x16x32_bf16 v[30:33], v[170:173], v[224:227], v[30:33]
	v_mfma_f32_16x16x32_bf16 v[26:29], v[178:181], v[224:227], v[26:29]
	v_mfma_f32_16x16x32_bf16 v[14:17], v[170:173], v[228:231], v[14:17]
	v_mfma_f32_16x16x32_bf16 v[10:13], v[178:181], v[228:231], v[10:13]
	v_mfma_f32_16x16x32_bf16 v[54:57], v[182:185], v[200:203], v[54:57]
	v_mfma_f32_16x16x32_bf16 v[50:53], v[190:193], v[200:203], v[50:53]
	v_mfma_f32_16x16x32_bf16 v[38:41], v[182:185], v[204:207], v[38:41]
	v_mfma_f32_16x16x32_bf16 v[34:37], v[190:193], v[204:207], v[34:37]
	v_mfma_f32_16x16x32_bf16 v[22:25], v[182:185], v[216:219], v[22:25]
	v_mfma_f32_16x16x32_bf16 v[18:21], v[190:193], v[216:219], v[18:21]
	v_mfma_f32_16x16x32_bf16 v[6:9], v[182:185], v[220:223], v[6:9]
	v_mfma_f32_16x16x32_bf16 v[2:5], v[190:193], v[220:223], v[2:5]
	v_mfma_f32_16x16x32_bf16 v[54:57], v[186:189], v[208:211], v[54:57]
	v_mfma_f32_16x16x32_bf16 v[50:53], v[194:197], v[208:211], v[50:53]
	v_mfma_f32_16x16x32_bf16 v[38:41], v[186:189], v[212:215], v[38:41]
	v_mfma_f32_16x16x32_bf16 v[34:37], v[194:197], v[212:215], v[34:37]
	v_mfma_f32_16x16x32_bf16 v[22:25], v[186:189], v[224:227], v[22:25]
	v_mfma_f32_16x16x32_bf16 v[18:21], v[194:197], v[224:227], v[18:21]
	v_mfma_f32_16x16x32_bf16 v[6:9], v[186:189], v[228:231], v[6:9]
	v_mfma_f32_16x16x32_bf16 v[2:5], v[194:197], v[228:231], v[2:5]
	s_setprio 0
	s_barrier
	s_add_i32 s54, s54, 2
	s_add_u32 s13, s13, 0x8000
	s_addc_u32 s53, s53, 0
	s_add_u32 s20, s20, 0x100
	s_addc_u32 s21, s21, 0
	s_cmp_gt_u32 s54, 13
	s_cbranch_scc1 .LBB0_2340

; #define PG8_STAGE(bufoff, gbase, voff) do { _Pragma("unroll") for (int _i = 0; _i < 2; ++_i) \
;         __builtin_amdgcn_global_load_lds((const unsigned*)((const char*)(gbase) + (voff)[_i]), (LAS unsigned*)(lds + (bufoff) + ldsw + _i * 8192), 16, 0, 0); } while (0)
; #define PG8_LDA(dst, b, h) do { _Pragma("unroll") for (int m = 0; m < 4; ++m) _Pragma("unroll") for (int k = 0; k < 2; ++k) dst[m][k] = *(const LAS bf16x8*)(lds + PG8_SA(b, h) + ((aoff ^ (k * 64)) + m * 2048)); } while (0)
; #define PG8_LDB(dst, b, h) do { _Pragma("unroll") for (int n = 0; n < 2; ++n) _Pragma("unroll") for (int k = 0; k < 2; ++k) dst[n][k] = *(const LAS bf16x8*)(lds + PG8_SB(b, h) + ((boff ^ (k * 64)) + n * 2048)); } while (0)
; #define PG8_MMA(ai, bj, At, Bt) do { __builtin_amdgcn_s_setprio(1); _Pragma("unroll") for (int m = 0; m < 4; ++m) _Pragma("unroll") for (int n = 0; n < 2; ++n) _Pragma("unroll") for (int k = 0; k < 2; ++k) \
;         acc[ai][bj][m][n] = __builtin_amdgcn_mfma_f32_16x16x32_bf16(Bt[n][k], At[m][k], acc[ai][bj][m][n], 0, 0, 0); __builtin_amdgcn_s_setprio(0); } while (0)
; #define PG8_WAIT_V(n) asm volatile("s_waitcnt vmcnt(" #n ")" ::: "memory")
; #define PG8_WAIT_L(n) asm volatile("s_waitcnt lgkmcnt(" #n ")" ::: "memory")
; #define PG8_BAR __builtin_amdgcn_s_barrier()
; #define PG8_SCHED __builtin_amdgcn_sched_barrier(0)
;     ...
;             PG8_LDB(B0, 0, 0); PG8_LDB(B1, 0, 1); PG8_SCHED; PG8_LDA(At, 0, 0); PG8_STAGE(PG8_SA(1, 1), a1, voffA[1]);
;             PG8_WAIT_V(8); PG8_WAIT_L(0); PG8_BAR; if (do0) { PG8_MMA(0, 0, At, B0); PG8_MMA(0, 1, At, B1); } PG8_BAR; PG8_SCHED;
;             PG8_LDA(At, 0, 1); PG8_STAGE(PG8_SB(0, 0), b2, voffB); PG8_STAGE(PG8_SB(0, 1), b2 + hstep, voffB); PG8_STAGE(PG8_SA(0, 0), a2, vs[0]);
;             PG8_WAIT_V(8); PG8_WAIT_L(0); PG8_BAR; if (do1) { PG8_MMA(1, 0, At, B0); PG8_MMA(1, 1, At, B1); } PG8_BAR; PG8_SCHED;
.LBB0_2411:
	ds_read_b128 v[146:149], v153
	ds_read_b128 v[168:171], v154
	ds_read_b128 v[172:175], v155
	ds_read_b128 v[176:179], v156
	ds_read_b128 v[180:183], v157
	ds_read_b128 v[184:187], v158
	ds_read_b128 v[188:191], v159
	ds_read_b128 v[192:195], v160
	s_add_u32 s20, s18, 0x4000
	s_addc_u32 s21, s19, 0
	s_cmp_eq_u32 s56, 40
	s_cselect_b32 s26, s14, s20
	s_cselect_b32 s27, s15, s21
	s_cselect_b32 s22, s16, s54
	s_cselect_b32 s23, s17, s55
	s_add_u32 s20, s26, 0x4000
	s_addc_u32 s21, s27, 0
	v_lshl_add_u64 v[196:197], s[18:19], 0, v[142:143]
	s_add_i32 m0, s34, 0xc000
	ds_read_b128 v[200:203], v161
	ds_read_b128 v[204:207], v161 offset:2048
	ds_read_b128 v[208:211], v162
	ds_read_b128 v[212:215], v162 offset:2048
	ds_read_b128 v[216:219], v161 offset:4096
	ds_read_b128 v[220:223], v161 offset:6144
	ds_read_b128 v[224:227], v162 offset:4096
	ds_read_b128 v[228:231], v162 offset:6144
	global_load_lds_dwordx4 v[196:197], off
	v_lshl_add_u64 v[196:197], s[18:19], 0, v[144:145]
	s_add_i32 m0, s34, 0xe000
	s_add_u32 s24, s22, 0x4000
	global_load_lds_dwordx4 v[196:197], off
	s_waitcnt vmcnt(8)
	s_waitcnt lgkmcnt(0)
	s_addc_u32 s25, s23, 0
	s_barrier
	s_setprio 1
	v_mfma_f32_16x16x32_bf16 v[126:129], v[146:149], v[200:203], v[126:129]
	v_mfma_f32_16x16x32_bf16 v[122:125], v[172:175], v[200:203], v[122:125]
	v_mfma_f32_16x16x32_bf16 v[114:117], v[146:149], v[204:207], v[114:117]
	v_mfma_f32_16x16x32_bf16 v[106:109], v[172:175], v[204:207], v[106:109]
	v_mfma_f32_16x16x32_bf16 v[98:101], v[146:149], v[216:219], v[98:101]
	v_mfma_f32_16x16x32_bf16 v[90:93], v[172:175], v[216:219], v[90:93]
	v_mfma_f32_16x16x32_bf16 v[82:85], v[146:149], v[220:223], v[82:85]
	v_mfma_f32_16x16x32_bf16 v[74:77], v[172:175], v[220:223], v[74:77]
	v_mfma_f32_16x16x32_bf16 v[126:129], v[168:171], v[208:211], v[126:129]
	v_mfma_f32_16x16x32_bf16 v[122:125], v[176:179], v[208:211], v[122:125]
	v_mfma_f32_16x16x32_bf16 v[114:117], v[168:171], v[212:215], v[114:117]
	v_mfma_f32_16x16x32_bf16 v[106:109], v[176:179], v[212:215], v[106:109]
	v_mfma_f32_16x16x32_bf16 v[98:101], v[168:171], v[224:227], v[98:101]
	v_mfma_f32_16x16x32_bf16 v[90:93], v[176:179], v[224:227], v[90:93]
	v_mfma_f32_16x16x32_bf16 v[82:85], v[168:171], v[228:231], v[82:85]
	v_mfma_f32_16x16x32_bf16 v[74:77], v[176:179], v[228:231], v[74:77]
	v_mfma_f32_16x16x32_bf16 v[118:121], v[180:183], v[200:203], v[118:121]
	v_mfma_f32_16x16x32_bf16 v[110:113], v[188:191], v[200:203], v[110:113]
	v_mfma_f32_16x16x32_bf16 v[102:105], v[180:183], v[204:207], v[102:105]
	v_mfma_f32_16x16x32_bf16 v[94:97], v[188:191], v[204:207], v[94:97]
	v_mfma_f32_16x16x32_bf16 v[86:89], v[180:183], v[216:219], v[86:89]
	v_mfma_f32_16x16x32_bf16 v[78:81], v[188:191], v[216:219], v[78:81]
	v_mfma_f32_16x16x32_bf16 v[70:73], v[180:183], v[220:223], v[70:73]
	v_mfma_f32_16x16x32_bf16 v[66:69], v[188:191], v[220:223], v[66:69]
	v_mfma_f32_16x16x32_bf16 v[118:121], v[184:187], v[208:211], v[118:121]
	v_mfma_f32_16x16x32_bf16 v[110:113], v[192:195], v[208:211], v[110:113]
	v_mfma_f32_16x16x32_bf16 v[102:105], v[184:187], v[212:215], v[102:105]
	v_mfma_f32_16x16x32_bf16 v[94:97], v[192:195], v[212:215], v[94:97]
	v_mfma_f32_16x16x32_bf16 v[86:89], v[184:187], v[224:227], v[86:89]
	v_mfma_f32_16x16x32_bf16 v[78:81], v[192:195], v[224:227], v[78:81]
	v_mfma_f32_16x16x32_bf16 v[70:73], v[184:187], v[228:231], v[70:73]
	v_mfma_f32_16x16x32_bf16 v[66:69], v[192:195], v[228:231], v[66:69]
	s_setprio 0
	s_barrier
	s_add_i32 s57, s42, s30
	v_lshl_add_u64 v[196:197], s[22:23], 0, v[132:133]
	s_mov_b32 m0, s57
	ds_read_b128 v[200:203], v161 offset:16384
	ds_read_b128 v[204:207], v161 offset:18432
	ds_read_b128 v[208:211], v162 offset:16384
	ds_read_b128 v[212:215], v162 offset:18432
	ds_read_b128 v[216:219], v161 offset:20480
	ds_read_b128 v[220:223], v161 offset:22528
	ds_read_b128 v[224:227], v162 offset:20480
	ds_read_b128 v[228:231], v162 offset:22528
	global_load_lds_dwordx4 v[196:197], off
	s_add_i32 m0, s57, 0x2000
	s_add_u32 s58, s22, 0xb0000
	v_lshl_add_u64 v[196:197], s[22:23], 0, v[130:131]
	s_addc_u32 s59, s23, 0
	s_add_i32 s57, s43, s30
	global_load_lds_dwordx4 v[196:197], off
	v_lshl_add_u64 v[196:197], s[58:59], 0, v[132:133]
	s_mov_b32 m0, s57
	s_nop 0
	global_load_lds_dwordx4 v[196:197], off
	v_lshl_add_u64 v[196:197], s[58:59], 0, v[130:131]
	s_add_i32 m0, s57, 0x2000
	s_nop 0
	global_load_lds_dwordx4 v[196:197], off
	v_lshl_add_u64 v[196:197], s[26:27], 0, v[134:135]
	s_mov_b32 m0, s34
	s_nop 0
	global_load_lds_dwordx4 v[196:197], off
	v_lshl_add_u64 v[196:197], s[26:27], 0, v[136:137]
	s_mov_b32 m0, s35
	s_nop 0
	global_load_lds_dwordx4 v[196:197], off
	s_waitcnt vmcnt(8)
	s_waitcnt lgkmcnt(0)
	s_barrier
; #define PG8_STAGE(bufoff, gbase, voff) do { _Pragma("unroll") for (int _i = 0; _i < 2; ++_i) \
;         __builtin_amdgcn_global_load_lds((const unsigned*)((const char*)(gbase) + (voff)[_i]), (LAS unsigned*)(lds + (bufoff) + ldsw + _i * 8192), 16, 0, 0); } while (0)
; #define PG8_LDA(dst, b, h) do { _Pragma("unroll") for (int m = 0; m < 4; ++m) _Pragma("unroll") for (int k = 0; k < 2; ++k) dst[m][k] = *(const LAS bf16x8*)(lds + PG8_SA(b, h) + ((aoff ^ (k * 64)) + m * 2048)); } while (0)
; #define PG8_LDB(dst, b, h) do { _Pragma("unroll") for (int n = 0; n < 2; ++n) _Pragma("unroll") for (int k = 0; k < 2; ++k) dst[n][k] = *(const LAS bf16x8*)(lds + PG8_SB(b, h) + ((boff ^ (k * 64)) + n * 2048)); } while (0)
; #define PG8_MMA(ai, bj, At, Bt) do { __builtin_amdgcn_s_setprio(1); _Pragma("unroll") for (int m = 0; m < 4; ++m) _Pragma("unroll") for (int n = 0; n < 2; ++n) _Pragma("unroll") for (int k = 0; k < 2; ++k) \
;         acc[ai][bj][m][n] = __builtin_amdgcn_mfma_f32_16x16x32_bf16(Bt[n][k], At[m][k], acc[ai][bj][m][n], 0, 0, 0); __builtin_amdgcn_s_setprio(0); } while (0)
; #define PG8_WAIT_V(n) asm volatile("s_waitcnt vmcnt(" #n ")" ::: "memory")
; #define PG8_WAIT_L(n) asm volatile("s_waitcnt lgkmcnt(" #n ")" ::: "memory")
; #define PG8_BAR __builtin_amdgcn_s_barrier()
; #define PG8_SCHED __builtin_amdgcn_sched_barrier(0)
;     ...
;             PG8_WAIT_V(8); PG8_WAIT_L(0); PG8_BAR; if (do1) { PG8_MMA(1, 0, At, B0); PG8_MMA(1, 1, At, B1); } PG8_BAR; PG8_SCHED;
;             PG8_LDB(B0, 1, 0); PG8_LDB(B1, 1, 1); PG8_SCHED; PG8_LDA(At, 1, 0); PG8_STAGE(PG8_SA(0, 1), a2, vs[1]);
;             PG8_WAIT_V(8); PG8_WAIT_L(0); PG8_BAR; if (do0) { PG8_MMA(0, 0, At, B0); PG8_MMA(0, 1, At, B1); } PG8_BAR; PG8_SCHED;
	s_setprio 1
	v_mfma_f32_16x16x32_bf16 v[62:65], v[146:149], v[200:203], v[62:65]
	v_mfma_f32_16x16x32_bf16 v[58:61], v[172:175], v[200:203], v[58:61]
	v_mfma_f32_16x16x32_bf16 v[46:49], v[146:149], v[204:207], v[46:49]
	v_mfma_f32_16x16x32_bf16 v[42:45], v[172:175], v[204:207], v[42:45]
	v_mfma_f32_16x16x32_bf16 v[30:33], v[146:149], v[216:219], v[30:33]
	v_mfma_f32_16x16x32_bf16 v[26:29], v[172:175], v[216:219], v[26:29]
	v_mfma_f32_16x16x32_bf16 v[14:17], v[146:149], v[220:223], v[14:17]
	v_mfma_f32_16x16x32_bf16 v[10:13], v[172:175], v[220:223], v[10:13]
	v_mfma_f32_16x16x32_bf16 v[62:65], v[168:171], v[208:211], v[62:65]
	v_mfma_f32_16x16x32_bf16 v[58:61], v[176:179], v[208:211], v[58:61]
	v_mfma_f32_16x16x32_bf16 v[46:49], v[168:171], v[212:215], v[46:49]
	v_mfma_f32_16x16x32_bf16 v[42:45], v[176:179], v[212:215], v[42:45]
	v_mfma_f32_16x16x32_bf16 v[30:33], v[168:171], v[224:227], v[30:33]
	v_mfma_f32_16x16x32_bf16 v[26:29], v[176:179], v[224:227], v[26:29]
	v_mfma_f32_16x16x32_bf16 v[14:17], v[168:171], v[228:231], v[14:17]
	v_mfma_f32_16x16x32_bf16 v[10:13], v[176:179], v[228:231], v[10:13]
	v_mfma_f32_16x16x32_bf16 v[54:57], v[180:183], v[200:203], v[54:57]
	v_mfma_f32_16x16x32_bf16 v[50:53], v[188:191], v[200:203], v[50:53]
	v_mfma_f32_16x16x32_bf16 v[38:41], v[180:183], v[204:207], v[38:41]
	v_mfma_f32_16x16x32_bf16 v[34:37], v[188:191], v[204:207], v[34:37]
	v_mfma_f32_16x16x32_bf16 v[22:25], v[180:183], v[216:219], v[22:25]
	v_mfma_f32_16x16x32_bf16 v[18:21], v[188:191], v[216:219], v[18:21]
	v_mfma_f32_16x16x32_bf16 v[6:9], v[180:183], v[220:223], v[6:9]
	v_mfma_f32_16x16x32_bf16 v[2:5], v[188:191], v[220:223], v[2:5]
	v_mfma_f32_16x16x32_bf16 v[54:57], v[184:187], v[208:211], v[54:57]
	v_mfma_f32_16x16x32_bf16 v[50:53], v[192:195], v[208:211], v[50:53]
	v_mfma_f32_16x16x32_bf16 v[38:41], v[184:187], v[212:215], v[38:41]
	v_mfma_f32_16x16x32_bf16 v[34:37], v[192:195], v[212:215], v[34:37]
	v_mfma_f32_16x16x32_bf16 v[22:25], v[184:187], v[224:227], v[22:25]
	v_mfma_f32_16x16x32_bf16 v[18:21], v[192:195], v[224:227], v[18:21]
	v_mfma_f32_16x16x32_bf16 v[6:9], v[184:187], v[228:231], v[6:9]
	v_mfma_f32_16x16x32_bf16 v[2:5], v[192:195], v[228:231], v[2:5]
	s_setprio 0
	s_barrier
	s_add_i32 s57, 0, 0x18000
	v_add_u32_e32 v146, s57, v150
	v_add_u32_e32 v167, s57, v151
	s_add_i32 s58, 0, 0x1c000
	ds_read_b128 v[146:149], v146
	ds_read_b128 v[168:171], v167
	ds_read_b128 v[172:175], v163
	ds_read_b128 v[176:179], v164
	v_add_u32_e32 v167, s58, v150
	v_add_u32_e32 v184, s58, v151
	ds_read_b128 v[180:183], v167
	ds_read_b128 v[184:187], v184
	ds_read_b128 v[188:191], v165
	ds_read_b128 v[192:195], v166
	s_mov_b32 m0, s36
	v_lshl_add_u64 v[196:197], s[26:27], 0, v[138:139]
	ds_read_b128 v[200:203], v161 offset:32768
	ds_read_b128 v[204:207], v161 offset:34816
	ds_read_b128 v[208:211], v162 offset:32768
	ds_read_b128 v[212:215], v162 offset:34816
	ds_read_b128 v[216:219], v161 offset:36864
	ds_read_b128 v[220:223], v161 offset:38912
	ds_read_b128 v[224:227], v162 offset:36864
	ds_read_b128 v[228:231], v162 offset:38912
	global_load_lds_dwordx4 v[196:197], off
	v_lshl_add_u64 v[196:197], s[26:27], 0, v[140:141]
	s_mov_b32 m0, s37
	s_nop 0
	global_load_lds_dwordx4 v[196:197], off
	s_waitcnt vmcnt(8)
	s_waitcnt lgkmcnt(0)
	s_barrier
	s_setprio 1
	v_mfma_f32_16x16x32_bf16 v[126:129], v[146:149], v[200:203], v[126:129]
	v_mfma_f32_16x16x32_bf16 v[122:125], v[172:175], v[200:203], v[122:125]
	v_mfma_f32_16x16x32_bf16 v[114:117], v[146:149], v[204:207], v[114:117]
	v_mfma_f32_16x16x32_bf16 v[106:109], v[172:175], v[204:207], v[106:109]
	v_mfma_f32_16x16x32_bf16 v[98:101], v[146:149], v[216:219], v[98:101]
	v_mfma_f32_16x16x32_bf16 v[90:93], v[172:175], v[216:219], v[90:93]
	v_mfma_f32_16x16x32_bf16 v[82:85], v[146:149], v[220:223], v[82:85]
	v_mfma_f32_16x16x32_bf16 v[74:77], v[172:175], v[220:223], v[74:77]
	v_mfma_f32_16x16x32_bf16 v[126:129], v[168:171], v[208:211], v[126:129]
	v_mfma_f32_16x16x32_bf16 v[122:125], v[176:179], v[208:211], v[122:125]
	v_mfma_f32_16x16x32_bf16 v[114:117], v[168:171], v[212:215], v[114:117]
	v_mfma_f32_16x16x32_bf16 v[106:109], v[176:179], v[212:215], v[106:109]
	v_mfma_f32_16x16x32_bf16 v[98:101], v[168:171], v[224:227], v[98:101]
	v_mfma_f32_16x16x32_bf16 v[90:93], v[176:179], v[224:227], v[90:93]
	v_mfma_f32_16x16x32_bf16 v[82:85], v[168:171], v[228:231], v[82:85]
	v_mfma_f32_16x16x32_bf16 v[74:77], v[176:179], v[228:231], v[74:77]
	v_mfma_f32_16x16x32_bf16 v[118:121], v[180:183], v[200:203], v[118:121]
	v_mfma_f32_16x16x32_bf16 v[110:113], v[188:191], v[200:203], v[110:113]
	v_mfma_f32_16x16x32_bf16 v[102:105], v[180:183], v[204:207], v[102:105]
	v_mfma_f32_16x16x32_bf16 v[94:97], v[188:191], v[204:207], v[94:97]
	v_mfma_f32_16x16x32_bf16 v[86:89], v[180:183], v[216:219], v[86:89]
	v_mfma_f32_16x16x32_bf16 v[78:81], v[188:191], v[216:219], v[78:81]
	v_mfma_f32_16x16x32_bf16 v[70:73], v[180:183], v[220:223], v[70:73]
	v_mfma_f32_16x16x32_bf16 v[66:69], v[188:191], v[220:223], v[66:69]
	v_mfma_f32_16x16x32_bf16 v[118:121], v[184:187], v[208:211], v[118:121]
	v_mfma_f32_16x16x32_bf16 v[110:113], v[192:195], v[208:211], v[110:113]
	v_mfma_f32_16x16x32_bf16 v[102:105], v[184:187], v[212:215], v[102:105]
	v_mfma_f32_16x16x32_bf16 v[94:97], v[192:195], v[212:215], v[94:97]
	v_mfma_f32_16x16x32_bf16 v[86:89], v[184:187], v[224:227], v[86:89]
	v_mfma_f32_16x16x32_bf16 v[78:81], v[192:195], v[224:227], v[78:81]
	v_mfma_f32_16x16x32_bf16 v[70:73], v[184:187], v[228:231], v[70:73]
	v_mfma_f32_16x16x32_bf16 v[66:69], v[192:195], v[228:231], v[66:69]
	s_setprio 0
	s_barrier
; #define PG8_STAGE(bufoff, gbase, voff) do { _Pragma("unroll") for (int _i = 0; _i < 2; ++_i) \
;         __builtin_amdgcn_global_load_lds((const unsigned*)((const char*)(gbase) + (voff)[_i]), (LAS unsigned*)(lds + (bufoff) + ldsw + _i * 8192), 16, 0, 0); } while (0)
; #define PG8_LDA(dst, b, h) do { _Pragma("unroll") for (int m = 0; m < 4; ++m) _Pragma("unroll") for (int k = 0; k < 2; ++k) dst[m][k] = *(const LAS bf16x8*)(lds + PG8_SA(b, h) + ((aoff ^ (k * 64)) + m * 2048)); } while (0)
; #define PG8_MMA(ai, bj, At, Bt) do { __builtin_amdgcn_s_setprio(1); _Pragma("unroll") for (int m = 0; m < 4; ++m) _Pragma("unroll") for (int n = 0; n < 2; ++n) _Pragma("unroll") for (int k = 0; k < 2; ++k) \
;         acc[ai][bj][m][n] = __builtin_amdgcn_mfma_f32_16x16x32_bf16(Bt[n][k], At[m][k], acc[ai][bj][m][n], 0, 0, 0); __builtin_amdgcn_s_setprio(0); } while (0)
; #define PG8_WAIT_V(n) asm volatile("s_waitcnt vmcnt(" #n ")" ::: "memory")
; #define PG8_WAIT_L(n) asm volatile("s_waitcnt lgkmcnt(" #n ")" ::: "memory")
; #define PG8_BAR __builtin_amdgcn_s_barrier()
; #define PG8_SCHED __builtin_amdgcn_sched_barrier(0)
;     ...
;             PG8_LDA(At, 1, 1); PG8_STAGE(PG8_SB(1, 0), b3, voffB); PG8_STAGE(PG8_SB(1, 1), b3 + hstep, voffB); PG8_STAGE(PG8_SA(1, 0), a3, vs[0]);
;             PG8_WAIT_V(8); PG8_WAIT_L(0); PG8_BAR; if (do1) { PG8_MMA(1, 0, At, B0); PG8_MMA(1, 1, At, B1); } PG8_BAR; PG8_SCHED;
;         }
	s_add_i32 s26, s57, s30
	v_lshl_add_u64 v[196:197], s[24:25], 0, v[132:133]
	s_mov_b32 m0, s26
	ds_read_b128 v[200:203], v161 offset:49152
	ds_read_b128 v[204:207], v161 offset:51200
	ds_read_b128 v[208:211], v162 offset:49152
	ds_read_b128 v[212:215], v162 offset:51200
	ds_read_b128 v[216:219], v161 offset:53248
	ds_read_b128 v[220:223], v161 offset:55296
	ds_read_b128 v[224:227], v162 offset:53248
	ds_read_b128 v[228:231], v162 offset:55296
	global_load_lds_dwordx4 v[196:197], off
	s_add_i32 m0, s26, 0x2000
	s_add_u32 s22, s22, 0xb4000
	v_lshl_add_u64 v[196:197], s[24:25], 0, v[130:131]
	s_addc_u32 s23, s23, 0
	s_add_i32 s24, s58, s30
	global_load_lds_dwordx4 v[196:197], off
	v_lshl_add_u64 v[196:197], s[22:23], 0, v[132:133]
	s_mov_b32 m0, s24
	s_nop 0
	global_load_lds_dwordx4 v[196:197], off
	v_lshl_add_u64 v[196:197], s[22:23], 0, v[130:131]
	s_add_i32 m0, s24, 0x2000
	s_nop 0
	global_load_lds_dwordx4 v[196:197], off
	v_lshl_add_u64 v[196:197], s[20:21], 0, v[134:135]
	s_mov_b32 m0, s39
	s_nop 0
	global_load_lds_dwordx4 v[196:197], off
	v_lshl_add_u64 v[196:197], s[20:21], 0, v[136:137]
	s_mov_b32 m0, s40
	s_nop 0
	global_load_lds_dwordx4 v[196:197], off
	s_waitcnt vmcnt(8)
	s_waitcnt lgkmcnt(0)
	s_barrier
	s_setprio 1
	v_mfma_f32_16x16x32_bf16 v[62:65], v[146:149], v[200:203], v[62:65]
	v_mfma_f32_16x16x32_bf16 v[58:61], v[172:175], v[200:203], v[58:61]
	v_mfma_f32_16x16x32_bf16 v[46:49], v[146:149], v[204:207], v[46:49]
	v_mfma_f32_16x16x32_bf16 v[42:45], v[172:175], v[204:207], v[42:45]
	v_mfma_f32_16x16x32_bf16 v[30:33], v[146:149], v[216:219], v[30:33]
	v_mfma_f32_16x16x32_bf16 v[26:29], v[172:175], v[216:219], v[26:29]
	v_mfma_f32_16x16x32_bf16 v[14:17], v[146:149], v[220:223], v[14:17]
	v_mfma_f32_16x16x32_bf16 v[10:13], v[172:175], v[220:223], v[10:13]
	v_mfma_f32_16x16x32_bf16 v[62:65], v[168:171], v[208:211], v[62:65]
	v_mfma_f32_16x16x32_bf16 v[58:61], v[176:179], v[208:211], v[58:61]
	v_mfma_f32_16x16x32_bf16 v[46:49], v[168:171], v[212:215], v[46:49]
	v_mfma_f32_16x16x32_bf16 v[42:45], v[176:179], v[212:215], v[42:45]
	v_mfma_f32_16x16x32_bf16 v[30:33], v[168:171], v[224:227], v[30:33]
	v_mfma_f32_16x16x32_bf16 v[26:29], v[176:179], v[224:227], v[26:29]
	v_mfma_f32_16x16x32_bf16 v[14:17], v[168:171], v[228:231], v[14:17]
	v_mfma_f32_16x16x32_bf16 v[10:13], v[176:179], v[228:231], v[10:13]
	v_mfma_f32_16x16x32_bf16 v[54:57], v[180:183], v[200:203], v[54:57]
	v_mfma_f32_16x16x32_bf16 v[50:53], v[188:191], v[200:203], v[50:53]
	v_mfma_f32_16x16x32_bf16 v[38:41], v[180:183], v[204:207], v[38:41]
	v_mfma_f32_16x16x32_bf16 v[34:37], v[188:191], v[204:207], v[34:37]
	v_mfma_f32_16x16x32_bf16 v[22:25], v[180:183], v[216:219], v[22:25]
	v_mfma_f32_16x16x32_bf16 v[18:21], v[188:191], v[216:219], v[18:21]
	v_mfma_f32_16x16x32_bf16 v[6:9], v[180:183], v[220:223], v[6:9]
	v_mfma_f32_16x16x32_bf16 v[2:5], v[188:191], v[220:223], v[2:5]
	v_mfma_f32_16x16x32_bf16 v[54:57], v[184:187], v[208:211], v[54:57]
	v_mfma_f32_16x16x32_bf16 v[50:53], v[192:195], v[208:211], v[50:53]
	v_mfma_f32_16x16x32_bf16 v[38:41], v[184:187], v[212:215], v[38:41]
	v_mfma_f32_16x16x32_bf16 v[34:37], v[192:195], v[212:215], v[34:37]
	v_mfma_f32_16x16x32_bf16 v[22:25], v[184:187], v[224:227], v[22:25]
	v_mfma_f32_16x16x32_bf16 v[18:21], v[192:195], v[224:227], v[18:21]
	v_mfma_f32_16x16x32_bf16 v[6:9], v[184:187], v[228:231], v[6:9]
	v_mfma_f32_16x16x32_bf16 v[2:5], v[192:195], v[228:231], v[2:5]
	s_setprio 0
	s_barrier
	s_add_i32 s56, s56, 2
	s_add_u32 s18, s18, 0x8000
	s_addc_u32 s19, s19, 0
	s_add_u32 s54, s54, 0x8000
	s_addc_u32 s55, s55, 0
	s_cmp_gt_u32 s56, 41
	s_cbranch_scc0 .LBB0_2411
	s_and_b64 vcc, exec, s[4:5]
	s_cbranch_vccz .LBB0_2414
	s_barrier
